# baseline (speedup 1.0000x reference)
.LBB8_27:
	ds_read_b128 v[72:75], v231
	ds_read_b128 v[80:83], v231 offset:1024
	ds_read_b128 v[88:91], v231 offset:2048
	ds_read_b128 v[92:95], v231 offset:3072
	s_add_u32 s40, s38, 0xfffd0080
	s_addc_u32 s41, s39, -1
	s_cmp_eq_u32 s87, 8
	s_cselect_b32 s43, s9, s41
	s_cselect_b32 s42, s8, s40
	s_cselect_b32 s41, s1, s86
	s_cselect_b32 s40, s0, s85
	v_lshl_add_u64 v[190:191], s[38:39], 0, v[184:185]
	s_add_i32 m0, s51, 0xc000
	ds_read_b128 v[136:139], v232
	ds_read_b128 v[148:151], v232 offset:1024
	ds_read_b128 v[152:155], v232 offset:2048
	ds_read_b128 v[156:159], v232 offset:3072
	ds_read_b128 v[160:163], v232 offset:4096
	ds_read_b128 v[164:167], v232 offset:5120
	ds_read_b128 v[168:171], v232 offset:6144
	ds_read_b128 v[172:175], v232 offset:7168
	global_load_lds_dwordx4 v[190:191], off
	v_lshl_add_u64 v[190:191], s[38:39], 0, v[186:187]
	s_add_i32 m0, s51, 0xe000
	s_nop 0
	global_load_lds_dwordx4 v[190:191], off
	s_cmp_eq_u32 s87, 8
	s_cbranch_scc0 .Lwarm_skip_r768
	s_lshl_b32 s91, s84, 8
	s_add_i32 s91, s91, s58
	s_lshl_b32 s92, s83, 8
	s_or_b32 s92, s92, s61
	s_mul_i32 s93, s91, 0x600
	s_lshl_b32 s94, s92, 1
	s_add_u32 s93, s93, s94
	s_add_u32 s94, s10, s93
	s_addc_u32 s95, s11, 0
	v_mul_u32_u24_e32 v250, 0x600, v234
	v_and_b32_e32 v251, 3, v234
	v_and_b32_e32 v253, 4, v234
	s_add_u32 s96, s94, 0x30000
	s_addc_u32 s97, s95, 0
	v_lshlrev_b32_e32 v251, 7, v251
	s_lshl_b32 s93, s91, 3
	global_load_dword v252, v250, s[94:95]
	v_lshl_or_b32 v251, v253, 8, v251
	s_add_u32 s98, s12, s93
	s_addc_u32 s99, s13, 0
	global_load_dword v252, v250, s[96:97]
	global_load_dword v252, v251, s[98:99]
.Lwarm_skip_r768:
	s_waitcnt lgkmcnt(8)
	s_barrier
	s_waitcnt lgkmcnt(0)
	s_setprio 1
	s_waitcnt lgkmcnt(0)
	v_mfma_f32_16x16x32_f16 v[144:147], v[72:75], v[136:139], v[144:147]
	v_mfma_f32_16x16x32_f16 v[140:143], v[88:91], v[136:139], v[140:143]
	v_mfma_f32_16x16x32_f16 v[124:127], v[72:75], v[152:155], v[124:127]
	v_mfma_f32_16x16x32_f16 v[120:123], v[88:91], v[152:155], v[120:123]
	v_mfma_f32_16x16x32_f16 v[108:111], v[72:75], v[160:163], v[108:111]
	v_mfma_f32_16x16x32_f16 v[104:107], v[88:91], v[160:163], v[104:107]
	v_mfma_f32_16x16x32_f16 v[84:87], v[72:75], v[168:171], v[84:87]
	v_mfma_f32_16x16x32_f16 v[76:79], v[88:91], v[168:171], v[76:79]
	v_mfma_f32_16x16x32_f16 v[144:147], v[80:83], v[148:151], v[144:147]
	v_mfma_f32_16x16x32_f16 v[140:143], v[92:95], v[148:151], v[140:143]
	v_mfma_f32_16x16x32_f16 v[124:127], v[80:83], v[156:159], v[124:127]
	v_mfma_f32_16x16x32_f16 v[120:123], v[92:95], v[156:159], v[120:123]
	v_mfma_f32_16x16x32_f16 v[108:111], v[80:83], v[164:167], v[108:111]
	v_mfma_f32_16x16x32_f16 v[104:107], v[92:95], v[164:167], v[104:107]
	v_mfma_f32_16x16x32_f16 v[84:87], v[80:83], v[172:175], v[84:87]
	v_mfma_f32_16x16x32_f16 v[76:79], v[92:95], v[172:175], v[76:79]
	s_setprio 0
	s_barrier
	s_add_i32 s88, s70, s50
	v_lshl_add_u64 v[206:207], s[40:41], 0, v[178:179]
	s_mov_b32 m0, s88
	ds_read_b128 v[190:193], v233
	ds_read_b128 v[194:197], v233 offset:1024
	ds_read_b128 v[198:201], v233 offset:2048
	ds_read_b128 v[202:205], v233 offset:3072
	global_load_lds_dwordx4 v[206:207], off
	v_lshl_add_u64 v[208:209], s[40:41], 0, v[182:183]
	s_add_i32 m0, s88, 0x2000
	s_nop 0
	global_load_lds_dwordx4 v[208:209], off
	s_barrier
	s_waitcnt lgkmcnt(0)
	s_setprio 1
	s_waitcnt lgkmcnt(0)
	v_mfma_f32_16x16x32_f16 v[132:135], v[190:193], v[136:139], v[132:135]
	v_mfma_f32_16x16x32_f16 v[128:131], v[198:201], v[136:139], v[128:131]
	v_mfma_f32_16x16x32_f16 v[116:119], v[190:193], v[152:155], v[116:119]
	v_mfma_f32_16x16x32_f16 v[112:115], v[198:201], v[152:155], v[112:115]
	v_mfma_f32_16x16x32_f16 v[100:103], v[190:193], v[160:163], v[100:103]
	v_mfma_f32_16x16x32_f16 v[96:99], v[198:201], v[160:163], v[96:99]
	v_mfma_f32_16x16x32_f16 v[68:71], v[190:193], v[168:171], v[68:71]
	v_mfma_f32_16x16x32_f16 v[64:67], v[198:201], v[168:171], v[64:67]
	v_mfma_f32_16x16x32_f16 v[132:135], v[194:197], v[148:151], v[132:135]
	v_mfma_f32_16x16x32_f16 v[128:131], v[202:205], v[148:151], v[128:131]
	v_mfma_f32_16x16x32_f16 v[116:119], v[194:197], v[156:159], v[116:119]
	v_mfma_f32_16x16x32_f16 v[112:115], v[202:205], v[156:159], v[112:115]
	v_mfma_f32_16x16x32_f16 v[100:103], v[194:197], v[164:167], v[100:103]
	v_mfma_f32_16x16x32_f16 v[96:99], v[202:205], v[164:167], v[96:99]
	v_mfma_f32_16x16x32_f16 v[68:71], v[194:197], v[172:175], v[68:71]
	v_mfma_f32_16x16x32_f16 v[64:67], v[202:205], v[172:175], v[64:67]
	s_setprio 0
	s_mov_b32 m0, s51
	v_lshl_add_u64 v[210:211], s[42:43], 0, v[176:177]
	s_barrier
	ds_read_b128 v[136:139], v232 offset:16384
	ds_read_b128 v[148:151], v232 offset:17408
	ds_read_b128 v[152:155], v232 offset:18432
	ds_read_b128 v[156:159], v232 offset:19456
	ds_read_b128 v[160:163], v232 offset:20480
	ds_read_b128 v[164:167], v232 offset:21504
	ds_read_b128 v[168:171], v232 offset:22528
	ds_read_b128 v[172:175], v232 offset:23552
	global_load_lds_dwordx4 v[210:211], off
	v_lshl_add_u64 v[212:213], s[42:43], 0, v[180:181]
	s_mov_b32 m0, s52
	s_nop 0
	global_load_lds_dwordx4 v[212:213], off
	s_barrier
	s_waitcnt lgkmcnt(0)
	s_setprio 1
	s_waitcnt lgkmcnt(0)
	v_mfma_f32_16x16x32_f16 v[60:63], v[72:75], v[136:139], v[60:63]
	v_mfma_f32_16x16x32_f16 v[56:59], v[88:91], v[136:139], v[56:59]
	v_mfma_f32_16x16x32_f16 v[44:47], v[72:75], v[152:155], v[44:47]
	v_mfma_f32_16x16x32_f16 v[40:43], v[88:91], v[152:155], v[40:43]
	v_mfma_f32_16x16x32_f16 v[28:31], v[72:75], v[160:163], v[28:31]
	v_mfma_f32_16x16x32_f16 v[24:27], v[88:91], v[160:163], v[24:27]
	v_mfma_f32_16x16x32_f16 v[12:15], v[72:75], v[168:171], v[12:15]
	v_mfma_f32_16x16x32_f16 v[8:11], v[88:91], v[168:171], v[8:11]
	v_mfma_f32_16x16x32_f16 v[60:63], v[80:83], v[148:151], v[60:63]
	v_mfma_f32_16x16x32_f16 v[56:59], v[92:95], v[148:151], v[56:59]
	v_mfma_f32_16x16x32_f16 v[44:47], v[80:83], v[156:159], v[44:47]
	v_mfma_f32_16x16x32_f16 v[40:43], v[92:95], v[156:159], v[40:43]
	v_mfma_f32_16x16x32_f16 v[28:31], v[80:83], v[164:167], v[28:31]
	v_mfma_f32_16x16x32_f16 v[24:27], v[92:95], v[164:167], v[24:27]
	v_mfma_f32_16x16x32_f16 v[12:15], v[80:83], v[172:175], v[12:15]
	v_mfma_f32_16x16x32_f16 v[8:11], v[92:95], v[172:175], v[8:11]
	s_setprio 0
	s_barrier
	s_add_u32 s88, s40, 0xc000
	s_addc_u32 s89, s41, 0
	s_add_i32 s90, s71, s50
	v_lshl_add_u64 v[72:73], s[88:89], 0, v[178:179]
	s_mov_b32 m0, s90
	s_nop 0
	global_load_lds_dwordx4 v[72:73], off
	v_lshl_add_u64 v[72:73], s[88:89], 0, v[182:183]
	s_add_i32 m0, s90, 0x2000
	s_nop 0
	global_load_lds_dwordx4 v[72:73], off
	s_cmp_eq_u32 s87, 8
	s_cbranch_scc1 .Lwarm_w9_r768
	s_waitcnt vmcnt(6)
	s_branch .Lwarm_wj_r768
.Lwarm_w9_r768:
	s_waitcnt vmcnt(9)
.Lwarm_wj_r768:
	s_barrier
	s_setprio 1
	v_mfma_f32_16x16x32_f16 v[52:55], v[190:193], v[136:139], v[52:55]
	v_mfma_f32_16x16x32_f16 v[48:51], v[198:201], v[136:139], v[48:51]
	v_mfma_f32_16x16x32_f16 v[36:39], v[190:193], v[152:155], v[36:39]
	v_mfma_f32_16x16x32_f16 v[32:35], v[198:201], v[152:155], v[32:35]
	v_mfma_f32_16x16x32_f16 v[20:23], v[190:193], v[160:163], v[20:23]
	v_mfma_f32_16x16x32_f16 v[16:19], v[198:201], v[160:163], v[16:19]
	v_mfma_f32_16x16x32_f16 v[4:7], v[190:193], v[168:171], v[4:7]
	v_mfma_f32_16x16x32_f16 v[0:3], v[198:201], v[168:171], v[0:3]
	v_mfma_f32_16x16x32_f16 v[52:55], v[194:197], v[148:151], v[52:55]
	v_mfma_f32_16x16x32_f16 v[48:51], v[202:205], v[148:151], v[48:51]
	v_mfma_f32_16x16x32_f16 v[36:39], v[194:197], v[156:159], v[36:39]
	v_mfma_f32_16x16x32_f16 v[32:35], v[202:205], v[156:159], v[32:35]
	v_mfma_f32_16x16x32_f16 v[20:23], v[194:197], v[164:167], v[20:23]
	v_mfma_f32_16x16x32_f16 v[16:19], v[202:205], v[164:167], v[16:19]
	v_mfma_f32_16x16x32_f16 v[4:7], v[194:197], v[172:175], v[4:7]
	v_mfma_f32_16x16x32_f16 v[0:3], v[202:205], v[172:175], v[0:3]
	s_setprio 0
	s_add_i32 s88, 0, 0x18000
	v_add_u32_e32 v92, s88, v228
	s_barrier
	ds_read_b128 v[72:75], v92
	ds_read_b128 v[80:83], v92 offset:1024
	ds_read_b128 v[88:91], v92 offset:2048
	ds_read_b128 v[92:95], v92 offset:3072
	s_add_u32 s42, s42, 0x30000
	s_addc_u32 s43, s43, 0
	s_mov_b32 m0, s53
	v_lshl_add_u64 v[190:191], s[42:43], 0, v[176:177]
	ds_read_b128 v[136:139], v232 offset:32768
	ds_read_b128 v[148:151], v232 offset:33792
	ds_read_b128 v[152:155], v232 offset:34816
	ds_read_b128 v[156:159], v232 offset:35840
	ds_read_b128 v[160:163], v232 offset:36864
	ds_read_b128 v[164:167], v232 offset:37888
	ds_read_b128 v[168:171], v232 offset:38912
	ds_read_b128 v[172:175], v232 offset:39936
	global_load_lds_dwordx4 v[190:191], off
	v_lshl_add_u64 v[190:191], s[42:43], 0, v[180:181]
	s_mov_b32 m0, s54
	s_nop 0
	global_load_lds_dwordx4 v[190:191], off
	s_waitcnt lgkmcnt(8)
	s_barrier
	s_waitcnt lgkmcnt(0)
	s_setprio 1
	s_waitcnt lgkmcnt(0)
	v_mfma_f32_16x16x32_f16 v[144:147], v[72:75], v[136:139], v[144:147]
	v_mfma_f32_16x16x32_f16 v[140:143], v[88:91], v[136:139], v[140:143]
	v_mfma_f32_16x16x32_f16 v[124:127], v[72:75], v[152:155], v[124:127]
	v_mfma_f32_16x16x32_f16 v[120:123], v[88:91], v[152:155], v[120:123]
	v_mfma_f32_16x16x32_f16 v[108:111], v[72:75], v[160:163], v[108:111]
	v_mfma_f32_16x16x32_f16 v[104:107], v[88:91], v[160:163], v[104:107]
	v_mfma_f32_16x16x32_f16 v[84:87], v[72:75], v[168:171], v[84:87]
	v_mfma_f32_16x16x32_f16 v[76:79], v[88:91], v[168:171], v[76:79]
	v_mfma_f32_16x16x32_f16 v[144:147], v[80:83], v[148:151], v[144:147]
	v_mfma_f32_16x16x32_f16 v[140:143], v[92:95], v[148:151], v[140:143]
	v_mfma_f32_16x16x32_f16 v[124:127], v[80:83], v[156:159], v[124:127]
	v_mfma_f32_16x16x32_f16 v[120:123], v[92:95], v[156:159], v[120:123]
	v_mfma_f32_16x16x32_f16 v[108:111], v[80:83], v[164:167], v[108:111]
	v_mfma_f32_16x16x32_f16 v[104:107], v[92:95], v[164:167], v[104:107]
	v_mfma_f32_16x16x32_f16 v[84:87], v[80:83], v[172:175], v[84:87]
	v_mfma_f32_16x16x32_f16 v[76:79], v[92:95], v[172:175], v[76:79]
	s_setprio 0
	s_barrier
	s_add_i32 s42, 0, 0x1c000
	s_add_i32 s43, s88, s50
	v_add_u32_e32 v202, s42, v228
	v_lshl_add_u64 v[206:207], v[206:207], 0, s[36:37]
	s_mov_b32 m0, s43
	ds_read_b128 v[190:193], v202
	ds_read_b128 v[194:197], v202 offset:1024
	ds_read_b128 v[198:201], v202 offset:2048
	ds_read_b128 v[202:205], v202 offset:3072
	global_load_lds_dwordx4 v[206:207], off
	v_lshl_add_u64 v[206:207], v[208:209], 0, s[36:37]
	s_add_i32 m0, s43, 0x2000
	s_nop 0
	global_load_lds_dwordx4 v[206:207], off
	s_barrier
	s_waitcnt lgkmcnt(0)
	s_setprio 1
	s_waitcnt lgkmcnt(0)
	v_mfma_f32_16x16x32_f16 v[132:135], v[190:193], v[136:139], v[132:135]
	v_mfma_f32_16x16x32_f16 v[128:131], v[198:201], v[136:139], v[128:131]
	v_mfma_f32_16x16x32_f16 v[116:119], v[190:193], v[152:155], v[116:119]
	v_mfma_f32_16x16x32_f16 v[112:115], v[198:201], v[152:155], v[112:115]
	v_mfma_f32_16x16x32_f16 v[100:103], v[190:193], v[160:163], v[100:103]
	v_mfma_f32_16x16x32_f16 v[96:99], v[198:201], v[160:163], v[96:99]
	v_mfma_f32_16x16x32_f16 v[68:71], v[190:193], v[168:171], v[68:71]
	v_mfma_f32_16x16x32_f16 v[64:67], v[198:201], v[168:171], v[64:67]
	v_mfma_f32_16x16x32_f16 v[132:135], v[194:197], v[148:151], v[132:135]
	v_mfma_f32_16x16x32_f16 v[128:131], v[202:205], v[148:151], v[128:131]
	v_mfma_f32_16x16x32_f16 v[116:119], v[194:197], v[156:159], v[116:119]
	v_mfma_f32_16x16x32_f16 v[112:115], v[202:205], v[156:159], v[112:115]
	v_mfma_f32_16x16x32_f16 v[100:103], v[194:197], v[164:167], v[100:103]
	v_mfma_f32_16x16x32_f16 v[96:99], v[202:205], v[164:167], v[96:99]
	v_mfma_f32_16x16x32_f16 v[68:71], v[194:197], v[172:175], v[68:71]
	v_mfma_f32_16x16x32_f16 v[64:67], v[202:205], v[172:175], v[64:67]
	s_setprio 0
	s_mov_b32 m0, s59
	v_lshl_add_u64 v[206:207], v[210:211], 0, s[36:37]
	s_barrier
	ds_read_b128 v[136:139], v232 offset:49152
	ds_read_b128 v[148:151], v232 offset:50176
	ds_read_b128 v[152:155], v232 offset:51200
	ds_read_b128 v[156:159], v232 offset:52224
	ds_read_b128 v[160:163], v232 offset:53248
	ds_read_b128 v[164:167], v232 offset:54272
	ds_read_b128 v[168:171], v232 offset:55296
	ds_read_b128 v[172:175], v232 offset:56320
	global_load_lds_dwordx4 v[206:207], off
	v_lshl_add_u64 v[206:207], v[212:213], 0, s[36:37]
	s_mov_b32 m0, s60
	s_nop 0
	global_load_lds_dwordx4 v[206:207], off
	s_barrier
	s_waitcnt lgkmcnt(0)
	s_setprio 1
	s_waitcnt lgkmcnt(0)
	v_mfma_f32_16x16x32_f16 v[60:63], v[72:75], v[136:139], v[60:63]
	v_mfma_f32_16x16x32_f16 v[56:59], v[88:91], v[136:139], v[56:59]
	v_mfma_f32_16x16x32_f16 v[44:47], v[72:75], v[152:155], v[44:47]
	v_mfma_f32_16x16x32_f16 v[40:43], v[88:91], v[152:155], v[40:43]
	v_mfma_f32_16x16x32_f16 v[28:31], v[72:75], v[160:163], v[28:31]
	v_mfma_f32_16x16x32_f16 v[24:27], v[88:91], v[160:163], v[24:27]
	v_mfma_f32_16x16x32_f16 v[12:15], v[72:75], v[168:171], v[12:15]
	v_mfma_f32_16x16x32_f16 v[8:11], v[88:91], v[168:171], v[8:11]
	v_mfma_f32_16x16x32_f16 v[60:63], v[80:83], v[148:151], v[60:63]
	v_mfma_f32_16x16x32_f16 v[56:59], v[92:95], v[148:151], v[56:59]
	v_mfma_f32_16x16x32_f16 v[44:47], v[80:83], v[156:159], v[44:47]
	v_mfma_f32_16x16x32_f16 v[40:43], v[92:95], v[156:159], v[40:43]
	v_mfma_f32_16x16x32_f16 v[28:31], v[80:83], v[164:167], v[28:31]
	v_mfma_f32_16x16x32_f16 v[24:27], v[92:95], v[164:167], v[24:27]
	v_mfma_f32_16x16x32_f16 v[12:15], v[80:83], v[172:175], v[12:15]
	v_mfma_f32_16x16x32_f16 v[8:11], v[92:95], v[172:175], v[8:11]
	s_setprio 0
	s_barrier
	s_add_u32 s40, s40, 0xc080
	s_addc_u32 s41, s41, 0
	s_add_i32 s42, s42, s50
	v_lshl_add_u64 v[72:73], s[40:41], 0, v[178:179]
	s_mov_b32 m0, s42
	s_nop 0
	global_load_lds_dwordx4 v[72:73], off
	v_lshl_add_u64 v[72:73], s[40:41], 0, v[182:183]
	s_add_i32 m0, s42, 0x2000
	s_nop 0
	global_load_lds_dwordx4 v[72:73], off
	s_waitcnt vmcnt(6)
	s_barrier
	s_setprio 1
	v_mfma_f32_16x16x32_f16 v[52:55], v[190:193], v[136:139], v[52:55]
	v_mfma_f32_16x16x32_f16 v[48:51], v[198:201], v[136:139], v[48:51]
	v_mfma_f32_16x16x32_f16 v[36:39], v[190:193], v[152:155], v[36:39]
	v_mfma_f32_16x16x32_f16 v[32:35], v[198:201], v[152:155], v[32:35]
	v_mfma_f32_16x16x32_f16 v[20:23], v[190:193], v[160:163], v[20:23]
	v_mfma_f32_16x16x32_f16 v[16:19], v[198:201], v[160:163], v[16:19]
	v_mfma_f32_16x16x32_f16 v[4:7], v[190:193], v[168:171], v[4:7]
	v_mfma_f32_16x16x32_f16 v[0:3], v[198:201], v[168:171], v[0:3]
	v_mfma_f32_16x16x32_f16 v[52:55], v[194:197], v[148:151], v[52:55]
	v_mfma_f32_16x16x32_f16 v[48:51], v[202:205], v[148:151], v[48:51]
	v_mfma_f32_16x16x32_f16 v[36:39], v[194:197], v[156:159], v[36:39]
	v_mfma_f32_16x16x32_f16 v[32:35], v[202:205], v[156:159], v[32:35]
	v_mfma_f32_16x16x32_f16 v[20:23], v[194:197], v[164:167], v[20:23]
	v_mfma_f32_16x16x32_f16 v[16:19], v[202:205], v[164:167], v[16:19]
	v_mfma_f32_16x16x32_f16 v[4:7], v[194:197], v[172:175], v[4:7]
	v_mfma_f32_16x16x32_f16 v[0:3], v[202:205], v[172:175], v[0:3]
	s_setprio 0
	s_add_i32 s87, s87, 2
	s_add_u32 s38, s38, 0x100
	s_addc_u32 s39, s39, 0
	s_add_u32 s85, s85, 0x100
	s_addc_u32 s86, s86, 0
	s_cmp_gt_u32 s87, 9
	s_barrier
	s_cbranch_scc0 .LBB8_27
	s_lshl_b32 s38, s84, 8
	s_lshl_b32 s39, s83, 8
	s_add_i32 s38, s38, s58
	s_or_b32 s39, s39, s61
	v_or_b32_e32 v72, s39, v226
	v_or_b32_e32 v220, s38, v227
	v_mov_b64_e32 v[74:75], s[10:11]
	v_mad_i64_i32 v[74:75], s[40:41], v220, s72, v[74:75]
	v_ashrrev_i32_e32 v73, 31, v72
	v_lshl_add_u64 v[214:215], v[72:73], 1, v[74:75]
	v_add_co_u32_e32 v74, vcc, 0x6000, v214
	global_load_dwordx4 v[172:175], v[214:215], off nt
	global_load_dwordx4 v[168:171], v[214:215], off offset:64 nt
	v_addc_co_u32_e32 v75, vcc, 0, v215, vcc
	global_load_dwordx4 v[164:167], v[74:75], off nt
	global_load_dwordx4 v[160:163], v[74:75], off offset:64 nt
	v_add_co_u32_e32 v74, vcc, 0xc000, v214
	v_ashrrev_i32_e32 v221, 31, v220
	s_nop 0
	v_addc_co_u32_e32 v75, vcc, 0, v215, vcc
	global_load_dwordx4 v[156:159], v[74:75], off nt
	global_load_dwordx4 v[152:155], v[74:75], off offset:64 nt
	v_add_co_u32_e32 v74, vcc, s57, v214
	v_lshlrev_b64 v[72:73], 2, v[72:73]
	s_nop 0
	v_addc_co_u32_e32 v75, vcc, 0, v215, vcc
	global_load_dwordx4 v[148:151], v[74:75], off nt
	global_load_dwordx4 v[136:139], v[74:75], off offset:64 nt
	v_lshl_add_u64 v[74:75], v[220:221], 3, s[12:13]
	v_lshl_add_u64 v[238:239], s[14:15], 0, v[72:73]
	global_load_dwordx2 v[224:225], v[74:75], off
	global_load_dwordx2 v[222:223], v[74:75], off offset:128
	global_load_dwordx2 v[218:219], v[74:75], off offset:256
	global_load_dwordx2 v[216:217], v[74:75], off offset:384
	global_load_dwordx2 v[212:213], v[74:75], off offset:1024
	global_load_dwordx2 v[210:211], v[74:75], off offset:1152
	global_load_dwordx2 v[196:197], v[74:75], off offset:1280
	global_load_dwordx2 v[190:191], v[74:75], off offset:1408
	v_lshl_add_u64 v[242:243], s[16:17], 0, v[72:73]
	v_lshl_add_u64 v[246:247], s[18:19], 0, v[72:73]
	global_load_dwordx4 v[88:91], v[238:239], off offset:16
	global_load_dwordx4 v[92:95], v[238:239], off
	global_load_dwordx4 v[72:75], v[242:243], off offset:16
	global_load_dwordx4 v[80:83], v[242:243], off
	global_load_dwordx4 v[192:195], v[246:247], off offset:16
	global_load_dwordx4 v[198:201], v[246:247], off
	v_or_b32_e32 v221, s38, v229
	v_mul_lo_u32 v221, v221, s56
	v_and_b32_e32 v237, 64, v234
	v_add_u32_e32 v237, 64, v237
	s_lshl_b32 s38, s83, 2
	s_waitcnt vmcnt(0)
	v_pk_add_f32 v[202:203], v[74:75], v[194:195]
	v_pk_add_f32 v[206:207], v[82:83], v[200:201]
	v_pk_add_f32 v[208:209], v[80:81], v[198:199]
	v_pk_add_f32 v[204:205], v[72:73], v[192:193]
	global_load_dwordx4 v[72:75], v[238:239], off offset:144
	global_load_dwordx4 v[80:83], v[238:239], off offset:128
	s_nop 0
	global_load_dwordx4 v[238:241], v[242:243], off offset:144
	global_load_dwordx4 v[192:195], v[242:243], off offset:128
	s_nop 0
	global_load_dwordx4 v[242:245], v[246:247], off offset:144
	s_nop 0
	global_load_dwordx4 v[246:249], v[246:247], off offset:128
	v_pk_add_f32 v[146:147], v[146:147], v[206:207]
	v_pk_add_f32 v[144:145], v[144:145], v[208:209]
	v_pk_add_f32 v[142:143], v[142:143], v[202:203]
	v_pk_add_f32 v[140:141], v[140:141], v[204:205]
	v_pk_add_f32 v[126:127], v[126:127], v[206:207]
	v_pk_add_f32 v[124:125], v[124:125], v[208:209]
	v_pk_add_f32 v[122:123], v[122:123], v[202:203]
	v_pk_add_f32 v[120:121], v[120:121], v[204:205]
	s_waitcnt vmcnt(0)
	v_pk_add_f32 v[198:199], v[194:195], v[248:249]
	v_pk_add_f32 v[194:195], v[238:239], v[242:243]
	v_add_u32_e32 v238, s39, v221
	v_xor_b32_e32 v221, 16, v234
	v_cmp_lt_i32_e32 vcc, v221, v237
	v_xor_b32_e32 v239, 32, v234
	v_pk_add_f32 v[200:201], v[192:193], v[246:247]
	v_cndmask_b32_e32 v221, v234, v221, vcc
	v_cmp_lt_i32_e32 vcc, v239, v237
	v_pk_add_f32 v[192:193], v[240:241], v[244:245]
	v_cvt_f32_f16_e32 v240, v172
	v_cndmask_b32_e32 v237, v234, v239, vcc
	v_cvt_f32_f16_sdwa v239, v172 dst_sel:DWORD dst_unused:UNUSED_PAD src0_sel:WORD_1
	v_cvt_f32_f16_sdwa v241, v173 dst_sel:DWORD dst_unused:UNUSED_PAD src0_sel:WORD_1
	v_cvt_f32_f16_e32 v172, v173
	v_cvt_f32_f16_sdwa v242, v174 dst_sel:DWORD dst_unused:UNUSED_PAD src0_sel:WORD_1
	v_cvt_f32_f16_e32 v243, v174
	v_cvt_f32_f16_sdwa v244, v175 dst_sel:DWORD dst_unused:UNUSED_PAD src0_sel:WORD_1
	v_cvt_f32_f16_e32 v245, v175
	v_sub_f32_e32 v172, v172, v224
	v_sub_f32_e32 v173, v241, v224
	v_sub_f32_e32 v174, v240, v224
	v_sub_f32_e32 v175, v239, v224
	v_pk_mul_f32 v[174:175], v[224:225], v[174:175] op_sel:[1,0]
	v_pk_mul_f32 v[172:173], v[224:225], v[172:173] op_sel:[1,0]
	v_pk_fma_f32 v[144:145], v[174:175], v[92:93], v[144:145]
	v_pk_fma_f32 v[146:147], v[172:173], v[94:95], v[146:147]
	v_sub_f32_e32 v172, v245, v224
	v_sub_f32_e32 v173, v244, v224
	v_sub_f32_e32 v174, v243, v224
	v_sub_f32_e32 v175, v242, v224
	v_pk_mul_f32 v[174:175], v[224:225], v[174:175] op_sel:[1,0]
	v_pk_mul_f32 v[172:173], v[224:225], v[172:173] op_sel:[1,0]
	v_pk_add_f32 v[134:135], v[134:135], v[198:199]
	v_pk_fma_f32 v[172:173], v[172:173], v[90:91], v[142:143]
	v_pk_fma_f32 v[142:143], v[174:175], v[88:89], v[140:141]
	v_cvt_f16_f32_e32 v174, v144
	v_cvt_f16_f32_e32 v175, v145
	v_cvt_pk_f16_f32 v140, v144, v145
	v_cvt_f16_f32_e32 v144, v146
	v_cvt_f16_f32_e32 v145, v147
	v_cvt_pk_f16_f32 v141, v146, v147
	v_cvt_f16_f32_e32 v146, v142
	v_cvt_f16_f32_e32 v147, v143
	v_cvt_f16_f32_e32 v239, v172
	v_cvt_f16_f32_e32 v240, v173
	v_cvt_pk_f16_f32 v142, v142, v143
	v_cvt_pk_f16_f32 v143, v172, v173
	ds_write_b128 v235, v[140:143]
	v_cvt_f32_f16_e32 v140, v174
	v_cvt_f32_f16_e32 v141, v175
	v_cvt_f32_f16_e32 v142, v144
	v_cvt_f32_f16_e32 v143, v145
	v_cvt_f32_f16_e32 v145, v146
	v_cvt_f32_f16_e32 v147, v147
	v_cvt_f32_f16_e32 v172, v239
	v_cvt_f32_f16_e32 v173, v240
	v_add_f32_e32 v140, v140, v141
	v_add_f32_e32 v142, v142, v143
	v_add_f32_e32 v140, v140, v142
	v_add_f32_e32 v142, v145, v147
	v_add_f32_e32 v145, v172, v173
	v_add_f32_e32 v142, v142, v145
	v_add_f32_e32 v140, v140, v142
	v_add_f32_e32 v145, 0, v140
	v_mul_f32_e32 v140, v141, v141
	v_mul_f32_e32 v141, v143, v143
	v_fma_mix_f32 v140, v174, v174, v140 op_sel_hi:[1,1,0]
	v_fma_mix_f32 v141, v144, v144, v141 op_sel_hi:[1,1,0]
	v_mul_f32_e32 v142, v173, v173
	v_add_f32_e32 v140, v140, v141
	v_mul_f32_e32 v141, v147, v147
	v_fma_mix_f32 v141, v146, v146, v141 op_sel_hi:[1,1,0]
	v_fma_mix_f32 v142, v239, v239, v142 op_sel_hi:[1,1,0]
	v_cvt_f32_f16_sdwa v143, v168 dst_sel:DWORD dst_unused:UNUSED_PAD src0_sel:WORD_1
	v_add_f32_e32 v141, v141, v142
	v_add_f32_e32 v144, v140, v141
	v_cvt_f32_f16_e32 v142, v168
	v_cvt_f32_f16_sdwa v141, v169 dst_sel:DWORD dst_unused:UNUSED_PAD src0_sel:WORD_1
	v_cvt_f32_f16_e32 v140, v169
	v_cvt_f32_f16_sdwa v146, v170 dst_sel:DWORD dst_unused:UNUSED_PAD src0_sel:WORD_1
	v_cvt_f32_f16_e32 v147, v170
	v_cvt_f32_f16_sdwa v168, v171 dst_sel:DWORD dst_unused:UNUSED_PAD src0_sel:WORD_1
	v_cvt_f32_f16_e32 v169, v171
	v_sub_f32_e32 v140, v140, v224
	v_sub_f32_e32 v141, v141, v224
	v_sub_f32_e32 v142, v142, v224
	v_sub_f32_e32 v143, v143, v224
	v_pk_add_f32 v[132:133], v[132:133], v[200:201]
	v_pk_mul_f32 v[142:143], v[224:225], v[142:143] op_sel:[1,0]
	v_pk_mul_f32 v[140:141], v[224:225], v[140:141] op_sel:[1,0]
	v_pk_fma_f32 v[132:133], v[142:143], v[80:81], v[132:133]
	v_pk_fma_f32 v[134:135], v[140:141], v[82:83], v[134:135]
	v_sub_f32_e32 v140, v169, v224
	v_sub_f32_e32 v141, v168, v224
	v_sub_f32_e32 v142, v147, v224
	v_sub_f32_e32 v143, v146, v224
	v_pk_add_f32 v[130:131], v[130:131], v[192:193]
	v_pk_add_f32 v[128:129], v[128:129], v[194:195]
	v_pk_mul_f32 v[142:143], v[224:225], v[142:143] op_sel:[1,0]
	v_pk_mul_f32 v[140:141], v[224:225], v[140:141] op_sel:[1,0]
	v_lshlrev_b32_e32 v221, 2, v221
	v_pk_fma_f32 v[140:141], v[140:141], v[74:75], v[130:131]
	v_pk_fma_f32 v[130:131], v[142:143], v[72:73], v[128:129]
	v_cvt_f16_f32_e32 v142, v132
	v_cvt_f16_f32_e32 v143, v133
	v_cvt_pk_f16_f32 v128, v132, v133
	v_cvt_f16_f32_e32 v132, v134
	v_cvt_f16_f32_e32 v133, v135
	v_cvt_pk_f16_f32 v129, v134, v135
	v_cvt_f16_f32_e32 v134, v130
	v_cvt_f16_f32_e32 v135, v131
	v_cvt_f16_f32_e32 v146, v140
	v_cvt_f16_f32_e32 v147, v141
	v_cvt_pk_f16_f32 v130, v130, v131
	v_cvt_pk_f16_f32 v131, v140, v141
	ds_write_b128 v235, v[128:131] offset:64
	v_cvt_f32_f16_e32 v128, v142
	v_cvt_f32_f16_e32 v129, v143
	v_cvt_f32_f16_e32 v130, v132
	v_cvt_f32_f16_e32 v131, v133
	v_cvt_f32_f16_e32 v133, v134
	v_cvt_f32_f16_e32 v135, v135
	v_cvt_f32_f16_e32 v140, v146
	v_cvt_f32_f16_e32 v141, v147
	v_add_f32_e32 v128, v128, v129
	v_add_f32_e32 v130, v130, v131
	v_add_f32_e32 v128, v128, v130
	v_add_f32_e32 v130, v133, v135
	v_add_f32_e32 v133, v140, v141
	v_add_f32_e32 v130, v130, v133
	v_add_f32_e32 v128, v128, v130
	v_add_f32_e32 v140, v145, v128
	v_mul_f32_e32 v128, v129, v129
	v_mul_f32_e32 v129, v131, v131
	v_fma_mix_f32 v128, v142, v142, v128 op_sel_hi:[1,1,0]
	v_fma_mix_f32 v129, v132, v132, v129 op_sel_hi:[1,1,0]
	v_mul_f32_e32 v130, v141, v141
	v_add_f32_e32 v128, v128, v129
	v_mul_f32_e32 v129, v135, v135
	ds_bpermute_b32 v142, v221, v140
	v_fma_mix_f32 v129, v134, v134, v129 op_sel_hi:[1,1,0]
	v_fma_mix_f32 v130, v146, v146, v130 op_sel_hi:[1,1,0]
	v_lshlrev_b32_e32 v237, 2, v237
	v_add_f32_e32 v129, v129, v130
	v_add_f32_e32 v128, v128, v129
	v_add_f32_e32 v141, v144, v128
	s_waitcnt lgkmcnt(0)
	v_add_f32_e32 v140, v140, v142
	ds_bpermute_b32 v142, v221, v141
	v_cvt_f32_f16_sdwa v145, v164 dst_sel:DWORD dst_unused:UNUSED_PAD src0_sel:WORD_1
	v_cvt_f32_f16_e32 v144, v164
	v_cvt_f32_f16_sdwa v146, v166 dst_sel:DWORD dst_unused:UNUSED_PAD src0_sel:WORD_1
	v_cvt_f32_f16_e32 v147, v166
	s_waitcnt lgkmcnt(0)
	v_add_f32_e32 v141, v141, v142
	ds_bpermute_b32 v142, v237, v140
	v_cvt_f32_f16_sdwa v164, v167 dst_sel:DWORD dst_unused:UNUSED_PAD src0_sel:WORD_1
	v_sub_f32_e32 v144, v144, v222
	v_sub_f32_e32 v145, v145, v222
	v_pk_mul_f32 v[144:145], v[222:223], v[144:145] op_sel:[1,0]
	s_waitcnt lgkmcnt(0)
	v_add_f32_e32 v142, v140, v142
	ds_bpermute_b32 v140, v237, v141
	v_pk_fma_f32 v[124:125], v[144:145], v[92:93], v[124:125]
	v_sub_f32_e32 v144, v147, v222
	v_sub_f32_e32 v145, v146, v222
	v_pk_mul_f32 v[144:145], v[222:223], v[144:145] op_sel:[1,0]
	s_waitcnt lgkmcnt(0)
	v_add_f32_e32 v143, v141, v140
	v_cvt_f32_f16_sdwa v141, v165 dst_sel:DWORD dst_unused:UNUSED_PAD src0_sel:WORD_1
	v_cvt_f32_f16_e32 v140, v165
	v_cvt_f32_f16_e32 v165, v167
	ds_read_b128 v[132:135], v236
	ds_read_b128 v[128:131], v236 offset:1152
	v_sub_f32_e32 v141, v141, v222
	v_sub_f32_e32 v140, v140, v222
	v_pk_mul_f32 v[140:141], v[222:223], v[140:141] op_sel:[1,0]
	v_pk_add_f32 v[118:119], v[118:119], v[198:199]
	v_pk_fma_f32 v[126:127], v[140:141], v[94:95], v[126:127]
	v_sub_f32_e32 v140, v165, v222
	v_sub_f32_e32 v141, v164, v222
	v_pk_mul_f32 v[140:141], v[222:223], v[140:141] op_sel:[1,0]
	v_pk_add_f32 v[116:117], v[116:117], v[200:201]
	v_pk_fma_f32 v[140:141], v[140:141], v[90:91], v[122:123]
	v_pk_fma_f32 v[122:123], v[144:145], v[88:89], v[120:121]
	v_cvt_f16_f32_e32 v144, v124
	v_cvt_f16_f32_e32 v145, v125
	v_cvt_pk_f16_f32 v120, v124, v125
	v_cvt_f16_f32_e32 v124, v126
	v_cvt_f16_f32_e32 v125, v127
	v_cvt_pk_f16_f32 v121, v126, v127
	v_cvt_f16_f32_e32 v126, v122
	v_cvt_f16_f32_e32 v127, v123
	v_cvt_f16_f32_e32 v146, v140
	v_cvt_f16_f32_e32 v147, v141
	v_cvt_pk_f16_f32 v122, v122, v123
	v_cvt_pk_f16_f32 v123, v140, v141
	ds_write_b128 v235, v[120:123]
	v_cvt_f32_f16_e32 v120, v144
	v_cvt_f32_f16_e32 v121, v145
	v_cvt_f32_f16_e32 v122, v124
	v_cvt_f32_f16_e32 v123, v125
	v_cvt_f32_f16_e32 v125, v126
	v_cvt_f32_f16_e32 v127, v127
	v_cvt_f32_f16_e32 v140, v146
	v_cvt_f32_f16_e32 v141, v147
	v_add_f32_e32 v120, v120, v121
	v_add_f32_e32 v122, v122, v123
	v_add_f32_e32 v120, v120, v122
	v_add_f32_e32 v122, v125, v127
	v_add_f32_e32 v125, v140, v141
	v_add_f32_e32 v122, v122, v125
	v_add_f32_e32 v120, v120, v122
	v_add_f32_e32 v125, 0, v120
	v_mul_f32_e32 v120, v121, v121
	v_mul_f32_e32 v121, v123, v123
	v_fma_mix_f32 v120, v144, v144, v120 op_sel_hi:[1,1,0]
	v_fma_mix_f32 v121, v124, v124, v121 op_sel_hi:[1,1,0]
	v_mul_f32_e32 v122, v141, v141
	v_add_f32_e32 v120, v120, v121
	v_mul_f32_e32 v121, v127, v127
	v_fma_mix_f32 v121, v126, v126, v121 op_sel_hi:[1,1,0]
	v_fma_mix_f32 v122, v146, v146, v122 op_sel_hi:[1,1,0]
	v_cvt_f32_f16_sdwa v123, v160 dst_sel:DWORD dst_unused:UNUSED_PAD src0_sel:WORD_1
	v_add_f32_e32 v121, v121, v122
	v_add_f32_e32 v124, v120, v121
	v_cvt_f32_f16_e32 v122, v160
	v_cvt_f32_f16_sdwa v121, v161 dst_sel:DWORD dst_unused:UNUSED_PAD src0_sel:WORD_1
	v_cvt_f32_f16_e32 v120, v161
	v_cvt_f32_f16_sdwa v126, v162 dst_sel:DWORD dst_unused:UNUSED_PAD src0_sel:WORD_1
	v_cvt_f32_f16_e32 v127, v162
	v_cvt_f32_f16_sdwa v140, v163 dst_sel:DWORD dst_unused:UNUSED_PAD src0_sel:WORD_1
	v_cvt_f32_f16_e32 v141, v163
	v_sub_f32_e32 v120, v120, v222
	v_sub_f32_e32 v121, v121, v222
	v_sub_f32_e32 v122, v122, v222
	v_sub_f32_e32 v123, v123, v222
	v_pk_mul_f32 v[122:123], v[222:223], v[122:123] op_sel:[1,0]
	v_pk_mul_f32 v[120:121], v[222:223], v[120:121] op_sel:[1,0]
	v_pk_fma_f32 v[116:117], v[122:123], v[80:81], v[116:117]
	v_pk_fma_f32 v[118:119], v[120:121], v[82:83], v[118:119]
	v_sub_f32_e32 v120, v141, v222
	v_sub_f32_e32 v121, v140, v222
	v_sub_f32_e32 v122, v127, v222
	v_sub_f32_e32 v123, v126, v222
	v_pk_add_f32 v[114:115], v[114:115], v[192:193]
	v_pk_add_f32 v[112:113], v[112:113], v[194:195]
	v_pk_mul_f32 v[122:123], v[222:223], v[122:123] op_sel:[1,0]
	v_pk_mul_f32 v[120:121], v[222:223], v[120:121] op_sel:[1,0]
	s_ashr_i32 s39, s38, 31
	v_pk_fma_f32 v[120:121], v[120:121], v[74:75], v[114:115]
	v_pk_fma_f32 v[114:115], v[122:123], v[72:73], v[112:113]
	v_cvt_f16_f32_e32 v122, v116
	v_cvt_f16_f32_e32 v123, v117
	v_cvt_pk_f16_f32 v112, v116, v117
	v_cvt_f16_f32_e32 v116, v118
	v_cvt_f16_f32_e32 v117, v119
	v_cvt_pk_f16_f32 v113, v118, v119
	v_cvt_f16_f32_e32 v118, v114
	v_cvt_f16_f32_e32 v119, v115
	v_cvt_f16_f32_e32 v126, v120
	v_cvt_f16_f32_e32 v127, v121
	v_cvt_pk_f16_f32 v114, v114, v115
	v_cvt_pk_f16_f32 v115, v120, v121
	ds_write_b128 v235, v[112:115] offset:64
	v_cvt_f32_f16_e32 v112, v122
	v_cvt_f32_f16_e32 v113, v123
	v_cvt_f32_f16_e32 v114, v116
	v_cvt_f32_f16_e32 v115, v117
	v_cvt_f32_f16_e32 v117, v118
	v_cvt_f32_f16_e32 v119, v119
	v_cvt_f32_f16_e32 v120, v126
	v_cvt_f32_f16_e32 v121, v127
	v_add_f32_e32 v112, v112, v113
	v_add_f32_e32 v114, v114, v115
	v_add_f32_e32 v112, v112, v114
	v_add_f32_e32 v114, v117, v119
	v_add_f32_e32 v117, v120, v121
	v_add_f32_e32 v114, v114, v117
	v_add_f32_e32 v112, v112, v114
	v_mul_f32_e32 v113, v113, v113
	v_mul_f32_e32 v114, v115, v115
	v_fma_mix_f32 v113, v122, v122, v113 op_sel_hi:[1,1,0]
	v_fma_mix_f32 v114, v116, v116, v114 op_sel_hi:[1,1,0]
	v_mul_f32_e32 v115, v121, v121
	v_add_f32_e32 v113, v113, v114
	v_mul_f32_e32 v114, v119, v119
	v_fma_mix_f32 v114, v118, v118, v114 op_sel_hi:[1,1,0]
	v_fma_mix_f32 v115, v126, v126, v115 op_sel_hi:[1,1,0]
	v_add_f32_e32 v112, v125, v112
	v_add_f32_e32 v114, v114, v115
	v_add_f32_e32 v113, v113, v114
	ds_bpermute_b32 v114, v221, v112
	v_add_f32_e32 v113, v124, v113
	ds_read_b128 v[160:163], v236
	ds_read_b128 v[164:167], v236 offset:1152
	s_waitcnt lgkmcnt(2)
	v_add_f32_e32 v112, v112, v114
	ds_bpermute_b32 v114, v221, v113
	s_waitcnt lgkmcnt(0)
	v_add_f32_e32 v113, v113, v114
	ds_bpermute_b32 v114, v237, v112
	s_waitcnt lgkmcnt(0)
	v_add_f32_e32 v146, v112, v114
	ds_bpermute_b32 v112, v237, v113
	s_waitcnt lgkmcnt(0)
	v_add_f32_e32 v147, v113, v112
	v_mov_b64_e32 v[112:113], s[28:29]
	v_mad_i64_i32 v[112:113], s[40:41], v220, s73, v[112:113]
	v_lshl_add_u64 v[140:141], s[38:39], 3, v[112:113]
	v_add_co_u32_e32 v112, vcc, s74, v214
	v_lshl_or_b32 v144, v238, 1, v230
	s_nop 0
	v_addc_co_u32_e32 v113, vcc, 0, v215, vcc
	global_load_dwordx4 v[124:127], v[112:113], off nt
	global_load_dwordx4 v[120:123], v[112:113], off offset:64 nt
	v_add_co_u32_e32 v112, vcc, s75, v214
	v_lshl_add_u64 v[140:141], v[140:141], 0, s[34:35]
	s_nop 0
	v_addc_co_u32_e32 v113, vcc, 0, v215, vcc
	global_load_dwordx4 v[116:119], v[112:113], off nt
	s_nop 0
	global_load_dwordx4 v[112:115], v[112:113], off offset:64 nt
	s_nop 0
	buffer_store_dwordx4 v[132:135], v144, s[24:27], 0 offen nt
	s_nop 1
	v_add_u32_e32 v132, 0x3000, v144
	buffer_store_dwordx4 v[128:131], v132, s[24:27], 0 offen nt
	global_store_dwordx2 v[140:141], v[142:143], off
	s_nop 0
	v_add_u32_e32 v128, 0x6000, v144
	buffer_store_dwordx4 v[160:163], v128, s[24:27], 0 offen nt
	v_add_u32_e32 v128, 0x9000, v144
	buffer_store_dwordx4 v[164:167], v128, s[24:27], 0 offen nt
	global_store_dwordx2 v[140:141], v[146:147], off offset:1536
	v_cvt_f32_f16_sdwa v131, v156 dst_sel:DWORD dst_unused:UNUSED_PAD src0_sel:WORD_1
	v_cvt_f32_f16_e32 v130, v156
	v_cvt_f32_f16_sdwa v129, v157 dst_sel:DWORD dst_unused:UNUSED_PAD src0_sel:WORD_1
	v_cvt_f32_f16_e32 v128, v157
	v_cvt_f32_f16_sdwa v132, v158 dst_sel:DWORD dst_unused:UNUSED_PAD src0_sel:WORD_1
	v_cvt_f32_f16_e32 v133, v158
	v_cvt_f32_f16_sdwa v134, v159 dst_sel:DWORD dst_unused:UNUSED_PAD src0_sel:WORD_1
	v_cvt_f32_f16_e32 v135, v159
	v_sub_f32_e32 v128, v128, v218
	v_sub_f32_e32 v129, v129, v218
	v_sub_f32_e32 v130, v130, v218
	v_sub_f32_e32 v131, v131, v218
	v_pk_add_f32 v[110:111], v[110:111], v[206:207]
	v_pk_add_f32 v[108:109], v[108:109], v[208:209]
	v_pk_mul_f32 v[130:131], v[218:219], v[130:131] op_sel:[1,0]
	v_pk_mul_f32 v[128:129], v[218:219], v[128:129] op_sel:[1,0]
	v_pk_fma_f32 v[108:109], v[130:131], v[92:93], v[108:109]
	v_pk_fma_f32 v[110:111], v[128:129], v[94:95], v[110:111]
	v_sub_f32_e32 v128, v135, v218
	v_sub_f32_e32 v129, v134, v218
	v_sub_f32_e32 v130, v133, v218
	v_sub_f32_e32 v131, v132, v218
	v_pk_add_f32 v[106:107], v[106:107], v[202:203]
	v_pk_add_f32 v[104:105], v[104:105], v[204:205]
	v_pk_mul_f32 v[130:131], v[218:219], v[130:131] op_sel:[1,0]
	v_pk_mul_f32 v[128:129], v[218:219], v[128:129] op_sel:[1,0]
	v_pk_add_f32 v[102:103], v[102:103], v[198:199]
	v_pk_fma_f32 v[128:129], v[128:129], v[90:91], v[106:107]
	v_pk_fma_f32 v[106:107], v[130:131], v[88:89], v[104:105]
	v_cvt_f16_f32_e32 v130, v108
	v_cvt_f16_f32_e32 v131, v109
	v_cvt_pk_f16_f32 v104, v108, v109
	v_cvt_f16_f32_e32 v108, v110
	v_cvt_f16_f32_e32 v109, v111
	v_cvt_pk_f16_f32 v105, v110, v111
	v_cvt_f16_f32_e32 v110, v106
	v_cvt_f16_f32_e32 v111, v107
	v_cvt_f16_f32_e32 v132, v128
	v_cvt_f16_f32_e32 v133, v129
	v_cvt_pk_f16_f32 v106, v106, v107
	v_cvt_pk_f16_f32 v107, v128, v129
	ds_write_b128 v235, v[104:107]
	v_cvt_f32_f16_e32 v104, v130
	v_cvt_f32_f16_e32 v105, v131
	v_cvt_f32_f16_e32 v106, v108
	v_cvt_f32_f16_e32 v107, v109
	v_cvt_f32_f16_e32 v109, v110
	v_cvt_f32_f16_e32 v111, v111
	v_cvt_f32_f16_e32 v128, v132
	v_cvt_f32_f16_e32 v129, v133
	v_add_f32_e32 v104, v104, v105
	v_add_f32_e32 v106, v106, v107
	v_add_f32_e32 v104, v104, v106
	v_add_f32_e32 v106, v109, v111
	v_add_f32_e32 v109, v128, v129
	v_add_f32_e32 v106, v106, v109
	v_add_f32_e32 v104, v104, v106
	v_add_f32_e32 v109, 0, v104
	v_mul_f32_e32 v104, v105, v105
	v_mul_f32_e32 v105, v107, v107
	v_fma_mix_f32 v104, v130, v130, v104 op_sel_hi:[1,1,0]
	v_fma_mix_f32 v105, v108, v108, v105 op_sel_hi:[1,1,0]
	v_mul_f32_e32 v106, v129, v129
	v_add_f32_e32 v104, v104, v105
	v_mul_f32_e32 v105, v111, v111
	v_fma_mix_f32 v105, v110, v110, v105 op_sel_hi:[1,1,0]
	v_fma_mix_f32 v106, v132, v132, v106 op_sel_hi:[1,1,0]
	v_cvt_f32_f16_sdwa v107, v152 dst_sel:DWORD dst_unused:UNUSED_PAD src0_sel:WORD_1
	v_add_f32_e32 v105, v105, v106
	v_add_f32_e32 v108, v104, v105
	v_cvt_f32_f16_e32 v106, v152
	v_cvt_f32_f16_sdwa v105, v153 dst_sel:DWORD dst_unused:UNUSED_PAD src0_sel:WORD_1
	v_cvt_f32_f16_e32 v104, v153
	v_cvt_f32_f16_sdwa v110, v154 dst_sel:DWORD dst_unused:UNUSED_PAD src0_sel:WORD_1
	v_cvt_f32_f16_e32 v111, v154
	v_cvt_f32_f16_sdwa v128, v155 dst_sel:DWORD dst_unused:UNUSED_PAD src0_sel:WORD_1
	v_cvt_f32_f16_e32 v129, v155
	v_sub_f32_e32 v104, v104, v218
	v_sub_f32_e32 v105, v105, v218
	v_sub_f32_e32 v106, v106, v218
	v_sub_f32_e32 v107, v107, v218
	v_pk_add_f32 v[100:101], v[100:101], v[200:201]
	v_pk_mul_f32 v[106:107], v[218:219], v[106:107] op_sel:[1,0]
	v_pk_mul_f32 v[104:105], v[218:219], v[104:105] op_sel:[1,0]
	v_pk_fma_f32 v[100:101], v[106:107], v[80:81], v[100:101]
	v_pk_fma_f32 v[102:103], v[104:105], v[82:83], v[102:103]
	v_sub_f32_e32 v104, v129, v218
	v_sub_f32_e32 v105, v128, v218
	v_sub_f32_e32 v106, v111, v218
	v_sub_f32_e32 v107, v110, v218
	v_pk_add_f32 v[98:99], v[98:99], v[192:193]
	v_pk_add_f32 v[96:97], v[96:97], v[194:195]
	v_pk_mul_f32 v[106:107], v[218:219], v[106:107] op_sel:[1,0]
	v_pk_mul_f32 v[104:105], v[218:219], v[104:105] op_sel:[1,0]
	v_pk_add_f32 v[86:87], v[86:87], v[206:207]
	v_pk_fma_f32 v[104:105], v[104:105], v[74:75], v[98:99]
	v_pk_fma_f32 v[98:99], v[106:107], v[72:73], v[96:97]
	v_cvt_f16_f32_e32 v106, v100
	v_cvt_f16_f32_e32 v107, v101
	v_cvt_pk_f16_f32 v96, v100, v101
	v_cvt_f16_f32_e32 v100, v102
	v_cvt_f16_f32_e32 v101, v103
	v_cvt_pk_f16_f32 v97, v102, v103
	v_cvt_f16_f32_e32 v103, v99
	v_cvt_f16_f32_e32 v111, v105
	v_cvt_f16_f32_e32 v102, v98
	v_cvt_f16_f32_e32 v110, v104
	v_cvt_pk_f16_f32 v98, v98, v99
	v_cvt_pk_f16_f32 v99, v104, v105
	v_cvt_f32_f16_e32 v105, v107
	v_cvt_f32_f16_e32 v107, v100
	v_cvt_f32_f16_e32 v101, v101
	v_cvt_f32_f16_e32 v103, v103
	v_cvt_f32_f16_e32 v104, v106
	v_cvt_f32_f16_e32 v111, v111
	v_cvt_f32_f16_e32 v128, v102
	v_cvt_f32_f16_e32 v129, v110
	v_add_f32_e32 v107, v107, v101
	v_mul_f32_e32 v101, v101, v101
	v_fma_mix_f32 v100, v100, v100, v101 op_sel_hi:[1,1,0]
	v_mul_f32_e32 v101, v103, v103
	v_add_f32_e32 v104, v104, v105
	v_mul_f32_e32 v105, v105, v105
	v_fma_mix_f32 v101, v102, v102, v101 op_sel_hi:[1,1,0]
	v_mul_f32_e32 v102, v111, v111
	v_add_f32_e32 v104, v104, v107
	v_add_f32_e32 v107, v128, v103
	v_add_f32_e32 v128, v129, v111
	v_fma_mix_f32 v105, v106, v106, v105 op_sel_hi:[1,1,0]
	v_fma_mix_f32 v102, v110, v110, v102 op_sel_hi:[1,1,0]
	v_add_f32_e32 v107, v107, v128
	v_add_f32_e32 v100, v105, v100
	v_add_f32_e32 v101, v101, v102
	v_add_f32_e32 v104, v104, v107
	v_add_f32_e32 v100, v100, v101
	v_add_f32_e32 v104, v109, v104
	v_add_f32_e32 v105, v108, v100
	ds_bpermute_b32 v106, v221, v104
	ds_bpermute_b32 v107, v221, v105
	v_cvt_f32_f16_sdwa v108, v150 dst_sel:DWORD dst_unused:UNUSED_PAD src0_sel:WORD_1
	v_cvt_f32_f16_e32 v109, v150
	v_cvt_f32_f16_sdwa v110, v151 dst_sel:DWORD dst_unused:UNUSED_PAD src0_sel:WORD_1
	s_waitcnt lgkmcnt(1)
	v_add_f32_e32 v128, v104, v106
	s_waitcnt lgkmcnt(0)
	v_add_f32_e32 v129, v105, v107
	v_cvt_f32_f16_sdwa v107, v148 dst_sel:DWORD dst_unused:UNUSED_PAD src0_sel:WORD_1
	v_cvt_f32_f16_e32 v106, v148
	v_cvt_f32_f16_sdwa v105, v149 dst_sel:DWORD dst_unused:UNUSED_PAD src0_sel:WORD_1
	v_cvt_f32_f16_e32 v104, v149
	v_cvt_f32_f16_e32 v111, v151
	v_sub_f32_e32 v106, v106, v216
	v_sub_f32_e32 v105, v105, v216
	v_sub_f32_e32 v104, v104, v216
	v_sub_f32_e32 v107, v107, v216
	v_pk_add_f32 v[84:85], v[84:85], v[208:209]
	v_pk_mul_f32 v[106:107], v[216:217], v[106:107] op_sel:[1,0]
	v_pk_mul_f32 v[104:105], v[216:217], v[104:105] op_sel:[1,0]
	v_pk_fma_f32 v[84:85], v[106:107], v[92:93], v[84:85]
	v_pk_fma_f32 v[86:87], v[104:105], v[94:95], v[86:87]
	v_sub_f32_e32 v104, v111, v216
	v_sub_f32_e32 v105, v110, v216
	v_sub_f32_e32 v106, v109, v216
	v_sub_f32_e32 v107, v108, v216
	v_pk_add_f32 v[78:79], v[78:79], v[202:203]
	v_pk_add_f32 v[76:77], v[76:77], v[204:205]
	v_pk_mul_f32 v[106:107], v[216:217], v[106:107] op_sel:[1,0]
	v_pk_mul_f32 v[104:105], v[216:217], v[104:105] op_sel:[1,0]
	ds_write_b128 v235, v[96:99] offset:64
	v_pk_fma_f32 v[104:105], v[104:105], v[90:91], v[78:79]
	v_pk_fma_f32 v[78:79], v[106:107], v[88:89], v[76:77]
	v_cvt_f16_f32_e32 v106, v84
	v_cvt_f16_f32_e32 v107, v85
	v_cvt_pk_f16_f32 v76, v84, v85
	v_cvt_f16_f32_e32 v84, v86
	v_cvt_f16_f32_e32 v85, v87
	v_cvt_pk_f16_f32 v77, v86, v87
	v_cvt_f16_f32_e32 v86, v78
	v_cvt_f16_f32_e32 v87, v79
	v_cvt_f16_f32_e32 v108, v104
	v_cvt_f16_f32_e32 v109, v105
	v_cvt_pk_f16_f32 v78, v78, v79
	v_cvt_pk_f16_f32 v79, v104, v105
	ds_read_b128 v[96:99], v236
	ds_read_b128 v[100:103], v236 offset:1152
	ds_write_b128 v235, v[76:79]
	v_cvt_f32_f16_e32 v76, v106
	v_cvt_f32_f16_e32 v77, v107
	v_cvt_f32_f16_e32 v78, v84
	v_cvt_f32_f16_e32 v79, v85
	v_cvt_f32_f16_e32 v85, v86
	v_cvt_f32_f16_e32 v87, v87
	v_cvt_f32_f16_e32 v104, v108
	v_cvt_f32_f16_e32 v105, v109
	v_add_f32_e32 v76, v76, v77
	v_add_f32_e32 v78, v78, v79
	v_add_f32_e32 v76, v76, v78
	v_add_f32_e32 v78, v85, v87
	v_add_f32_e32 v85, v104, v105
	v_add_f32_e32 v78, v78, v85
	v_add_f32_e32 v76, v76, v78
	v_add_f32_e32 v85, 0, v76
	v_mul_f32_e32 v76, v77, v77
	v_mul_f32_e32 v77, v79, v79
	v_fma_mix_f32 v76, v106, v106, v76 op_sel_hi:[1,1,0]
	v_fma_mix_f32 v77, v84, v84, v77 op_sel_hi:[1,1,0]
	v_mul_f32_e32 v78, v105, v105
	v_add_f32_e32 v76, v76, v77
	v_mul_f32_e32 v77, v87, v87
	v_fma_mix_f32 v77, v86, v86, v77 op_sel_hi:[1,1,0]
	v_fma_mix_f32 v78, v108, v108, v78 op_sel_hi:[1,1,0]
	v_cvt_f32_f16_sdwa v79, v136 dst_sel:DWORD dst_unused:UNUSED_PAD src0_sel:WORD_1
	v_add_f32_e32 v77, v77, v78
	v_add_f32_e32 v84, v76, v77
	v_cvt_f32_f16_e32 v78, v136
	v_cvt_f32_f16_sdwa v77, v137 dst_sel:DWORD dst_unused:UNUSED_PAD src0_sel:WORD_1
	v_cvt_f32_f16_e32 v76, v137
	v_cvt_f32_f16_sdwa v86, v138 dst_sel:DWORD dst_unused:UNUSED_PAD src0_sel:WORD_1
	v_cvt_f32_f16_e32 v87, v138
	v_cvt_f32_f16_sdwa v104, v139 dst_sel:DWORD dst_unused:UNUSED_PAD src0_sel:WORD_1
	v_cvt_f32_f16_e32 v105, v139
	v_sub_f32_e32 v76, v76, v216
	v_sub_f32_e32 v77, v77, v216
	v_sub_f32_e32 v78, v78, v216
	v_sub_f32_e32 v79, v79, v216
	v_pk_add_f32 v[70:71], v[70:71], v[198:199]
	v_pk_add_f32 v[68:69], v[68:69], v[200:201]
	v_pk_mul_f32 v[78:79], v[216:217], v[78:79] op_sel:[1,0]
	v_pk_mul_f32 v[76:77], v[216:217], v[76:77] op_sel:[1,0]
	v_pk_fma_f32 v[68:69], v[78:79], v[80:81], v[68:69]
	v_pk_fma_f32 v[70:71], v[76:77], v[82:83], v[70:71]
	v_sub_f32_e32 v76, v105, v216
	v_sub_f32_e32 v77, v104, v216
	v_sub_f32_e32 v78, v87, v216
	v_sub_f32_e32 v79, v86, v216
	v_pk_add_f32 v[66:67], v[66:67], v[192:193]
	v_pk_add_f32 v[64:65], v[64:65], v[194:195]
	v_pk_mul_f32 v[78:79], v[216:217], v[78:79] op_sel:[1,0]
	v_pk_mul_f32 v[76:77], v[216:217], v[76:77] op_sel:[1,0]
	ds_bpermute_b32 v130, v237, v128
	v_pk_fma_f32 v[76:77], v[76:77], v[74:75], v[66:67]
	v_pk_fma_f32 v[66:67], v[78:79], v[72:73], v[64:65]
	v_cvt_f16_f32_e32 v78, v68
	v_cvt_f16_f32_e32 v79, v69
	v_cvt_pk_f16_f32 v64, v68, v69
	v_cvt_f16_f32_e32 v68, v70
	v_cvt_f16_f32_e32 v69, v71
	v_cvt_pk_f16_f32 v65, v70, v71
	v_cvt_f16_f32_e32 v71, v67
	v_cvt_f16_f32_e32 v87, v77
	v_cvt_f16_f32_e32 v70, v66
	v_cvt_f16_f32_e32 v86, v76
	v_cvt_f32_f16_e32 v105, v68
	v_cvt_f32_f16_e32 v69, v69
	v_cvt_f32_f16_e32 v71, v71
	v_cvt_f32_f16_e32 v104, v78
	v_cvt_f32_f16_e32 v79, v79
	v_cvt_f32_f16_e32 v87, v87
	v_cvt_f32_f16_e32 v106, v70
	v_cvt_f32_f16_e32 v107, v86
	v_add_f32_e32 v105, v105, v69
	v_mul_f32_e32 v69, v69, v69
	v_fma_mix_f32 v68, v68, v68, v69 op_sel_hi:[1,1,0]
	v_mul_f32_e32 v69, v71, v71
	v_add_f32_e32 v104, v104, v79
	v_mul_f32_e32 v79, v79, v79
	v_fma_mix_f32 v69, v70, v70, v69 op_sel_hi:[1,1,0]
	v_mul_f32_e32 v70, v87, v87
	v_add_f32_e32 v104, v104, v105
	v_add_f32_e32 v105, v106, v71
	v_add_f32_e32 v106, v107, v87
	v_fma_mix_f32 v78, v78, v78, v79 op_sel_hi:[1,1,0]
	v_fma_mix_f32 v70, v86, v86, v70 op_sel_hi:[1,1,0]
	v_add_f32_e32 v105, v105, v106
	v_add_f32_e32 v68, v78, v68
	v_add_f32_e32 v69, v69, v70
	v_add_f32_e32 v104, v104, v105
	v_add_f32_e32 v68, v68, v69
	v_add_f32_e32 v85, v85, v104
	v_add_f32_e32 v68, v84, v68
	ds_bpermute_b32 v69, v221, v85
	ds_bpermute_b32 v70, v221, v68
	v_cvt_pk_f16_f32 v66, v66, v67
	v_cvt_pk_f16_f32 v67, v76, v77
	ds_write_b128 v235, v[64:67] offset:64
	s_waitcnt lgkmcnt(2)
	v_add_f32_e32 v64, v85, v69
	s_waitcnt lgkmcnt(1)
	v_add_f32_e32 v65, v68, v70
	ds_bpermute_b32 v131, v237, v129
	ds_bpermute_b32 v66, v237, v64
	ds_bpermute_b32 v67, v237, v65
	ds_read_b128 v[104:107], v236
	ds_read_b128 v[108:111], v236 offset:1152
	v_add_f32_e32 v128, v128, v130
	s_waitcnt lgkmcnt(4)
	v_add_f32_e32 v129, v129, v131
	s_waitcnt lgkmcnt(3)
	v_add_f32_e32 v130, v64, v66
	s_waitcnt lgkmcnt(2)
	v_add_f32_e32 v131, v65, v67
	v_add_co_u32_e32 v64, vcc, s77, v214
	s_nop 1
	v_addc_co_u32_e32 v65, vcc, 0, v215, vcc
	global_load_dwordx4 v[84:87], v[64:65], off nt
	global_load_dwordx4 v[76:79], v[64:65], off offset:64 nt
	v_add_co_u32_e32 v64, vcc, s78, v214
	s_nop 1
	v_addc_co_u32_e32 v65, vcc, 0, v215, vcc
	global_load_dwordx4 v[68:71], v[64:65], off nt
	s_nop 0
	global_load_dwordx4 v[64:67], v[64:65], off offset:64 nt
	v_add_u32_e32 v132, 0xc000, v144
	buffer_store_dwordx4 v[96:99], v132, s[24:27], 0 offen nt
	s_nop 1
	v_add_u32_e32 v96, 0xf000, v144
	buffer_store_dwordx4 v[100:103], v96, s[24:27], 0 offen nt
	v_add_u32_e32 v96, 0x12000, v144
	global_store_dwordx2 v[140:141], v[128:129], off offset:3072
	s_waitcnt lgkmcnt(1)
	buffer_store_dwordx4 v[104:107], v96, s[24:27], 0 offen nt
	v_add_u32_e32 v96, 0x15000, v144
	s_waitcnt lgkmcnt(0)
	buffer_store_dwordx4 v[108:111], v96, s[24:27], 0 offen nt
	v_add_co_u32_e32 v96, vcc, s79, v140
	s_nop 1
	v_addc_co_u32_e32 v97, vcc, 0, v141, vcc
	global_store_dwordx2 v[96:97], v[130:131], off offset:512
	s_waitcnt vmcnt(19)
	v_cvt_f32_f16_sdwa v99, v124 dst_sel:DWORD dst_unused:UNUSED_PAD src0_sel:WORD_1
	v_cvt_f32_f16_e32 v98, v124
	v_cvt_f32_f16_sdwa v97, v125 dst_sel:DWORD dst_unused:UNUSED_PAD src0_sel:WORD_1
	v_cvt_f32_f16_e32 v96, v125
	v_cvt_f32_f16_sdwa v100, v126 dst_sel:DWORD dst_unused:UNUSED_PAD src0_sel:WORD_1
	v_cvt_f32_f16_e32 v101, v126
	v_cvt_f32_f16_sdwa v102, v127 dst_sel:DWORD dst_unused:UNUSED_PAD src0_sel:WORD_1
	v_cvt_f32_f16_e32 v103, v127
	v_sub_f32_e32 v96, v96, v212
	v_sub_f32_e32 v97, v97, v212
	v_sub_f32_e32 v98, v98, v212
	v_sub_f32_e32 v99, v99, v212
	v_pk_add_f32 v[62:63], v[62:63], v[206:207]
	v_pk_add_f32 v[60:61], v[60:61], v[208:209]
	v_pk_mul_f32 v[98:99], v[212:213], v[98:99] op_sel:[1,0]
	v_pk_mul_f32 v[96:97], v[212:213], v[96:97] op_sel:[1,0]
	v_pk_fma_f32 v[60:61], v[92:93], v[98:99], v[60:61]
	v_pk_fma_f32 v[62:63], v[94:95], v[96:97], v[62:63]
	v_sub_f32_e32 v96, v103, v212
	v_sub_f32_e32 v97, v102, v212
	v_sub_f32_e32 v98, v101, v212
	v_sub_f32_e32 v99, v100, v212
	v_pk_add_f32 v[58:59], v[58:59], v[202:203]
	v_pk_add_f32 v[56:57], v[56:57], v[204:205]
	v_pk_mul_f32 v[98:99], v[212:213], v[98:99] op_sel:[1,0]
	v_pk_mul_f32 v[96:97], v[212:213], v[96:97] op_sel:[1,0]
	v_pk_add_f32 v[54:55], v[54:55], v[198:199]
	v_pk_fma_f32 v[96:97], v[90:91], v[96:97], v[58:59]
	v_pk_fma_f32 v[58:59], v[88:89], v[98:99], v[56:57]
	v_cvt_f16_f32_e32 v98, v60
	v_cvt_f16_f32_e32 v99, v61
	v_cvt_pk_f16_f32 v56, v60, v61
	v_cvt_f16_f32_e32 v60, v62
	v_cvt_f16_f32_e32 v61, v63
	v_cvt_pk_f16_f32 v57, v62, v63
	v_cvt_f16_f32_e32 v62, v58
	v_cvt_f16_f32_e32 v63, v59
	v_cvt_f16_f32_e32 v100, v96
	v_cvt_f16_f32_e32 v101, v97
	v_cvt_pk_f16_f32 v58, v58, v59
	v_cvt_pk_f16_f32 v59, v96, v97
	ds_write_b128 v235, v[56:59]
	v_cvt_f32_f16_e32 v56, v98
	v_cvt_f32_f16_e32 v57, v99
	v_cvt_f32_f16_e32 v58, v60
	v_cvt_f32_f16_e32 v59, v61
	v_cvt_f32_f16_e32 v61, v62
	v_cvt_f32_f16_e32 v63, v63
	v_cvt_f32_f16_e32 v96, v100
	v_cvt_f32_f16_e32 v97, v101
	v_add_f32_e32 v56, v56, v57
	v_add_f32_e32 v58, v58, v59
	v_add_f32_e32 v56, v56, v58
	v_add_f32_e32 v58, v61, v63
	v_add_f32_e32 v61, v96, v97
	v_add_f32_e32 v58, v58, v61
	v_add_f32_e32 v56, v56, v58
	v_add_f32_e32 v61, 0, v56
	v_mul_f32_e32 v56, v57, v57
	v_mul_f32_e32 v57, v59, v59
	v_fma_mix_f32 v56, v98, v98, v56 op_sel_hi:[1,1,0]
	v_fma_mix_f32 v57, v60, v60, v57 op_sel_hi:[1,1,0]
	v_mul_f32_e32 v58, v97, v97
	v_add_f32_e32 v56, v56, v57
	v_mul_f32_e32 v57, v63, v63
	v_fma_mix_f32 v57, v62, v62, v57 op_sel_hi:[1,1,0]
	v_fma_mix_f32 v58, v100, v100, v58 op_sel_hi:[1,1,0]
	s_waitcnt vmcnt(18)
	v_cvt_f32_f16_sdwa v59, v120 dst_sel:DWORD dst_unused:UNUSED_PAD src0_sel:WORD_1
	v_add_f32_e32 v57, v57, v58
	v_add_f32_e32 v60, v56, v57
	v_cvt_f32_f16_e32 v58, v120
	v_cvt_f32_f16_sdwa v57, v121 dst_sel:DWORD dst_unused:UNUSED_PAD src0_sel:WORD_1
	v_cvt_f32_f16_e32 v56, v121
	v_cvt_f32_f16_sdwa v62, v122 dst_sel:DWORD dst_unused:UNUSED_PAD src0_sel:WORD_1
	v_cvt_f32_f16_e32 v63, v122
	v_cvt_f32_f16_sdwa v96, v123 dst_sel:DWORD dst_unused:UNUSED_PAD src0_sel:WORD_1
	v_cvt_f32_f16_e32 v97, v123
	v_sub_f32_e32 v56, v56, v212
	v_sub_f32_e32 v57, v57, v212
	v_sub_f32_e32 v58, v58, v212
	v_sub_f32_e32 v59, v59, v212
	v_pk_add_f32 v[52:53], v[52:53], v[200:201]
	v_pk_mul_f32 v[58:59], v[212:213], v[58:59] op_sel:[1,0]
	v_pk_mul_f32 v[56:57], v[212:213], v[56:57] op_sel:[1,0]
	v_pk_fma_f32 v[52:53], v[80:81], v[58:59], v[52:53]
	v_pk_fma_f32 v[54:55], v[82:83], v[56:57], v[54:55]
	v_sub_f32_e32 v56, v97, v212
	v_sub_f32_e32 v57, v96, v212
	v_sub_f32_e32 v58, v63, v212
	v_sub_f32_e32 v59, v62, v212
	v_pk_add_f32 v[50:51], v[50:51], v[192:193]
	v_pk_add_f32 v[48:49], v[48:49], v[194:195]
	v_pk_mul_f32 v[58:59], v[212:213], v[58:59] op_sel:[1,0]
	v_pk_mul_f32 v[56:57], v[212:213], v[56:57] op_sel:[1,0]
	s_waitcnt vmcnt(17)
	v_cvt_f32_f16_sdwa v98, v119 dst_sel:DWORD dst_unused:UNUSED_PAD src0_sel:WORD_1
	v_pk_fma_f32 v[56:57], v[74:75], v[56:57], v[50:51]
	v_pk_fma_f32 v[50:51], v[72:73], v[58:59], v[48:49]
	v_cvt_f16_f32_e32 v58, v52
	v_cvt_f16_f32_e32 v59, v53
	v_cvt_pk_f16_f32 v48, v52, v53
	v_cvt_f16_f32_e32 v52, v54
	v_cvt_f16_f32_e32 v53, v55
	v_cvt_pk_f16_f32 v49, v54, v55
	v_cvt_f16_f32_e32 v55, v51
	v_cvt_f16_f32_e32 v63, v57
	v_cvt_f16_f32_e32 v54, v50
	v_cvt_f16_f32_e32 v62, v56
	v_cvt_pk_f16_f32 v50, v50, v51
	v_cvt_pk_f16_f32 v51, v56, v57
	v_cvt_f32_f16_e32 v57, v59
	v_cvt_f32_f16_e32 v59, v52
	v_cvt_f32_f16_e32 v53, v53
	v_cvt_f32_f16_e32 v55, v55
	v_cvt_f32_f16_e32 v56, v58
	v_cvt_f32_f16_e32 v63, v63
	v_cvt_f32_f16_e32 v96, v54
	v_cvt_f32_f16_e32 v97, v62
	v_add_f32_e32 v59, v59, v53
	v_mul_f32_e32 v53, v53, v53
	v_fma_mix_f32 v52, v52, v52, v53 op_sel_hi:[1,1,0]
	v_mul_f32_e32 v53, v55, v55
	v_add_f32_e32 v56, v56, v57
	v_mul_f32_e32 v57, v57, v57
	v_fma_mix_f32 v53, v54, v54, v53 op_sel_hi:[1,1,0]
	v_mul_f32_e32 v54, v63, v63
	v_add_f32_e32 v56, v56, v59
	v_add_f32_e32 v59, v96, v55
	v_add_f32_e32 v96, v97, v63
	v_fma_mix_f32 v57, v58, v58, v57 op_sel_hi:[1,1,0]
	v_fma_mix_f32 v54, v62, v62, v54 op_sel_hi:[1,1,0]
	v_add_f32_e32 v59, v59, v96
	v_add_f32_e32 v52, v57, v52
	v_add_f32_e32 v53, v53, v54
	v_add_f32_e32 v56, v56, v59
	v_add_f32_e32 v52, v52, v53
	v_add_f32_e32 v56, v61, v56
	v_add_f32_e32 v57, v60, v52
	ds_bpermute_b32 v58, v221, v56
	ds_bpermute_b32 v59, v221, v57
	v_cvt_f32_f16_sdwa v96, v118 dst_sel:DWORD dst_unused:UNUSED_PAD src0_sel:WORD_1
	v_cvt_f32_f16_e32 v97, v118
	v_cvt_f32_f16_e32 v99, v119
	s_waitcnt lgkmcnt(1)
	v_add_f32_e32 v60, v56, v58
	s_waitcnt lgkmcnt(0)
	v_add_f32_e32 v61, v57, v59
	v_cvt_f32_f16_sdwa v59, v116 dst_sel:DWORD dst_unused:UNUSED_PAD src0_sel:WORD_1
	v_cvt_f32_f16_e32 v58, v116
	v_cvt_f32_f16_sdwa v57, v117 dst_sel:DWORD dst_unused:UNUSED_PAD src0_sel:WORD_1
	v_cvt_f32_f16_e32 v56, v117
	v_sub_f32_e32 v59, v59, v210
	v_sub_f32_e32 v58, v58, v210
	v_sub_f32_e32 v57, v57, v210
	v_sub_f32_e32 v56, v56, v210
	v_pk_add_f32 v[46:47], v[46:47], v[206:207]
	v_pk_add_f32 v[44:45], v[44:45], v[208:209]
	v_pk_mul_f32 v[58:59], v[210:211], v[58:59] op_sel:[1,0]
	v_pk_mul_f32 v[56:57], v[210:211], v[56:57] op_sel:[1,0]
	v_pk_fma_f32 v[44:45], v[92:93], v[58:59], v[44:45]
	v_pk_fma_f32 v[46:47], v[94:95], v[56:57], v[46:47]
	v_sub_f32_e32 v56, v99, v210
	v_sub_f32_e32 v57, v98, v210
	v_sub_f32_e32 v58, v97, v210
	v_sub_f32_e32 v59, v96, v210
	v_pk_add_f32 v[42:43], v[42:43], v[202:203]
	v_pk_add_f32 v[40:41], v[40:41], v[204:205]
	v_pk_mul_f32 v[58:59], v[210:211], v[58:59] op_sel:[1,0]
	v_pk_mul_f32 v[56:57], v[210:211], v[56:57] op_sel:[1,0]
	ds_write_b128 v235, v[48:51] offset:64
	v_pk_fma_f32 v[56:57], v[90:91], v[56:57], v[42:43]
	v_pk_fma_f32 v[42:43], v[88:89], v[58:59], v[40:41]
	v_cvt_f16_f32_e32 v58, v44
	v_cvt_f16_f32_e32 v59, v45
	v_cvt_pk_f16_f32 v40, v44, v45
	v_cvt_f16_f32_e32 v44, v46
	v_cvt_f16_f32_e32 v45, v47
	v_cvt_pk_f16_f32 v41, v46, v47
	v_cvt_f16_f32_e32 v46, v42
	v_cvt_f16_f32_e32 v47, v43
	v_cvt_f16_f32_e32 v96, v56
	v_cvt_f16_f32_e32 v97, v57
	v_cvt_pk_f16_f32 v42, v42, v43
	v_cvt_pk_f16_f32 v43, v56, v57
	ds_read_b128 v[48:51], v236
	ds_read_b128 v[52:55], v236 offset:1152
	ds_write_b128 v235, v[40:43]
	v_cvt_f32_f16_e32 v40, v58
	v_cvt_f32_f16_e32 v41, v59
	v_cvt_f32_f16_e32 v42, v44
	v_cvt_f32_f16_e32 v43, v45
	v_cvt_f32_f16_e32 v45, v46
	v_cvt_f32_f16_e32 v47, v47
	v_cvt_f32_f16_e32 v56, v96
	v_cvt_f32_f16_e32 v57, v97
	v_add_f32_e32 v40, v40, v41
	v_add_f32_e32 v42, v42, v43
	v_add_f32_e32 v40, v40, v42
	v_add_f32_e32 v42, v45, v47
	v_add_f32_e32 v45, v56, v57
	v_add_f32_e32 v42, v42, v45
	v_add_f32_e32 v40, v40, v42
	v_add_f32_e32 v45, 0, v40
	v_mul_f32_e32 v40, v41, v41
	v_mul_f32_e32 v41, v43, v43
	v_fma_mix_f32 v40, v58, v58, v40 op_sel_hi:[1,1,0]
	v_fma_mix_f32 v41, v44, v44, v41 op_sel_hi:[1,1,0]
	v_mul_f32_e32 v42, v57, v57
	v_add_f32_e32 v40, v40, v41
	v_mul_f32_e32 v41, v47, v47
	v_fma_mix_f32 v41, v46, v46, v41 op_sel_hi:[1,1,0]
	v_fma_mix_f32 v42, v96, v96, v42 op_sel_hi:[1,1,0]
	s_waitcnt vmcnt(16)
	v_cvt_f32_f16_sdwa v43, v112 dst_sel:DWORD dst_unused:UNUSED_PAD src0_sel:WORD_1
	v_add_f32_e32 v41, v41, v42
	v_add_f32_e32 v44, v40, v41
	v_cvt_f32_f16_e32 v42, v112
	v_cvt_f32_f16_sdwa v41, v113 dst_sel:DWORD dst_unused:UNUSED_PAD src0_sel:WORD_1
	v_cvt_f32_f16_e32 v40, v113
	v_cvt_f32_f16_sdwa v46, v114 dst_sel:DWORD dst_unused:UNUSED_PAD src0_sel:WORD_1
	v_cvt_f32_f16_e32 v47, v114
	v_cvt_f32_f16_sdwa v56, v115 dst_sel:DWORD dst_unused:UNUSED_PAD src0_sel:WORD_1
	v_cvt_f32_f16_e32 v57, v115
	v_sub_f32_e32 v40, v40, v210
	v_sub_f32_e32 v41, v41, v210
	v_sub_f32_e32 v42, v42, v210
	v_sub_f32_e32 v43, v43, v210
	v_pk_add_f32 v[38:39], v[38:39], v[198:199]
	v_pk_add_f32 v[36:37], v[36:37], v[200:201]
	v_pk_mul_f32 v[42:43], v[210:211], v[42:43] op_sel:[1,0]
	v_pk_mul_f32 v[40:41], v[210:211], v[40:41] op_sel:[1,0]
	v_pk_fma_f32 v[36:37], v[80:81], v[42:43], v[36:37]
	v_pk_fma_f32 v[38:39], v[82:83], v[40:41], v[38:39]
	v_sub_f32_e32 v40, v57, v210
	v_sub_f32_e32 v41, v56, v210
	v_sub_f32_e32 v42, v47, v210
	v_sub_f32_e32 v43, v46, v210
	v_pk_add_f32 v[34:35], v[34:35], v[192:193]
	v_pk_add_f32 v[32:33], v[32:33], v[194:195]
	v_pk_mul_f32 v[42:43], v[210:211], v[42:43] op_sel:[1,0]
	v_pk_mul_f32 v[40:41], v[210:211], v[40:41] op_sel:[1,0]
	ds_bpermute_b32 v62, v237, v60
	v_pk_fma_f32 v[40:41], v[74:75], v[40:41], v[34:35]
	v_pk_fma_f32 v[34:35], v[72:73], v[42:43], v[32:33]
	v_cvt_f16_f32_e32 v42, v36
	v_cvt_f16_f32_e32 v43, v37
	v_cvt_pk_f16_f32 v32, v36, v37
	v_cvt_f16_f32_e32 v36, v38
	v_cvt_f16_f32_e32 v37, v39
	v_cvt_pk_f16_f32 v33, v38, v39
	v_cvt_f16_f32_e32 v39, v35
	v_cvt_f16_f32_e32 v47, v41
	v_cvt_f16_f32_e32 v38, v34
	v_cvt_f16_f32_e32 v46, v40
	v_cvt_f32_f16_e32 v57, v36
	v_cvt_f32_f16_e32 v37, v37
	v_cvt_f32_f16_e32 v39, v39
	v_cvt_f32_f16_e32 v56, v42
	v_cvt_f32_f16_e32 v43, v43
	v_cvt_f32_f16_e32 v47, v47
	v_cvt_f32_f16_e32 v58, v38
	v_cvt_f32_f16_e32 v59, v46
	v_add_f32_e32 v57, v57, v37
	v_mul_f32_e32 v37, v37, v37
	v_fma_mix_f32 v36, v36, v36, v37 op_sel_hi:[1,1,0]
	v_mul_f32_e32 v37, v39, v39
	v_add_f32_e32 v56, v56, v43
	v_mul_f32_e32 v43, v43, v43
	v_fma_mix_f32 v37, v38, v38, v37 op_sel_hi:[1,1,0]
	v_mul_f32_e32 v38, v47, v47
	v_add_f32_e32 v56, v56, v57
	v_add_f32_e32 v57, v58, v39
	v_add_f32_e32 v58, v59, v47
	v_fma_mix_f32 v42, v42, v42, v43 op_sel_hi:[1,1,0]
	v_fma_mix_f32 v38, v46, v46, v38 op_sel_hi:[1,1,0]
	v_add_f32_e32 v57, v57, v58
	v_add_f32_e32 v36, v42, v36
	v_add_f32_e32 v37, v37, v38
	v_add_f32_e32 v56, v56, v57
	v_add_f32_e32 v36, v36, v37
	v_add_f32_e32 v45, v45, v56
	v_add_f32_e32 v36, v44, v36
	ds_bpermute_b32 v37, v221, v45
	ds_bpermute_b32 v38, v221, v36
	v_cvt_pk_f16_f32 v34, v34, v35
	v_cvt_pk_f16_f32 v35, v40, v41
	ds_write_b128 v235, v[32:35] offset:64
	s_waitcnt lgkmcnt(2)
	v_add_f32_e32 v32, v45, v37
	s_waitcnt lgkmcnt(1)
	v_add_f32_e32 v33, v36, v38
	ds_bpermute_b32 v63, v237, v61
	ds_bpermute_b32 v44, v237, v32
	ds_bpermute_b32 v45, v237, v33
	ds_read_b128 v[34:37], v236
	ds_read_b128 v[38:41], v236 offset:1152
	v_add_f32_e32 v42, v60, v62
	s_waitcnt lgkmcnt(4)
	v_add_f32_e32 v43, v61, v63
	s_waitcnt lgkmcnt(3)
	v_add_f32_e32 v44, v32, v44
	s_waitcnt lgkmcnt(2)
	v_add_f32_e32 v45, v33, v45
	v_add_u32_e32 v32, 0x30000, v144
	buffer_store_dwordx4 v[48:51], v32, s[24:27], 0 offen nt
	v_add_u32_e32 v32, 0x33000, v144
	buffer_store_dwordx4 v[52:55], v32, s[24:27], 0 offen nt
	v_add_co_u32_e32 v32, vcc, s76, v140
	s_nop 1
	v_addc_co_u32_e32 v33, vcc, 0, v141, vcc
	global_store_dwordx2 v[32:33], v[42:43], off
	v_add_u32_e32 v42, 0x36000, v144
	s_waitcnt lgkmcnt(1)
	buffer_store_dwordx4 v[34:37], v42, s[24:27], 0 offen nt
	s_nop 1
	v_add_u32_e32 v34, 0x39000, v144
	s_waitcnt lgkmcnt(0)
	buffer_store_dwordx4 v[38:41], v34, s[24:27], 0 offen nt
	global_store_dwordx2 v[32:33], v[44:45], off offset:1536
	s_waitcnt vmcnt(15)
	v_cvt_f32_f16_sdwa v37, v84 dst_sel:DWORD dst_unused:UNUSED_PAD src0_sel:WORD_1
	v_cvt_f32_f16_e32 v36, v84
	v_cvt_f32_f16_sdwa v35, v85 dst_sel:DWORD dst_unused:UNUSED_PAD src0_sel:WORD_1
	v_cvt_f32_f16_e32 v34, v85
	v_cvt_f32_f16_sdwa v38, v86 dst_sel:DWORD dst_unused:UNUSED_PAD src0_sel:WORD_1
	v_cvt_f32_f16_e32 v39, v86
	v_cvt_f32_f16_sdwa v40, v87 dst_sel:DWORD dst_unused:UNUSED_PAD src0_sel:WORD_1
	v_cvt_f32_f16_e32 v41, v87
	v_sub_f32_e32 v34, v34, v196
	v_sub_f32_e32 v35, v35, v196
	v_sub_f32_e32 v36, v36, v196
	v_sub_f32_e32 v37, v37, v196
	v_pk_add_f32 v[30:31], v[30:31], v[206:207]
	v_pk_add_f32 v[28:29], v[28:29], v[208:209]
	v_pk_mul_f32 v[36:37], v[196:197], v[36:37] op_sel:[1,0]
	v_pk_mul_f32 v[34:35], v[196:197], v[34:35] op_sel:[1,0]
	v_pk_fma_f32 v[28:29], v[92:93], v[36:37], v[28:29]
	v_pk_fma_f32 v[30:31], v[94:95], v[34:35], v[30:31]
	v_sub_f32_e32 v34, v41, v196
	v_sub_f32_e32 v35, v40, v196
	v_sub_f32_e32 v36, v39, v196
	v_sub_f32_e32 v37, v38, v196
	v_pk_add_f32 v[26:27], v[26:27], v[202:203]
	v_pk_add_f32 v[24:25], v[24:25], v[204:205]
	v_pk_mul_f32 v[36:37], v[196:197], v[36:37] op_sel:[1,0]
	v_pk_mul_f32 v[34:35], v[196:197], v[34:35] op_sel:[1,0]
	v_pk_add_f32 v[22:23], v[22:23], v[198:199]
	v_pk_fma_f32 v[34:35], v[90:91], v[34:35], v[26:27]
	v_pk_fma_f32 v[26:27], v[88:89], v[36:37], v[24:25]
	v_cvt_f16_f32_e32 v36, v28
	v_cvt_f16_f32_e32 v37, v29
	v_cvt_pk_f16_f32 v24, v28, v29
	v_cvt_f16_f32_e32 v28, v30
	v_cvt_f16_f32_e32 v29, v31
	v_cvt_pk_f16_f32 v25, v30, v31
	v_cvt_f16_f32_e32 v30, v26
	v_cvt_f16_f32_e32 v31, v27
	v_cvt_f16_f32_e32 v38, v34
	v_cvt_f16_f32_e32 v39, v35
	v_cvt_pk_f16_f32 v26, v26, v27
	v_cvt_pk_f16_f32 v27, v34, v35
	ds_write_b128 v235, v[24:27]
	v_cvt_f32_f16_e32 v24, v36
	v_cvt_f32_f16_e32 v25, v37
	v_cvt_f32_f16_e32 v26, v28
	v_cvt_f32_f16_e32 v27, v29
	v_cvt_f32_f16_e32 v29, v30
	v_cvt_f32_f16_e32 v31, v31
	v_cvt_f32_f16_e32 v34, v38
	v_cvt_f32_f16_e32 v35, v39
	v_add_f32_e32 v24, v24, v25
	v_add_f32_e32 v26, v26, v27
	v_add_f32_e32 v24, v24, v26
	v_add_f32_e32 v26, v29, v31
	v_add_f32_e32 v29, v34, v35
	v_add_f32_e32 v26, v26, v29
	v_add_f32_e32 v24, v24, v26
	v_add_f32_e32 v29, 0, v24
	v_mul_f32_e32 v24, v25, v25
	v_mul_f32_e32 v25, v27, v27
	v_fma_mix_f32 v24, v36, v36, v24 op_sel_hi:[1,1,0]
	v_fma_mix_f32 v25, v28, v28, v25 op_sel_hi:[1,1,0]
	v_mul_f32_e32 v26, v35, v35
	v_add_f32_e32 v24, v24, v25
	v_mul_f32_e32 v25, v31, v31
	v_fma_mix_f32 v25, v30, v30, v25 op_sel_hi:[1,1,0]
	v_fma_mix_f32 v26, v38, v38, v26 op_sel_hi:[1,1,0]
	s_waitcnt vmcnt(14)
	v_cvt_f32_f16_sdwa v27, v76 dst_sel:DWORD dst_unused:UNUSED_PAD src0_sel:WORD_1
	v_add_f32_e32 v25, v25, v26
	v_add_f32_e32 v28, v24, v25
	v_cvt_f32_f16_e32 v26, v76
	v_cvt_f32_f16_sdwa v25, v77 dst_sel:DWORD dst_unused:UNUSED_PAD src0_sel:WORD_1
	v_cvt_f32_f16_e32 v24, v77
	v_cvt_f32_f16_sdwa v30, v78 dst_sel:DWORD dst_unused:UNUSED_PAD src0_sel:WORD_1
	v_cvt_f32_f16_e32 v31, v78
	v_cvt_f32_f16_sdwa v34, v79 dst_sel:DWORD dst_unused:UNUSED_PAD src0_sel:WORD_1
	v_cvt_f32_f16_e32 v35, v79
	v_sub_f32_e32 v24, v24, v196
	v_sub_f32_e32 v25, v25, v196
	v_sub_f32_e32 v26, v26, v196
	v_sub_f32_e32 v27, v27, v196
	v_pk_add_f32 v[20:21], v[20:21], v[200:201]
	v_pk_mul_f32 v[26:27], v[196:197], v[26:27] op_sel:[1,0]
	v_pk_mul_f32 v[24:25], v[196:197], v[24:25] op_sel:[1,0]
	v_pk_fma_f32 v[20:21], v[80:81], v[26:27], v[20:21]
	v_pk_fma_f32 v[22:23], v[82:83], v[24:25], v[22:23]
	v_sub_f32_e32 v24, v35, v196
	v_sub_f32_e32 v25, v34, v196
	v_sub_f32_e32 v26, v31, v196
	v_sub_f32_e32 v27, v30, v196
	v_pk_add_f32 v[18:19], v[18:19], v[192:193]
	v_pk_add_f32 v[16:17], v[16:17], v[194:195]
	v_pk_mul_f32 v[26:27], v[196:197], v[26:27] op_sel:[1,0]
	v_pk_mul_f32 v[24:25], v[196:197], v[24:25] op_sel:[1,0]
	s_waitcnt vmcnt(13)
	v_cvt_f32_f16_sdwa v36, v71 dst_sel:DWORD dst_unused:UNUSED_PAD src0_sel:WORD_1
	v_pk_fma_f32 v[24:25], v[74:75], v[24:25], v[18:19]
	v_pk_fma_f32 v[18:19], v[72:73], v[26:27], v[16:17]
	v_cvt_f16_f32_e32 v26, v20
	v_cvt_f16_f32_e32 v27, v21
	v_cvt_pk_f16_f32 v16, v20, v21
	v_cvt_f16_f32_e32 v20, v22
	v_cvt_f16_f32_e32 v21, v23
	v_cvt_pk_f16_f32 v17, v22, v23
	v_cvt_f16_f32_e32 v23, v19
	v_cvt_f16_f32_e32 v31, v25
	v_cvt_f16_f32_e32 v22, v18
	v_cvt_f16_f32_e32 v30, v24
	v_cvt_pk_f16_f32 v18, v18, v19
	v_cvt_pk_f16_f32 v19, v24, v25
	v_cvt_f32_f16_e32 v25, v27
	v_cvt_f32_f16_e32 v27, v20
	v_cvt_f32_f16_e32 v21, v21
	v_cvt_f32_f16_e32 v23, v23
	v_cvt_f32_f16_e32 v24, v26
	v_cvt_f32_f16_e32 v31, v31
	v_cvt_f32_f16_e32 v34, v22
	v_cvt_f32_f16_e32 v35, v30
	v_add_f32_e32 v27, v27, v21
	v_mul_f32_e32 v21, v21, v21
	v_fma_mix_f32 v20, v20, v20, v21 op_sel_hi:[1,1,0]
	v_mul_f32_e32 v21, v23, v23
	v_add_f32_e32 v24, v24, v25
	v_mul_f32_e32 v25, v25, v25
	v_fma_mix_f32 v21, v22, v22, v21 op_sel_hi:[1,1,0]
	v_mul_f32_e32 v22, v31, v31
	v_add_f32_e32 v24, v24, v27
	v_add_f32_e32 v27, v34, v23
	v_add_f32_e32 v34, v35, v31
	v_fma_mix_f32 v25, v26, v26, v25 op_sel_hi:[1,1,0]
	v_fma_mix_f32 v22, v30, v30, v22 op_sel_hi:[1,1,0]
	v_add_f32_e32 v27, v27, v34
	v_add_f32_e32 v20, v25, v20
	v_add_f32_e32 v21, v21, v22
	v_add_f32_e32 v24, v24, v27
	v_add_f32_e32 v20, v20, v21
	v_add_f32_e32 v24, v29, v24
	v_add_f32_e32 v25, v28, v20
	ds_bpermute_b32 v26, v221, v24
	ds_bpermute_b32 v27, v221, v25
	v_cvt_f32_f16_sdwa v34, v70 dst_sel:DWORD dst_unused:UNUSED_PAD src0_sel:WORD_1
	v_cvt_f32_f16_e32 v35, v70
	v_cvt_f32_f16_e32 v37, v71
	s_waitcnt lgkmcnt(1)
	v_add_f32_e32 v28, v24, v26
	s_waitcnt lgkmcnt(0)
	v_add_f32_e32 v29, v25, v27
	v_cvt_f32_f16_sdwa v27, v68 dst_sel:DWORD dst_unused:UNUSED_PAD src0_sel:WORD_1
	v_cvt_f32_f16_e32 v26, v68
	v_cvt_f32_f16_sdwa v25, v69 dst_sel:DWORD dst_unused:UNUSED_PAD src0_sel:WORD_1
	v_cvt_f32_f16_e32 v24, v69
	v_sub_f32_e32 v27, v27, v190
	v_sub_f32_e32 v26, v26, v190
	v_sub_f32_e32 v25, v25, v190
	v_sub_f32_e32 v24, v24, v190
	v_pk_add_f32 v[14:15], v[14:15], v[206:207]
	v_pk_add_f32 v[12:13], v[12:13], v[208:209]
	v_pk_mul_f32 v[26:27], v[190:191], v[26:27] op_sel:[1,0]
	v_pk_mul_f32 v[24:25], v[190:191], v[24:25] op_sel:[1,0]
	v_pk_fma_f32 v[12:13], v[92:93], v[26:27], v[12:13]
	v_pk_fma_f32 v[14:15], v[94:95], v[24:25], v[14:15]
	v_sub_f32_e32 v24, v37, v190
	v_sub_f32_e32 v25, v36, v190
	v_sub_f32_e32 v26, v35, v190
	v_sub_f32_e32 v27, v34, v190
	v_pk_add_f32 v[10:11], v[10:11], v[202:203]
	v_pk_add_f32 v[8:9], v[8:9], v[204:205]
	v_pk_mul_f32 v[26:27], v[190:191], v[26:27] op_sel:[1,0]
	v_pk_mul_f32 v[24:25], v[190:191], v[24:25] op_sel:[1,0]
	ds_write_b128 v235, v[16:19] offset:64
	v_pk_fma_f32 v[24:25], v[90:91], v[24:25], v[10:11]
	v_pk_fma_f32 v[10:11], v[88:89], v[26:27], v[8:9]
	v_cvt_f16_f32_e32 v26, v12
	v_cvt_f16_f32_e32 v27, v13
	v_cvt_pk_f16_f32 v8, v12, v13
	v_cvt_f16_f32_e32 v12, v14
	v_cvt_f16_f32_e32 v13, v15
	v_cvt_pk_f16_f32 v9, v14, v15
	v_cvt_f16_f32_e32 v14, v10
	v_cvt_f16_f32_e32 v15, v11
	v_cvt_f16_f32_e32 v34, v24
	v_cvt_f16_f32_e32 v35, v25
	v_cvt_pk_f16_f32 v10, v10, v11
	v_cvt_pk_f16_f32 v11, v24, v25
	ds_read_b128 v[16:19], v236
	ds_read_b128 v[20:23], v236 offset:1152
	ds_write_b128 v235, v[8:11]
	v_cvt_f32_f16_e32 v8, v26
	v_cvt_f32_f16_e32 v9, v27
	v_cvt_f32_f16_e32 v10, v12
	v_cvt_f32_f16_e32 v11, v13
	v_cvt_f32_f16_e32 v13, v14
	v_cvt_f32_f16_e32 v15, v15
	v_cvt_f32_f16_e32 v24, v34
	v_cvt_f32_f16_e32 v25, v35
	v_add_f32_e32 v8, v8, v9
	v_add_f32_e32 v10, v10, v11
	v_add_f32_e32 v8, v8, v10
	v_add_f32_e32 v10, v13, v15
	v_add_f32_e32 v13, v24, v25
	v_add_f32_e32 v10, v10, v13
	v_add_f32_e32 v8, v8, v10
	v_add_f32_e32 v13, 0, v8
	v_mul_f32_e32 v8, v9, v9
	v_mul_f32_e32 v9, v11, v11
	v_fma_mix_f32 v8, v26, v26, v8 op_sel_hi:[1,1,0]
	v_fma_mix_f32 v9, v12, v12, v9 op_sel_hi:[1,1,0]
	v_mul_f32_e32 v10, v25, v25
	v_add_f32_e32 v8, v8, v9
	v_mul_f32_e32 v9, v15, v15
	v_fma_mix_f32 v9, v14, v14, v9 op_sel_hi:[1,1,0]
	v_fma_mix_f32 v10, v34, v34, v10 op_sel_hi:[1,1,0]
	s_waitcnt vmcnt(12)
	v_cvt_f32_f16_sdwa v11, v64 dst_sel:DWORD dst_unused:UNUSED_PAD src0_sel:WORD_1
	v_add_f32_e32 v9, v9, v10
	v_add_f32_e32 v12, v8, v9
	v_cvt_f32_f16_e32 v10, v64
	v_cvt_f32_f16_sdwa v9, v65 dst_sel:DWORD dst_unused:UNUSED_PAD src0_sel:WORD_1
	v_cvt_f32_f16_e32 v8, v65
	v_cvt_f32_f16_sdwa v14, v66 dst_sel:DWORD dst_unused:UNUSED_PAD src0_sel:WORD_1
	v_cvt_f32_f16_e32 v15, v66
	v_cvt_f32_f16_sdwa v24, v67 dst_sel:DWORD dst_unused:UNUSED_PAD src0_sel:WORD_1
	v_cvt_f32_f16_e32 v25, v67
	v_sub_f32_e32 v8, v8, v190
	v_sub_f32_e32 v9, v9, v190
	v_sub_f32_e32 v10, v10, v190
	v_sub_f32_e32 v11, v11, v190
	v_pk_add_f32 v[6:7], v[6:7], v[198:199]
	v_pk_add_f32 v[4:5], v[4:5], v[200:201]
	v_pk_mul_f32 v[10:11], v[190:191], v[10:11] op_sel:[1,0]
	v_pk_mul_f32 v[8:9], v[190:191], v[8:9] op_sel:[1,0]
	v_pk_fma_f32 v[4:5], v[80:81], v[10:11], v[4:5]
	v_pk_fma_f32 v[6:7], v[82:83], v[8:9], v[6:7]
	v_sub_f32_e32 v8, v25, v190
	v_sub_f32_e32 v9, v24, v190
	v_sub_f32_e32 v10, v15, v190
	v_sub_f32_e32 v11, v14, v190
	v_pk_add_f32 v[2:3], v[2:3], v[192:193]
	v_pk_add_f32 v[0:1], v[0:1], v[194:195]
	v_pk_mul_f32 v[10:11], v[190:191], v[10:11] op_sel:[1,0]
	v_pk_mul_f32 v[8:9], v[190:191], v[8:9] op_sel:[1,0]
	ds_bpermute_b32 v30, v237, v28
	v_pk_fma_f32 v[8:9], v[74:75], v[8:9], v[2:3]
	v_pk_fma_f32 v[2:3], v[72:73], v[10:11], v[0:1]
	v_cvt_f16_f32_e32 v10, v4
	v_cvt_f16_f32_e32 v11, v5
	v_cvt_pk_f16_f32 v0, v4, v5
	v_cvt_f16_f32_e32 v4, v6
	v_cvt_f16_f32_e32 v5, v7
	v_cvt_pk_f16_f32 v1, v6, v7
	v_cvt_f16_f32_e32 v7, v3
	v_cvt_f16_f32_e32 v15, v9
	v_cvt_f16_f32_e32 v6, v2
	v_cvt_f16_f32_e32 v14, v8
	v_cvt_f32_f16_e32 v25, v4
	v_cvt_f32_f16_e32 v5, v5
	v_cvt_f32_f16_e32 v7, v7
	v_cvt_f32_f16_e32 v24, v10
	v_cvt_f32_f16_e32 v11, v11
	v_cvt_f32_f16_e32 v15, v15
	v_cvt_f32_f16_e32 v26, v6
	v_cvt_f32_f16_e32 v27, v14
	v_add_f32_e32 v25, v25, v5
	v_mul_f32_e32 v5, v5, v5
	v_fma_mix_f32 v4, v4, v4, v5 op_sel_hi:[1,1,0]
	v_mul_f32_e32 v5, v7, v7
	v_add_f32_e32 v24, v24, v11
	v_mul_f32_e32 v11, v11, v11
	v_fma_mix_f32 v5, v6, v6, v5 op_sel_hi:[1,1,0]
	v_mul_f32_e32 v6, v15, v15
	v_add_f32_e32 v24, v24, v25
	v_add_f32_e32 v25, v26, v7
	v_add_f32_e32 v26, v27, v15
	v_fma_mix_f32 v10, v10, v10, v11 op_sel_hi:[1,1,0]
	v_fma_mix_f32 v6, v14, v14, v6 op_sel_hi:[1,1,0]
	v_add_f32_e32 v25, v25, v26
	v_add_f32_e32 v4, v10, v4
	v_add_f32_e32 v5, v5, v6
	v_add_f32_e32 v24, v24, v25
	v_add_f32_e32 v4, v4, v5
	v_add_f32_e32 v13, v13, v24
	v_add_f32_e32 v4, v12, v4
	ds_bpermute_b32 v5, v221, v13
	ds_bpermute_b32 v6, v221, v4
	v_cvt_pk_f16_f32 v2, v2, v3
	v_cvt_pk_f16_f32 v3, v8, v9
	ds_write_b128 v235, v[0:3] offset:64
	s_waitcnt lgkmcnt(2)
	v_add_f32_e32 v10, v13, v5
	s_waitcnt lgkmcnt(1)
	v_add_f32_e32 v11, v4, v6
	ds_bpermute_b32 v31, v237, v29
	ds_bpermute_b32 v12, v237, v10
	ds_bpermute_b32 v13, v237, v11
	ds_read_b128 v[0:3], v236
	ds_read_b128 v[4:7], v236 offset:1152
	v_add_f32_e32 v8, v28, v30
	s_waitcnt lgkmcnt(4)
	v_add_f32_e32 v9, v29, v31
	s_waitcnt lgkmcnt(3)
	v_add_f32_e32 v10, v10, v12
	s_waitcnt lgkmcnt(2)
	v_add_f32_e32 v11, v11, v13
	v_add_u32_e32 v12, 0x3c000, v144
	buffer_store_dwordx4 v[16:19], v12, s[24:27], 0 offen nt
	v_add_u32_e32 v12, 0x3f000, v144
	buffer_store_dwordx4 v[20:23], v12, s[24:27], 0 offen nt
	global_store_dwordx2 v[32:33], v[8:9], off offset:3072
	v_add_u32_e32 v8, 0x42000, v144
	s_waitcnt lgkmcnt(1)
	buffer_store_dwordx4 v[0:3], v8, s[24:27], 0 offen nt
	s_nop 1
	v_add_u32_e32 v0, 0x45000, v144
	s_waitcnt lgkmcnt(0)
	buffer_store_dwordx4 v[4:7], v0, s[24:27], 0 offen nt
	v_add_co_u32_e32 v0, vcc, 0x4000, v140
	s_nop 1
	v_addc_co_u32_e32 v1, vcc, 0, v141, vcc
	global_store_dwordx2 v[0:1], v[10:11], off offset:512
	s_mov_b32 s83, s81
	s_mov_b32 s84, s82
	s_mov_b64 s[40:41], s[0:1]
	s_mov_b64 s[38:39], s[8:9]
	s_mov_b64 vcc, s[6:7]
	s_cbranch_vccz .LBB8_12
	s_waitcnt vmcnt(0)
	s_cmpk_gt_u32 s44, 0xff
	s_cbranch_scc1 .LBB8_31
	s_barrier

.LBB8_32:
	s_endpgm
	s_endpgm
	s_endpgm
	s_endpgm
	s_endpgm
	s_endpgm
	s_endpgm
	s_endpgm
	s_endpgm
	s_endpgm
	s_endpgm
	s_endpgm
	s_endpgm
	s_endpgm
	s_endpgm
	s_endpgm
	s_endpgm
	s_endpgm
	s_endpgm
	s_endpgm
	s_endpgm
	s_endpgm
	s_endpgm
	s_endpgm
	s_endpgm
	s_endpgm
	s_endpgm
	s_endpgm
	s_endpgm
	s_endpgm
	s_endpgm
	s_endpgm
	s_endpgm
	s_endpgm
	s_endpgm
	s_endpgm
	s_endpgm
	s_endpgm
	s_endpgm
	s_endpgm
	s_endpgm
	s_endpgm
	s_endpgm
	s_endpgm
	s_endpgm
	s_endpgm
	s_endpgm
	s_endpgm
	s_endpgm
	s_endpgm
	s_endpgm
	s_endpgm
	s_endpgm
	s_endpgm
	.section	.rodata,"a",@progbits
	.p2align	6, 0x0
	.amdhsa_kernel _Z6k_gemmIN2pg6EpiResELi768EEvNS0_4GemmET_
		.amdhsa_group_segment_fixed_size 0
		.amdhsa_private_segment_fixed_size 0
		.amdhsa_kernarg_size 344
		.amdhsa_user_sgpr_count 2
		.amdhsa_user_sgpr_dispatch_ptr 0
		.amdhsa_user_sgpr_queue_ptr 0
		.amdhsa_user_sgpr_kernarg_segment_ptr 1
		.amdhsa_user_sgpr_dispatch_id 0
		.amdhsa_user_sgpr_kernarg_preload_length 0
		.amdhsa_user_sgpr_kernarg_preload_offset 0
		.amdhsa_user_sgpr_private_segment_size 0
		.amdhsa_uses_dynamic_stack 0
		.amdhsa_enable_private_segment 0
		.amdhsa_system_sgpr_workgroup_id_x 1
		.amdhsa_system_sgpr_workgroup_id_y 0
		.amdhsa_system_sgpr_workgroup_id_z 0
		.amdhsa_system_sgpr_workgroup_info 0
		.amdhsa_system_vgpr_workitem_id 0
		.amdhsa_next_free_vgpr 254
		.amdhsa_next_free_sgpr 100
		.amdhsa_accum_offset 256
		.amdhsa_reserve_vcc 1
		.amdhsa_float_round_mode_32 0
		.amdhsa_float_round_mode_16_64 0
		.amdhsa_float_denorm_mode_32 3
		.amdhsa_float_denorm_mode_16_64 3
		.amdhsa_dx10_clamp 1
		.amdhsa_ieee_mode 1
		.amdhsa_fp16_overflow 0
		.amdhsa_tg_split 0
		.amdhsa_exception_fp_ieee_invalid_op 0
		.amdhsa_exception_fp_denorm_src 0
		.amdhsa_exception_fp_ieee_div_zero 0
		.amdhsa_exception_fp_ieee_overflow 0
		.amdhsa_exception_fp_ieee_underflow 0
		.amdhsa_exception_fp_ieee_inexact 0
		.amdhsa_exception_int_div_zero 0
	.end_amdhsa_kernel

.LBB10_27:
	ds_read_b128 v[72:75], v231
	ds_read_b128 v[80:83], v231 offset:1024
	ds_read_b128 v[88:91], v231 offset:2048
	ds_read_b128 v[92:95], v231 offset:3072
	s_add_u32 s40, s38, 0xfff40080
	s_addc_u32 s41, s39, -1
	s_cmp_eq_u32 s87, 44
	s_cselect_b32 s43, s9, s41
	s_cselect_b32 s42, s8, s40
	s_cselect_b32 s41, s1, s86
	s_cselect_b32 s40, s0, s85
	v_lshl_add_u64 v[190:191], s[38:39], 0, v[184:185]
	s_add_i32 m0, s51, 0xc000
	ds_read_b128 v[136:139], v232
	ds_read_b128 v[148:151], v232 offset:1024
	ds_read_b128 v[152:155], v232 offset:2048
	ds_read_b128 v[156:159], v232 offset:3072
	ds_read_b128 v[160:163], v232 offset:4096
	ds_read_b128 v[164:167], v232 offset:5120
	ds_read_b128 v[168:171], v232 offset:6144
	ds_read_b128 v[172:175], v232 offset:7168
	global_load_lds_dwordx4 v[190:191], off
	v_lshl_add_u64 v[190:191], s[38:39], 0, v[186:187]
	s_add_i32 m0, s51, 0xe000
	s_nop 0
	global_load_lds_dwordx4 v[190:191], off
	s_cmp_eq_u32 s87, 44
	s_cbranch_scc0 .Lwarm_skip_r3072
	s_lshl_b32 s91, s84, 8
	s_add_i32 s91, s91, s57
	s_lshl_b32 s92, s83, 8
	s_or_b32 s92, s92, s60
	s_mul_i32 s93, s91, 0x600
	s_lshl_b32 s94, s92, 1
	s_add_u32 s93, s93, s94
	s_add_u32 s94, s10, s93
	s_addc_u32 s95, s11, 0
	v_mul_u32_u24_e32 v250, 0x600, v234
	v_and_b32_e32 v251, 3, v234
	v_and_b32_e32 v253, 4, v234
	s_add_u32 s96, s94, 0x30000
	s_addc_u32 s97, s95, 0
	v_lshlrev_b32_e32 v251, 7, v251
	s_lshl_b32 s93, s91, 3
	global_load_dword v252, v250, s[94:95]
	v_lshl_or_b32 v251, v253, 8, v251
	s_add_u32 s98, s12, s93
	s_addc_u32 s99, s13, 0
	global_load_dword v252, v250, s[96:97]
	global_load_dword v252, v251, s[98:99]
.Lwarm_skip_r3072:
	s_waitcnt lgkmcnt(8)
	s_barrier
	s_waitcnt lgkmcnt(0)
	s_setprio 1
	s_waitcnt lgkmcnt(0)
	v_mfma_f32_16x16x32_f16 v[144:147], v[72:75], v[136:139], v[144:147]
	v_mfma_f32_16x16x32_f16 v[140:143], v[88:91], v[136:139], v[140:143]
	v_mfma_f32_16x16x32_f16 v[124:127], v[72:75], v[152:155], v[124:127]
	v_mfma_f32_16x16x32_f16 v[120:123], v[88:91], v[152:155], v[120:123]
	v_mfma_f32_16x16x32_f16 v[108:111], v[72:75], v[160:163], v[108:111]
	v_mfma_f32_16x16x32_f16 v[104:107], v[88:91], v[160:163], v[104:107]
	v_mfma_f32_16x16x32_f16 v[84:87], v[72:75], v[168:171], v[84:87]
	v_mfma_f32_16x16x32_f16 v[76:79], v[88:91], v[168:171], v[76:79]
	v_mfma_f32_16x16x32_f16 v[144:147], v[80:83], v[148:151], v[144:147]
	v_mfma_f32_16x16x32_f16 v[140:143], v[92:95], v[148:151], v[140:143]
	v_mfma_f32_16x16x32_f16 v[124:127], v[80:83], v[156:159], v[124:127]
	v_mfma_f32_16x16x32_f16 v[120:123], v[92:95], v[156:159], v[120:123]
	v_mfma_f32_16x16x32_f16 v[108:111], v[80:83], v[164:167], v[108:111]
	v_mfma_f32_16x16x32_f16 v[104:107], v[92:95], v[164:167], v[104:107]
	v_mfma_f32_16x16x32_f16 v[84:87], v[80:83], v[172:175], v[84:87]
	v_mfma_f32_16x16x32_f16 v[76:79], v[92:95], v[172:175], v[76:79]
	s_setprio 0
	s_barrier
	s_add_i32 s88, s69, s50
	v_lshl_add_u64 v[206:207], s[40:41], 0, v[178:179]
	s_mov_b32 m0, s88
	ds_read_b128 v[190:193], v233
	ds_read_b128 v[194:197], v233 offset:1024
	ds_read_b128 v[198:201], v233 offset:2048
	ds_read_b128 v[202:205], v233 offset:3072
	global_load_lds_dwordx4 v[206:207], off
	v_lshl_add_u64 v[208:209], s[40:41], 0, v[182:183]
	s_add_i32 m0, s88, 0x2000
	s_nop 0
	global_load_lds_dwordx4 v[208:209], off
	s_barrier
	s_waitcnt lgkmcnt(0)
	s_setprio 1
	s_waitcnt lgkmcnt(0)
	v_mfma_f32_16x16x32_f16 v[132:135], v[190:193], v[136:139], v[132:135]
	v_mfma_f32_16x16x32_f16 v[128:131], v[198:201], v[136:139], v[128:131]
	v_mfma_f32_16x16x32_f16 v[116:119], v[190:193], v[152:155], v[116:119]
	v_mfma_f32_16x16x32_f16 v[112:115], v[198:201], v[152:155], v[112:115]
	v_mfma_f32_16x16x32_f16 v[100:103], v[190:193], v[160:163], v[100:103]
	v_mfma_f32_16x16x32_f16 v[96:99], v[198:201], v[160:163], v[96:99]
	v_mfma_f32_16x16x32_f16 v[68:71], v[190:193], v[168:171], v[68:71]
	v_mfma_f32_16x16x32_f16 v[64:67], v[198:201], v[168:171], v[64:67]
	v_mfma_f32_16x16x32_f16 v[132:135], v[194:197], v[148:151], v[132:135]
	v_mfma_f32_16x16x32_f16 v[128:131], v[202:205], v[148:151], v[128:131]
	v_mfma_f32_16x16x32_f16 v[116:119], v[194:197], v[156:159], v[116:119]
	v_mfma_f32_16x16x32_f16 v[112:115], v[202:205], v[156:159], v[112:115]
	v_mfma_f32_16x16x32_f16 v[100:103], v[194:197], v[164:167], v[100:103]
	v_mfma_f32_16x16x32_f16 v[96:99], v[202:205], v[164:167], v[96:99]
	v_mfma_f32_16x16x32_f16 v[68:71], v[194:197], v[172:175], v[68:71]
	v_mfma_f32_16x16x32_f16 v[64:67], v[202:205], v[172:175], v[64:67]
	s_setprio 0
	s_mov_b32 m0, s51
	v_lshl_add_u64 v[210:211], s[42:43], 0, v[176:177]
	s_barrier
	ds_read_b128 v[136:139], v232 offset:16384
	ds_read_b128 v[148:151], v232 offset:17408
	ds_read_b128 v[152:155], v232 offset:18432
	ds_read_b128 v[156:159], v232 offset:19456
	ds_read_b128 v[160:163], v232 offset:20480
	ds_read_b128 v[164:167], v232 offset:21504
	ds_read_b128 v[168:171], v232 offset:22528
	ds_read_b128 v[172:175], v232 offset:23552
	global_load_lds_dwordx4 v[210:211], off
	v_lshl_add_u64 v[212:213], s[42:43], 0, v[180:181]
	s_mov_b32 m0, s52
	s_nop 0
	global_load_lds_dwordx4 v[212:213], off
	s_barrier
	s_waitcnt lgkmcnt(0)
	s_setprio 1
	s_waitcnt lgkmcnt(0)
	v_mfma_f32_16x16x32_f16 v[60:63], v[72:75], v[136:139], v[60:63]
	v_mfma_f32_16x16x32_f16 v[56:59], v[88:91], v[136:139], v[56:59]
	v_mfma_f32_16x16x32_f16 v[44:47], v[72:75], v[152:155], v[44:47]
	v_mfma_f32_16x16x32_f16 v[40:43], v[88:91], v[152:155], v[40:43]
	v_mfma_f32_16x16x32_f16 v[28:31], v[72:75], v[160:163], v[28:31]
	v_mfma_f32_16x16x32_f16 v[24:27], v[88:91], v[160:163], v[24:27]
	v_mfma_f32_16x16x32_f16 v[12:15], v[72:75], v[168:171], v[12:15]
	v_mfma_f32_16x16x32_f16 v[8:11], v[88:91], v[168:171], v[8:11]
	v_mfma_f32_16x16x32_f16 v[60:63], v[80:83], v[148:151], v[60:63]
	v_mfma_f32_16x16x32_f16 v[56:59], v[92:95], v[148:151], v[56:59]
	v_mfma_f32_16x16x32_f16 v[44:47], v[80:83], v[156:159], v[44:47]
	v_mfma_f32_16x16x32_f16 v[40:43], v[92:95], v[156:159], v[40:43]
	v_mfma_f32_16x16x32_f16 v[28:31], v[80:83], v[164:167], v[28:31]
	v_mfma_f32_16x16x32_f16 v[24:27], v[92:95], v[164:167], v[24:27]
	v_mfma_f32_16x16x32_f16 v[12:15], v[80:83], v[172:175], v[12:15]
	v_mfma_f32_16x16x32_f16 v[8:11], v[92:95], v[172:175], v[8:11]
	s_setprio 0
	s_barrier
	s_add_u32 s88, s40, 0x30000
	s_addc_u32 s89, s41, 0
	s_add_i32 s90, s70, s50
	v_lshl_add_u64 v[72:73], s[88:89], 0, v[178:179]
	s_mov_b32 m0, s90
	s_nop 0
	global_load_lds_dwordx4 v[72:73], off
	v_lshl_add_u64 v[72:73], s[88:89], 0, v[182:183]
	s_add_i32 m0, s90, 0x2000
	s_nop 0
	global_load_lds_dwordx4 v[72:73], off
	s_cmp_eq_u32 s87, 44
	s_cbranch_scc1 .Lwarm_w9_r3072
	s_waitcnt vmcnt(6)
	s_branch .Lwarm_wj_r3072

.Lwarm_wj_r3072:
	s_barrier
	s_setprio 1
	v_mfma_f32_16x16x32_f16 v[52:55], v[190:193], v[136:139], v[52:55]
	v_mfma_f32_16x16x32_f16 v[48:51], v[198:201], v[136:139], v[48:51]
	v_mfma_f32_16x16x32_f16 v[36:39], v[190:193], v[152:155], v[36:39]
	v_mfma_f32_16x16x32_f16 v[32:35], v[198:201], v[152:155], v[32:35]
	v_mfma_f32_16x16x32_f16 v[20:23], v[190:193], v[160:163], v[20:23]
	v_mfma_f32_16x16x32_f16 v[16:19], v[198:201], v[160:163], v[16:19]
	v_mfma_f32_16x16x32_f16 v[4:7], v[190:193], v[168:171], v[4:7]
	v_mfma_f32_16x16x32_f16 v[0:3], v[198:201], v[168:171], v[0:3]
	v_mfma_f32_16x16x32_f16 v[52:55], v[194:197], v[148:151], v[52:55]
	v_mfma_f32_16x16x32_f16 v[48:51], v[202:205], v[148:151], v[48:51]
	v_mfma_f32_16x16x32_f16 v[36:39], v[194:197], v[156:159], v[36:39]
	v_mfma_f32_16x16x32_f16 v[32:35], v[202:205], v[156:159], v[32:35]
	v_mfma_f32_16x16x32_f16 v[20:23], v[194:197], v[164:167], v[20:23]
	v_mfma_f32_16x16x32_f16 v[16:19], v[202:205], v[164:167], v[16:19]
	v_mfma_f32_16x16x32_f16 v[4:7], v[194:197], v[172:175], v[4:7]
	v_mfma_f32_16x16x32_f16 v[0:3], v[202:205], v[172:175], v[0:3]
	s_setprio 0
	s_add_i32 s88, 0, 0x18000
	v_add_u32_e32 v92, s88, v228
	s_barrier
	ds_read_b128 v[72:75], v92
	ds_read_b128 v[80:83], v92 offset:1024
	ds_read_b128 v[88:91], v92 offset:2048
	ds_read_b128 v[92:95], v92 offset:3072
	s_add_u32 s42, s42, 0xc0000
	s_addc_u32 s43, s43, 0
	s_mov_b32 m0, s53
	v_lshl_add_u64 v[190:191], s[42:43], 0, v[176:177]
	ds_read_b128 v[136:139], v232 offset:32768
	ds_read_b128 v[148:151], v232 offset:33792
	ds_read_b128 v[152:155], v232 offset:34816
	ds_read_b128 v[156:159], v232 offset:35840
	ds_read_b128 v[160:163], v232 offset:36864
	ds_read_b128 v[164:167], v232 offset:37888
	ds_read_b128 v[168:171], v232 offset:38912
	ds_read_b128 v[172:175], v232 offset:39936
	global_load_lds_dwordx4 v[190:191], off
	v_lshl_add_u64 v[190:191], s[42:43], 0, v[180:181]
	s_mov_b32 m0, s54
	s_nop 0
	global_load_lds_dwordx4 v[190:191], off
	s_waitcnt lgkmcnt(8)
	s_barrier
	s_waitcnt lgkmcnt(0)
	s_setprio 1
	s_waitcnt lgkmcnt(0)
	v_mfma_f32_16x16x32_f16 v[144:147], v[72:75], v[136:139], v[144:147]
	v_mfma_f32_16x16x32_f16 v[140:143], v[88:91], v[136:139], v[140:143]
	v_mfma_f32_16x16x32_f16 v[124:127], v[72:75], v[152:155], v[124:127]
	v_mfma_f32_16x16x32_f16 v[120:123], v[88:91], v[152:155], v[120:123]
	v_mfma_f32_16x16x32_f16 v[108:111], v[72:75], v[160:163], v[108:111]
	v_mfma_f32_16x16x32_f16 v[104:107], v[88:91], v[160:163], v[104:107]
	v_mfma_f32_16x16x32_f16 v[84:87], v[72:75], v[168:171], v[84:87]
	v_mfma_f32_16x16x32_f16 v[76:79], v[88:91], v[168:171], v[76:79]
	v_mfma_f32_16x16x32_f16 v[144:147], v[80:83], v[148:151], v[144:147]
	v_mfma_f32_16x16x32_f16 v[140:143], v[92:95], v[148:151], v[140:143]
	v_mfma_f32_16x16x32_f16 v[124:127], v[80:83], v[156:159], v[124:127]
	v_mfma_f32_16x16x32_f16 v[120:123], v[92:95], v[156:159], v[120:123]
	v_mfma_f32_16x16x32_f16 v[108:111], v[80:83], v[164:167], v[108:111]
	v_mfma_f32_16x16x32_f16 v[104:107], v[92:95], v[164:167], v[104:107]
	v_mfma_f32_16x16x32_f16 v[84:87], v[80:83], v[172:175], v[84:87]
	v_mfma_f32_16x16x32_f16 v[76:79], v[92:95], v[172:175], v[76:79]
	s_setprio 0
	s_barrier
	s_add_i32 s42, 0, 0x1c000
	s_add_i32 s43, s88, s50
	v_add_u32_e32 v202, s42, v228
	v_lshl_add_u64 v[206:207], v[206:207], 0, s[36:37]
	s_mov_b32 m0, s43
	ds_read_b128 v[190:193], v202
	ds_read_b128 v[194:197], v202 offset:1024
	ds_read_b128 v[198:201], v202 offset:2048
	ds_read_b128 v[202:205], v202 offset:3072
	global_load_lds_dwordx4 v[206:207], off
	v_lshl_add_u64 v[206:207], v[208:209], 0, s[36:37]
	s_add_i32 m0, s43, 0x2000
	s_nop 0
	global_load_lds_dwordx4 v[206:207], off
	s_barrier
	s_waitcnt lgkmcnt(0)
	s_setprio 1
	s_waitcnt lgkmcnt(0)
	v_mfma_f32_16x16x32_f16 v[132:135], v[190:193], v[136:139], v[132:135]
	v_mfma_f32_16x16x32_f16 v[128:131], v[198:201], v[136:139], v[128:131]
	v_mfma_f32_16x16x32_f16 v[116:119], v[190:193], v[152:155], v[116:119]
	v_mfma_f32_16x16x32_f16 v[112:115], v[198:201], v[152:155], v[112:115]
	v_mfma_f32_16x16x32_f16 v[100:103], v[190:193], v[160:163], v[100:103]
	v_mfma_f32_16x16x32_f16 v[96:99], v[198:201], v[160:163], v[96:99]
	v_mfma_f32_16x16x32_f16 v[68:71], v[190:193], v[168:171], v[68:71]
	v_mfma_f32_16x16x32_f16 v[64:67], v[198:201], v[168:171], v[64:67]
	v_mfma_f32_16x16x32_f16 v[132:135], v[194:197], v[148:151], v[132:135]
	v_mfma_f32_16x16x32_f16 v[128:131], v[202:205], v[148:151], v[128:131]
	v_mfma_f32_16x16x32_f16 v[116:119], v[194:197], v[156:159], v[116:119]
	v_mfma_f32_16x16x32_f16 v[112:115], v[202:205], v[156:159], v[112:115]
	v_mfma_f32_16x16x32_f16 v[100:103], v[194:197], v[164:167], v[100:103]
	v_mfma_f32_16x16x32_f16 v[96:99], v[202:205], v[164:167], v[96:99]
	v_mfma_f32_16x16x32_f16 v[68:71], v[194:197], v[172:175], v[68:71]
	v_mfma_f32_16x16x32_f16 v[64:67], v[202:205], v[172:175], v[64:67]
	s_setprio 0
	s_mov_b32 m0, s58
	v_lshl_add_u64 v[206:207], v[210:211], 0, s[36:37]
	s_barrier
	ds_read_b128 v[136:139], v232 offset:49152
	ds_read_b128 v[148:151], v232 offset:50176
	ds_read_b128 v[152:155], v232 offset:51200
	ds_read_b128 v[156:159], v232 offset:52224
	ds_read_b128 v[160:163], v232 offset:53248
	ds_read_b128 v[164:167], v232 offset:54272
	ds_read_b128 v[168:171], v232 offset:55296
	ds_read_b128 v[172:175], v232 offset:56320
	global_load_lds_dwordx4 v[206:207], off
	v_lshl_add_u64 v[206:207], v[212:213], 0, s[36:37]
	s_mov_b32 m0, s59
	s_nop 0
	global_load_lds_dwordx4 v[206:207], off
	s_barrier
	s_waitcnt lgkmcnt(0)
	s_setprio 1
	s_waitcnt lgkmcnt(0)
	v_mfma_f32_16x16x32_f16 v[60:63], v[72:75], v[136:139], v[60:63]
	v_mfma_f32_16x16x32_f16 v[56:59], v[88:91], v[136:139], v[56:59]
	v_mfma_f32_16x16x32_f16 v[44:47], v[72:75], v[152:155], v[44:47]
	v_mfma_f32_16x16x32_f16 v[40:43], v[88:91], v[152:155], v[40:43]
	v_mfma_f32_16x16x32_f16 v[28:31], v[72:75], v[160:163], v[28:31]
	v_mfma_f32_16x16x32_f16 v[24:27], v[88:91], v[160:163], v[24:27]
	v_mfma_f32_16x16x32_f16 v[12:15], v[72:75], v[168:171], v[12:15]
	v_mfma_f32_16x16x32_f16 v[8:11], v[88:91], v[168:171], v[8:11]
	v_mfma_f32_16x16x32_f16 v[60:63], v[80:83], v[148:151], v[60:63]
	v_mfma_f32_16x16x32_f16 v[56:59], v[92:95], v[148:151], v[56:59]
	v_mfma_f32_16x16x32_f16 v[44:47], v[80:83], v[156:159], v[44:47]
	v_mfma_f32_16x16x32_f16 v[40:43], v[92:95], v[156:159], v[40:43]
	v_mfma_f32_16x16x32_f16 v[28:31], v[80:83], v[164:167], v[28:31]
	v_mfma_f32_16x16x32_f16 v[24:27], v[92:95], v[164:167], v[24:27]
	v_mfma_f32_16x16x32_f16 v[12:15], v[80:83], v[172:175], v[12:15]
	v_mfma_f32_16x16x32_f16 v[8:11], v[92:95], v[172:175], v[8:11]
	s_setprio 0
	s_barrier
	s_add_u32 s40, s40, 0x30080
	s_addc_u32 s41, s41, 0
	s_add_i32 s42, s42, s50
	v_lshl_add_u64 v[72:73], s[40:41], 0, v[178:179]
	s_mov_b32 m0, s42
	s_nop 0
	global_load_lds_dwordx4 v[72:73], off
	v_lshl_add_u64 v[72:73], s[40:41], 0, v[182:183]
	s_add_i32 m0, s42, 0x2000
	s_nop 0
	global_load_lds_dwordx4 v[72:73], off
	s_waitcnt vmcnt(6)
	s_barrier
	s_setprio 1
	v_mfma_f32_16x16x32_f16 v[52:55], v[190:193], v[136:139], v[52:55]
	v_mfma_f32_16x16x32_f16 v[48:51], v[198:201], v[136:139], v[48:51]
	v_mfma_f32_16x16x32_f16 v[36:39], v[190:193], v[152:155], v[36:39]
	v_mfma_f32_16x16x32_f16 v[32:35], v[198:201], v[152:155], v[32:35]
	v_mfma_f32_16x16x32_f16 v[20:23], v[190:193], v[160:163], v[20:23]
	v_mfma_f32_16x16x32_f16 v[16:19], v[198:201], v[160:163], v[16:19]
	v_mfma_f32_16x16x32_f16 v[4:7], v[190:193], v[168:171], v[4:7]
	v_mfma_f32_16x16x32_f16 v[0:3], v[198:201], v[168:171], v[0:3]
	v_mfma_f32_16x16x32_f16 v[52:55], v[194:197], v[148:151], v[52:55]
	v_mfma_f32_16x16x32_f16 v[48:51], v[202:205], v[148:151], v[48:51]
	v_mfma_f32_16x16x32_f16 v[36:39], v[194:197], v[156:159], v[36:39]
	v_mfma_f32_16x16x32_f16 v[32:35], v[202:205], v[156:159], v[32:35]
	v_mfma_f32_16x16x32_f16 v[20:23], v[194:197], v[164:167], v[20:23]
	v_mfma_f32_16x16x32_f16 v[16:19], v[202:205], v[164:167], v[16:19]
	v_mfma_f32_16x16x32_f16 v[4:7], v[194:197], v[172:175], v[4:7]
	v_mfma_f32_16x16x32_f16 v[0:3], v[202:205], v[172:175], v[0:3]
	s_setprio 0
	s_add_i32 s87, s87, 2
	s_add_u32 s38, s38, 0x100
	s_addc_u32 s39, s39, 0
	s_add_u32 s85, s85, 0x100
	s_addc_u32 s86, s86, 0
	s_cmp_gt_u32 s87, 45
	s_barrier
	s_cbranch_scc0 .LBB10_27
	s_lshl_b32 s38, s84, 8
	s_lshl_b32 s39, s83, 8
	s_add_i32 s38, s38, s57
	s_or_b32 s39, s39, s60
	v_or_b32_e32 v72, s39, v226
	v_or_b32_e32 v220, s38, v227
	v_mov_b64_e32 v[74:75], s[10:11]
	v_mad_i64_i32 v[74:75], s[40:41], v220, s71, v[74:75]
	v_ashrrev_i32_e32 v73, 31, v72
	v_lshl_add_u64 v[214:215], v[72:73], 1, v[74:75]
	v_add_co_u32_e32 v74, vcc, 0x6000, v214
	global_load_dwordx4 v[172:175], v[214:215], off nt
	global_load_dwordx4 v[168:171], v[214:215], off offset:64 nt
	v_addc_co_u32_e32 v75, vcc, 0, v215, vcc
	global_load_dwordx4 v[164:167], v[74:75], off nt
	global_load_dwordx4 v[160:163], v[74:75], off offset:64 nt
	v_add_co_u32_e32 v74, vcc, 0xc000, v214
	v_ashrrev_i32_e32 v221, 31, v220
	s_nop 0
	v_addc_co_u32_e32 v75, vcc, 0, v215, vcc
	global_load_dwordx4 v[156:159], v[74:75], off nt
	global_load_dwordx4 v[152:155], v[74:75], off offset:64 nt
	v_add_co_u32_e32 v74, vcc, s56, v214
	v_lshlrev_b64 v[72:73], 2, v[72:73]
	s_nop 0
	v_addc_co_u32_e32 v75, vcc, 0, v215, vcc
	global_load_dwordx4 v[148:151], v[74:75], off nt
	global_load_dwordx4 v[136:139], v[74:75], off offset:64 nt
	v_lshl_add_u64 v[74:75], v[220:221], 3, s[12:13]
	v_lshl_add_u64 v[238:239], s[14:15], 0, v[72:73]
	global_load_dwordx2 v[224:225], v[74:75], off
	global_load_dwordx2 v[222:223], v[74:75], off offset:128
	global_load_dwordx2 v[218:219], v[74:75], off offset:256
	global_load_dwordx2 v[216:217], v[74:75], off offset:384
	global_load_dwordx2 v[212:213], v[74:75], off offset:1024
	global_load_dwordx2 v[210:211], v[74:75], off offset:1152
	global_load_dwordx2 v[196:197], v[74:75], off offset:1280
	global_load_dwordx2 v[190:191], v[74:75], off offset:1408
	v_lshl_add_u64 v[242:243], s[16:17], 0, v[72:73]
	v_lshl_add_u64 v[246:247], s[18:19], 0, v[72:73]
	global_load_dwordx4 v[88:91], v[238:239], off offset:16
	global_load_dwordx4 v[92:95], v[238:239], off
	global_load_dwordx4 v[72:75], v[242:243], off offset:16
	global_load_dwordx4 v[80:83], v[242:243], off
	global_load_dwordx4 v[192:195], v[246:247], off offset:16
	global_load_dwordx4 v[198:201], v[246:247], off
	v_or_b32_e32 v221, s38, v229
	v_mul_lo_u32 v221, v221, s72
	v_and_b32_e32 v237, 64, v234
	v_add_u32_e32 v237, 64, v237
	s_lshl_b32 s38, s83, 2
	s_waitcnt vmcnt(0)
	v_pk_add_f32 v[202:203], v[74:75], v[194:195]
	v_pk_add_f32 v[206:207], v[82:83], v[200:201]
	v_pk_add_f32 v[208:209], v[80:81], v[198:199]
	v_pk_add_f32 v[204:205], v[72:73], v[192:193]
	global_load_dwordx4 v[72:75], v[238:239], off offset:144
	global_load_dwordx4 v[80:83], v[238:239], off offset:128
	s_nop 0
	global_load_dwordx4 v[238:241], v[242:243], off offset:144
	global_load_dwordx4 v[192:195], v[242:243], off offset:128
	s_nop 0
	global_load_dwordx4 v[242:245], v[246:247], off offset:144
	s_nop 0
	global_load_dwordx4 v[246:249], v[246:247], off offset:128
	v_pk_add_f32 v[146:147], v[146:147], v[206:207]
	v_pk_add_f32 v[144:145], v[144:145], v[208:209]
	v_pk_add_f32 v[142:143], v[142:143], v[202:203]
	v_pk_add_f32 v[140:141], v[140:141], v[204:205]
	v_pk_add_f32 v[126:127], v[126:127], v[206:207]
	v_pk_add_f32 v[124:125], v[124:125], v[208:209]
	v_pk_add_f32 v[122:123], v[122:123], v[202:203]
	v_pk_add_f32 v[120:121], v[120:121], v[204:205]
	s_waitcnt vmcnt(0)
	v_pk_add_f32 v[198:199], v[194:195], v[248:249]
	v_pk_add_f32 v[194:195], v[238:239], v[242:243]
	v_add_u32_e32 v238, s39, v221
	v_xor_b32_e32 v221, 16, v234
	v_cmp_lt_i32_e32 vcc, v221, v237
	v_xor_b32_e32 v239, 32, v234
	v_pk_add_f32 v[200:201], v[192:193], v[246:247]
	v_cndmask_b32_e32 v221, v234, v221, vcc
	v_cmp_lt_i32_e32 vcc, v239, v237
	v_pk_add_f32 v[192:193], v[240:241], v[244:245]
	v_cvt_f32_f16_e32 v240, v172
	v_cndmask_b32_e32 v237, v234, v239, vcc
	v_cvt_f32_f16_sdwa v239, v172 dst_sel:DWORD dst_unused:UNUSED_PAD src0_sel:WORD_1
	v_cvt_f32_f16_sdwa v241, v173 dst_sel:DWORD dst_unused:UNUSED_PAD src0_sel:WORD_1
	v_cvt_f32_f16_e32 v172, v173
	v_cvt_f32_f16_sdwa v242, v174 dst_sel:DWORD dst_unused:UNUSED_PAD src0_sel:WORD_1
	v_cvt_f32_f16_e32 v243, v174
	v_cvt_f32_f16_sdwa v244, v175 dst_sel:DWORD dst_unused:UNUSED_PAD src0_sel:WORD_1
	v_cvt_f32_f16_e32 v245, v175
	v_sub_f32_e32 v172, v172, v224
	v_sub_f32_e32 v173, v241, v224
	v_sub_f32_e32 v174, v240, v224
	v_sub_f32_e32 v175, v239, v224
	v_pk_mul_f32 v[174:175], v[224:225], v[174:175] op_sel:[1,0]
	v_pk_mul_f32 v[172:173], v[224:225], v[172:173] op_sel:[1,0]
	v_pk_fma_f32 v[144:145], v[174:175], v[92:93], v[144:145]
	v_pk_fma_f32 v[146:147], v[172:173], v[94:95], v[146:147]
	v_sub_f32_e32 v172, v245, v224
	v_sub_f32_e32 v173, v244, v224
	v_sub_f32_e32 v174, v243, v224
	v_sub_f32_e32 v175, v242, v224
	v_pk_mul_f32 v[174:175], v[224:225], v[174:175] op_sel:[1,0]
	v_pk_mul_f32 v[172:173], v[224:225], v[172:173] op_sel:[1,0]
	v_pk_add_f32 v[134:135], v[134:135], v[198:199]
	v_pk_fma_f32 v[172:173], v[172:173], v[90:91], v[142:143]
	v_pk_fma_f32 v[142:143], v[174:175], v[88:89], v[140:141]
	v_cvt_f16_f32_e32 v174, v144
	v_cvt_f16_f32_e32 v175, v145
	v_cvt_pk_f16_f32 v140, v144, v145
	v_cvt_f16_f32_e32 v144, v146
	v_cvt_f16_f32_e32 v145, v147
	v_cvt_pk_f16_f32 v141, v146, v147
	v_cvt_f16_f32_e32 v146, v142
	v_cvt_f16_f32_e32 v147, v143
	v_cvt_f16_f32_e32 v239, v172
	v_cvt_f16_f32_e32 v240, v173
	v_cvt_pk_f16_f32 v142, v142, v143
	v_cvt_pk_f16_f32 v143, v172, v173
	ds_write_b128 v235, v[140:143]
	v_cvt_f32_f16_e32 v140, v174
	v_cvt_f32_f16_e32 v141, v175
	v_cvt_f32_f16_e32 v142, v144
	v_cvt_f32_f16_e32 v143, v145
	v_cvt_f32_f16_e32 v145, v146
	v_cvt_f32_f16_e32 v147, v147
	v_cvt_f32_f16_e32 v172, v239
	v_cvt_f32_f16_e32 v173, v240
	v_add_f32_e32 v140, v140, v141
	v_add_f32_e32 v142, v142, v143
	v_add_f32_e32 v140, v140, v142
	v_add_f32_e32 v142, v145, v147
	v_add_f32_e32 v145, v172, v173
	v_add_f32_e32 v142, v142, v145
	v_add_f32_e32 v140, v140, v142
	v_add_f32_e32 v145, 0, v140
	v_mul_f32_e32 v140, v141, v141
	v_mul_f32_e32 v141, v143, v143
	v_fma_mix_f32 v140, v174, v174, v140 op_sel_hi:[1,1,0]
	v_fma_mix_f32 v141, v144, v144, v141 op_sel_hi:[1,1,0]
	v_mul_f32_e32 v142, v173, v173
	v_add_f32_e32 v140, v140, v141
	v_mul_f32_e32 v141, v147, v147
	v_fma_mix_f32 v141, v146, v146, v141 op_sel_hi:[1,1,0]
	v_fma_mix_f32 v142, v239, v239, v142 op_sel_hi:[1,1,0]
	v_cvt_f32_f16_sdwa v143, v168 dst_sel:DWORD dst_unused:UNUSED_PAD src0_sel:WORD_1
	v_add_f32_e32 v141, v141, v142
	v_add_f32_e32 v144, v140, v141
	v_cvt_f32_f16_e32 v142, v168
	v_cvt_f32_f16_sdwa v141, v169 dst_sel:DWORD dst_unused:UNUSED_PAD src0_sel:WORD_1
	v_cvt_f32_f16_e32 v140, v169
	v_cvt_f32_f16_sdwa v146, v170 dst_sel:DWORD dst_unused:UNUSED_PAD src0_sel:WORD_1
	v_cvt_f32_f16_e32 v147, v170
	v_cvt_f32_f16_sdwa v168, v171 dst_sel:DWORD dst_unused:UNUSED_PAD src0_sel:WORD_1
	v_cvt_f32_f16_e32 v169, v171
	v_sub_f32_e32 v140, v140, v224
	v_sub_f32_e32 v141, v141, v224
	v_sub_f32_e32 v142, v142, v224
	v_sub_f32_e32 v143, v143, v224
	v_pk_add_f32 v[132:133], v[132:133], v[200:201]
	v_pk_mul_f32 v[142:143], v[224:225], v[142:143] op_sel:[1,0]
	v_pk_mul_f32 v[140:141], v[224:225], v[140:141] op_sel:[1,0]
	v_pk_fma_f32 v[132:133], v[142:143], v[80:81], v[132:133]
	v_pk_fma_f32 v[134:135], v[140:141], v[82:83], v[134:135]
	v_sub_f32_e32 v140, v169, v224
	v_sub_f32_e32 v141, v168, v224
	v_sub_f32_e32 v142, v147, v224
	v_sub_f32_e32 v143, v146, v224
	v_pk_add_f32 v[130:131], v[130:131], v[192:193]
	v_pk_add_f32 v[128:129], v[128:129], v[194:195]
	v_pk_mul_f32 v[142:143], v[224:225], v[142:143] op_sel:[1,0]
	v_pk_mul_f32 v[140:141], v[224:225], v[140:141] op_sel:[1,0]
	v_lshlrev_b32_e32 v221, 2, v221
	v_pk_fma_f32 v[140:141], v[140:141], v[74:75], v[130:131]
	v_pk_fma_f32 v[130:131], v[142:143], v[72:73], v[128:129]
	v_cvt_f16_f32_e32 v142, v132
	v_cvt_f16_f32_e32 v143, v133
	v_cvt_pk_f16_f32 v128, v132, v133
	v_cvt_f16_f32_e32 v132, v134
	v_cvt_f16_f32_e32 v133, v135
	v_cvt_pk_f16_f32 v129, v134, v135
	v_cvt_f16_f32_e32 v134, v130
	v_cvt_f16_f32_e32 v135, v131
	v_cvt_f16_f32_e32 v146, v140
	v_cvt_f16_f32_e32 v147, v141
	v_cvt_pk_f16_f32 v130, v130, v131
	v_cvt_pk_f16_f32 v131, v140, v141
	ds_write_b128 v235, v[128:131] offset:64
	v_cvt_f32_f16_e32 v128, v142
	v_cvt_f32_f16_e32 v129, v143
	v_cvt_f32_f16_e32 v130, v132
	v_cvt_f32_f16_e32 v131, v133
	v_cvt_f32_f16_e32 v133, v134
	v_cvt_f32_f16_e32 v135, v135
	v_cvt_f32_f16_e32 v140, v146
	v_cvt_f32_f16_e32 v141, v147
	v_add_f32_e32 v128, v128, v129
	v_add_f32_e32 v130, v130, v131
	v_add_f32_e32 v128, v128, v130
	v_add_f32_e32 v130, v133, v135
	v_add_f32_e32 v133, v140, v141
	v_add_f32_e32 v130, v130, v133
	v_add_f32_e32 v128, v128, v130
	v_add_f32_e32 v140, v145, v128
	v_mul_f32_e32 v128, v129, v129
	v_mul_f32_e32 v129, v131, v131
	v_fma_mix_f32 v128, v142, v142, v128 op_sel_hi:[1,1,0]
	v_fma_mix_f32 v129, v132, v132, v129 op_sel_hi:[1,1,0]
	v_mul_f32_e32 v130, v141, v141
	v_add_f32_e32 v128, v128, v129
	v_mul_f32_e32 v129, v135, v135
	ds_bpermute_b32 v142, v221, v140
	v_fma_mix_f32 v129, v134, v134, v129 op_sel_hi:[1,1,0]
	v_fma_mix_f32 v130, v146, v146, v130 op_sel_hi:[1,1,0]
	v_lshlrev_b32_e32 v237, 2, v237
	v_add_f32_e32 v129, v129, v130
	v_add_f32_e32 v128, v128, v129
	v_add_f32_e32 v141, v144, v128
	s_waitcnt lgkmcnt(0)
	v_add_f32_e32 v140, v140, v142
	ds_bpermute_b32 v142, v221, v141
	v_cvt_f32_f16_sdwa v145, v164 dst_sel:DWORD dst_unused:UNUSED_PAD src0_sel:WORD_1
	v_cvt_f32_f16_e32 v144, v164
	v_cvt_f32_f16_sdwa v146, v166 dst_sel:DWORD dst_unused:UNUSED_PAD src0_sel:WORD_1
	v_cvt_f32_f16_e32 v147, v166
	s_waitcnt lgkmcnt(0)
	v_add_f32_e32 v141, v141, v142
	ds_bpermute_b32 v142, v237, v140
	v_cvt_f32_f16_sdwa v164, v167 dst_sel:DWORD dst_unused:UNUSED_PAD src0_sel:WORD_1
	v_sub_f32_e32 v144, v144, v222
	v_sub_f32_e32 v145, v145, v222
	v_pk_mul_f32 v[144:145], v[222:223], v[144:145] op_sel:[1,0]
	s_waitcnt lgkmcnt(0)
	v_add_f32_e32 v142, v140, v142
	ds_bpermute_b32 v140, v237, v141
	v_pk_fma_f32 v[124:125], v[144:145], v[92:93], v[124:125]
	v_sub_f32_e32 v144, v147, v222
	v_sub_f32_e32 v145, v146, v222
	v_pk_mul_f32 v[144:145], v[222:223], v[144:145] op_sel:[1,0]
	s_waitcnt lgkmcnt(0)
	v_add_f32_e32 v143, v141, v140
	v_cvt_f32_f16_sdwa v141, v165 dst_sel:DWORD dst_unused:UNUSED_PAD src0_sel:WORD_1
	v_cvt_f32_f16_e32 v140, v165
	v_cvt_f32_f16_e32 v165, v167
	ds_read_b128 v[132:135], v236
	ds_read_b128 v[128:131], v236 offset:1152
	v_sub_f32_e32 v141, v141, v222
	v_sub_f32_e32 v140, v140, v222
	v_pk_mul_f32 v[140:141], v[222:223], v[140:141] op_sel:[1,0]
	v_pk_add_f32 v[118:119], v[118:119], v[198:199]
	v_pk_fma_f32 v[126:127], v[140:141], v[94:95], v[126:127]
	v_sub_f32_e32 v140, v165, v222
	v_sub_f32_e32 v141, v164, v222
	v_pk_mul_f32 v[140:141], v[222:223], v[140:141] op_sel:[1,0]
	v_pk_add_f32 v[116:117], v[116:117], v[200:201]
	v_pk_fma_f32 v[140:141], v[140:141], v[90:91], v[122:123]
	v_pk_fma_f32 v[122:123], v[144:145], v[88:89], v[120:121]
	v_cvt_f16_f32_e32 v144, v124
	v_cvt_f16_f32_e32 v145, v125
	v_cvt_pk_f16_f32 v120, v124, v125
	v_cvt_f16_f32_e32 v124, v126
	v_cvt_f16_f32_e32 v125, v127
	v_cvt_pk_f16_f32 v121, v126, v127
	v_cvt_f16_f32_e32 v126, v122
	v_cvt_f16_f32_e32 v127, v123
	v_cvt_f16_f32_e32 v146, v140
	v_cvt_f16_f32_e32 v147, v141
	v_cvt_pk_f16_f32 v122, v122, v123
	v_cvt_pk_f16_f32 v123, v140, v141
	ds_write_b128 v235, v[120:123]
	v_cvt_f32_f16_e32 v120, v144
	v_cvt_f32_f16_e32 v121, v145
	v_cvt_f32_f16_e32 v122, v124
	v_cvt_f32_f16_e32 v123, v125
	v_cvt_f32_f16_e32 v125, v126
	v_cvt_f32_f16_e32 v127, v127
	v_cvt_f32_f16_e32 v140, v146
	v_cvt_f32_f16_e32 v141, v147
	v_add_f32_e32 v120, v120, v121
	v_add_f32_e32 v122, v122, v123
	v_add_f32_e32 v120, v120, v122
	v_add_f32_e32 v122, v125, v127
	v_add_f32_e32 v125, v140, v141
	v_add_f32_e32 v122, v122, v125
	v_add_f32_e32 v120, v120, v122
	v_add_f32_e32 v125, 0, v120
	v_mul_f32_e32 v120, v121, v121
	v_mul_f32_e32 v121, v123, v123
	v_fma_mix_f32 v120, v144, v144, v120 op_sel_hi:[1,1,0]
	v_fma_mix_f32 v121, v124, v124, v121 op_sel_hi:[1,1,0]
	v_mul_f32_e32 v122, v141, v141
	v_add_f32_e32 v120, v120, v121
	v_mul_f32_e32 v121, v127, v127
	v_fma_mix_f32 v121, v126, v126, v121 op_sel_hi:[1,1,0]
	v_fma_mix_f32 v122, v146, v146, v122 op_sel_hi:[1,1,0]
	v_cvt_f32_f16_sdwa v123, v160 dst_sel:DWORD dst_unused:UNUSED_PAD src0_sel:WORD_1
	v_add_f32_e32 v121, v121, v122
	v_add_f32_e32 v124, v120, v121
	v_cvt_f32_f16_e32 v122, v160
	v_cvt_f32_f16_sdwa v121, v161 dst_sel:DWORD dst_unused:UNUSED_PAD src0_sel:WORD_1
	v_cvt_f32_f16_e32 v120, v161
	v_cvt_f32_f16_sdwa v126, v162 dst_sel:DWORD dst_unused:UNUSED_PAD src0_sel:WORD_1
	v_cvt_f32_f16_e32 v127, v162
	v_cvt_f32_f16_sdwa v140, v163 dst_sel:DWORD dst_unused:UNUSED_PAD src0_sel:WORD_1
	v_cvt_f32_f16_e32 v141, v163
	v_sub_f32_e32 v120, v120, v222
	v_sub_f32_e32 v121, v121, v222
	v_sub_f32_e32 v122, v122, v222
	v_sub_f32_e32 v123, v123, v222
	v_pk_mul_f32 v[122:123], v[222:223], v[122:123] op_sel:[1,0]
	v_pk_mul_f32 v[120:121], v[222:223], v[120:121] op_sel:[1,0]
	v_pk_fma_f32 v[116:117], v[122:123], v[80:81], v[116:117]
	v_pk_fma_f32 v[118:119], v[120:121], v[82:83], v[118:119]
	v_sub_f32_e32 v120, v141, v222
	v_sub_f32_e32 v121, v140, v222
	v_sub_f32_e32 v122, v127, v222
	v_sub_f32_e32 v123, v126, v222
	v_pk_add_f32 v[114:115], v[114:115], v[192:193]
	v_pk_add_f32 v[112:113], v[112:113], v[194:195]
	v_pk_mul_f32 v[122:123], v[222:223], v[122:123] op_sel:[1,0]
	v_pk_mul_f32 v[120:121], v[222:223], v[120:121] op_sel:[1,0]
	s_ashr_i32 s39, s38, 31
	v_pk_fma_f32 v[120:121], v[120:121], v[74:75], v[114:115]
	v_pk_fma_f32 v[114:115], v[122:123], v[72:73], v[112:113]
	v_cvt_f16_f32_e32 v122, v116
	v_cvt_f16_f32_e32 v123, v117
	v_cvt_pk_f16_f32 v112, v116, v117
	v_cvt_f16_f32_e32 v116, v118
	v_cvt_f16_f32_e32 v117, v119
	v_cvt_pk_f16_f32 v113, v118, v119
	v_cvt_f16_f32_e32 v118, v114
	v_cvt_f16_f32_e32 v119, v115
	v_cvt_f16_f32_e32 v126, v120
	v_cvt_f16_f32_e32 v127, v121
	v_cvt_pk_f16_f32 v114, v114, v115
	v_cvt_pk_f16_f32 v115, v120, v121
	ds_write_b128 v235, v[112:115] offset:64
	v_cvt_f32_f16_e32 v112, v122
	v_cvt_f32_f16_e32 v113, v123
	v_cvt_f32_f16_e32 v114, v116
	v_cvt_f32_f16_e32 v115, v117
	v_cvt_f32_f16_e32 v117, v118
	v_cvt_f32_f16_e32 v119, v119
	v_cvt_f32_f16_e32 v120, v126
	v_cvt_f32_f16_e32 v121, v127
	v_add_f32_e32 v112, v112, v113
	v_add_f32_e32 v114, v114, v115
	v_add_f32_e32 v112, v112, v114
	v_add_f32_e32 v114, v117, v119
	v_add_f32_e32 v117, v120, v121
	v_add_f32_e32 v114, v114, v117
	v_add_f32_e32 v112, v112, v114
	v_mul_f32_e32 v113, v113, v113
	v_mul_f32_e32 v114, v115, v115
	v_fma_mix_f32 v113, v122, v122, v113 op_sel_hi:[1,1,0]
	v_fma_mix_f32 v114, v116, v116, v114 op_sel_hi:[1,1,0]
	v_mul_f32_e32 v115, v121, v121
	v_add_f32_e32 v113, v113, v114
	v_mul_f32_e32 v114, v119, v119
	v_fma_mix_f32 v114, v118, v118, v114 op_sel_hi:[1,1,0]
	v_fma_mix_f32 v115, v126, v126, v115 op_sel_hi:[1,1,0]
	v_add_f32_e32 v112, v125, v112
	v_add_f32_e32 v114, v114, v115
	v_add_f32_e32 v113, v113, v114
	ds_bpermute_b32 v114, v221, v112
	v_add_f32_e32 v113, v124, v113
	ds_read_b128 v[160:163], v236
	ds_read_b128 v[164:167], v236 offset:1152
	s_waitcnt lgkmcnt(2)
	v_add_f32_e32 v112, v112, v114
	ds_bpermute_b32 v114, v221, v113
	s_waitcnt lgkmcnt(0)
	v_add_f32_e32 v113, v113, v114
	ds_bpermute_b32 v114, v237, v112
	s_waitcnt lgkmcnt(0)
	v_add_f32_e32 v146, v112, v114
	ds_bpermute_b32 v112, v237, v113
	s_waitcnt lgkmcnt(0)
	v_add_f32_e32 v147, v113, v112
	v_mov_b64_e32 v[112:113], s[28:29]
	v_mad_i64_i32 v[112:113], s[40:41], v220, s73, v[112:113]
	v_lshl_add_u64 v[140:141], s[38:39], 3, v[112:113]
	v_add_co_u32_e32 v112, vcc, s74, v214
	v_lshl_or_b32 v144, v238, 1, v230
	s_nop 0
	v_addc_co_u32_e32 v113, vcc, 0, v215, vcc
	global_load_dwordx4 v[124:127], v[112:113], off nt
	global_load_dwordx4 v[120:123], v[112:113], off offset:64 nt
	v_add_co_u32_e32 v112, vcc, s75, v214
	v_lshl_add_u64 v[140:141], v[140:141], 0, s[34:35]
	s_nop 0
	v_addc_co_u32_e32 v113, vcc, 0, v215, vcc
	global_load_dwordx4 v[116:119], v[112:113], off nt
	s_nop 0
	global_load_dwordx4 v[112:115], v[112:113], off offset:64 nt
	s_nop 0
	buffer_store_dwordx4 v[132:135], v144, s[24:27], 0 offen nt
	s_nop 1
	v_add_u32_e32 v132, 0x3000, v144
	buffer_store_dwordx4 v[128:131], v132, s[24:27], 0 offen nt
	global_store_dwordx2 v[140:141], v[142:143], off
	s_nop 0
	v_add_u32_e32 v128, 0x6000, v144
	buffer_store_dwordx4 v[160:163], v128, s[24:27], 0 offen nt
	v_add_u32_e32 v128, 0x9000, v144
	buffer_store_dwordx4 v[164:167], v128, s[24:27], 0 offen nt
	global_store_dwordx2 v[140:141], v[146:147], off offset:1536
	v_cvt_f32_f16_sdwa v131, v156 dst_sel:DWORD dst_unused:UNUSED_PAD src0_sel:WORD_1
	v_cvt_f32_f16_e32 v130, v156
	v_cvt_f32_f16_sdwa v129, v157 dst_sel:DWORD dst_unused:UNUSED_PAD src0_sel:WORD_1
	v_cvt_f32_f16_e32 v128, v157
	v_cvt_f32_f16_sdwa v132, v158 dst_sel:DWORD dst_unused:UNUSED_PAD src0_sel:WORD_1
	v_cvt_f32_f16_e32 v133, v158
	v_cvt_f32_f16_sdwa v134, v159 dst_sel:DWORD dst_unused:UNUSED_PAD src0_sel:WORD_1
	v_cvt_f32_f16_e32 v135, v159
	v_sub_f32_e32 v128, v128, v218
	v_sub_f32_e32 v129, v129, v218
	v_sub_f32_e32 v130, v130, v218
	v_sub_f32_e32 v131, v131, v218
	v_pk_add_f32 v[110:111], v[110:111], v[206:207]
	v_pk_add_f32 v[108:109], v[108:109], v[208:209]
	v_pk_mul_f32 v[130:131], v[218:219], v[130:131] op_sel:[1,0]
	v_pk_mul_f32 v[128:129], v[218:219], v[128:129] op_sel:[1,0]
	v_pk_fma_f32 v[108:109], v[130:131], v[92:93], v[108:109]
	v_pk_fma_f32 v[110:111], v[128:129], v[94:95], v[110:111]
	v_sub_f32_e32 v128, v135, v218
	v_sub_f32_e32 v129, v134, v218
	v_sub_f32_e32 v130, v133, v218
	v_sub_f32_e32 v131, v132, v218
	v_pk_add_f32 v[106:107], v[106:107], v[202:203]
	v_pk_add_f32 v[104:105], v[104:105], v[204:205]
	v_pk_mul_f32 v[130:131], v[218:219], v[130:131] op_sel:[1,0]
	v_pk_mul_f32 v[128:129], v[218:219], v[128:129] op_sel:[1,0]
	v_pk_add_f32 v[102:103], v[102:103], v[198:199]
	v_pk_fma_f32 v[128:129], v[128:129], v[90:91], v[106:107]
	v_pk_fma_f32 v[106:107], v[130:131], v[88:89], v[104:105]
	v_cvt_f16_f32_e32 v130, v108
	v_cvt_f16_f32_e32 v131, v109
	v_cvt_pk_f16_f32 v104, v108, v109
	v_cvt_f16_f32_e32 v108, v110
	v_cvt_f16_f32_e32 v109, v111
	v_cvt_pk_f16_f32 v105, v110, v111
	v_cvt_f16_f32_e32 v110, v106
	v_cvt_f16_f32_e32 v111, v107
	v_cvt_f16_f32_e32 v132, v128
	v_cvt_f16_f32_e32 v133, v129
	v_cvt_pk_f16_f32 v106, v106, v107
	v_cvt_pk_f16_f32 v107, v128, v129
	ds_write_b128 v235, v[104:107]
	v_cvt_f32_f16_e32 v104, v130
	v_cvt_f32_f16_e32 v105, v131
	v_cvt_f32_f16_e32 v106, v108
	v_cvt_f32_f16_e32 v107, v109
	v_cvt_f32_f16_e32 v109, v110
	v_cvt_f32_f16_e32 v111, v111
	v_cvt_f32_f16_e32 v128, v132
	v_cvt_f32_f16_e32 v129, v133
	v_add_f32_e32 v104, v104, v105
	v_add_f32_e32 v106, v106, v107
	v_add_f32_e32 v104, v104, v106
	v_add_f32_e32 v106, v109, v111
	v_add_f32_e32 v109, v128, v129
	v_add_f32_e32 v106, v106, v109
	v_add_f32_e32 v104, v104, v106
	v_add_f32_e32 v109, 0, v104
	v_mul_f32_e32 v104, v105, v105
	v_mul_f32_e32 v105, v107, v107
	v_fma_mix_f32 v104, v130, v130, v104 op_sel_hi:[1,1,0]
	v_fma_mix_f32 v105, v108, v108, v105 op_sel_hi:[1,1,0]
	v_mul_f32_e32 v106, v129, v129
	v_add_f32_e32 v104, v104, v105
	v_mul_f32_e32 v105, v111, v111
	v_fma_mix_f32 v105, v110, v110, v105 op_sel_hi:[1,1,0]
	v_fma_mix_f32 v106, v132, v132, v106 op_sel_hi:[1,1,0]
	v_cvt_f32_f16_sdwa v107, v152 dst_sel:DWORD dst_unused:UNUSED_PAD src0_sel:WORD_1
	v_add_f32_e32 v105, v105, v106
	v_add_f32_e32 v108, v104, v105
	v_cvt_f32_f16_e32 v106, v152
	v_cvt_f32_f16_sdwa v105, v153 dst_sel:DWORD dst_unused:UNUSED_PAD src0_sel:WORD_1
	v_cvt_f32_f16_e32 v104, v153
	v_cvt_f32_f16_sdwa v110, v154 dst_sel:DWORD dst_unused:UNUSED_PAD src0_sel:WORD_1
	v_cvt_f32_f16_e32 v111, v154
	v_cvt_f32_f16_sdwa v128, v155 dst_sel:DWORD dst_unused:UNUSED_PAD src0_sel:WORD_1
	v_cvt_f32_f16_e32 v129, v155
	v_sub_f32_e32 v104, v104, v218
	v_sub_f32_e32 v105, v105, v218
	v_sub_f32_e32 v106, v106, v218
	v_sub_f32_e32 v107, v107, v218
	v_pk_add_f32 v[100:101], v[100:101], v[200:201]
	v_pk_mul_f32 v[106:107], v[218:219], v[106:107] op_sel:[1,0]
	v_pk_mul_f32 v[104:105], v[218:219], v[104:105] op_sel:[1,0]
	v_pk_fma_f32 v[100:101], v[106:107], v[80:81], v[100:101]
	v_pk_fma_f32 v[102:103], v[104:105], v[82:83], v[102:103]
	v_sub_f32_e32 v104, v129, v218
	v_sub_f32_e32 v105, v128, v218
	v_sub_f32_e32 v106, v111, v218
	v_sub_f32_e32 v107, v110, v218
	v_pk_add_f32 v[98:99], v[98:99], v[192:193]
	v_pk_add_f32 v[96:97], v[96:97], v[194:195]
	v_pk_mul_f32 v[106:107], v[218:219], v[106:107] op_sel:[1,0]
	v_pk_mul_f32 v[104:105], v[218:219], v[104:105] op_sel:[1,0]
	v_pk_add_f32 v[86:87], v[86:87], v[206:207]
	v_pk_fma_f32 v[104:105], v[104:105], v[74:75], v[98:99]
	v_pk_fma_f32 v[98:99], v[106:107], v[72:73], v[96:97]
	v_cvt_f16_f32_e32 v106, v100
	v_cvt_f16_f32_e32 v107, v101
	v_cvt_pk_f16_f32 v96, v100, v101
	v_cvt_f16_f32_e32 v100, v102
	v_cvt_f16_f32_e32 v101, v103
	v_cvt_pk_f16_f32 v97, v102, v103
	v_cvt_f16_f32_e32 v103, v99
	v_cvt_f16_f32_e32 v111, v105
	v_cvt_f16_f32_e32 v102, v98
	v_cvt_f16_f32_e32 v110, v104
	v_cvt_pk_f16_f32 v98, v98, v99
	v_cvt_pk_f16_f32 v99, v104, v105
	v_cvt_f32_f16_e32 v105, v107
	v_cvt_f32_f16_e32 v107, v100
	v_cvt_f32_f16_e32 v101, v101
	v_cvt_f32_f16_e32 v103, v103
	v_cvt_f32_f16_e32 v104, v106
	v_cvt_f32_f16_e32 v111, v111
	v_cvt_f32_f16_e32 v128, v102
	v_cvt_f32_f16_e32 v129, v110
	v_add_f32_e32 v107, v107, v101
	v_mul_f32_e32 v101, v101, v101
	v_fma_mix_f32 v100, v100, v100, v101 op_sel_hi:[1,1,0]
	v_mul_f32_e32 v101, v103, v103
	v_add_f32_e32 v104, v104, v105
	v_mul_f32_e32 v105, v105, v105
	v_fma_mix_f32 v101, v102, v102, v101 op_sel_hi:[1,1,0]
	v_mul_f32_e32 v102, v111, v111
	v_add_f32_e32 v104, v104, v107
	v_add_f32_e32 v107, v128, v103
	v_add_f32_e32 v128, v129, v111
	v_fma_mix_f32 v105, v106, v106, v105 op_sel_hi:[1,1,0]
	v_fma_mix_f32 v102, v110, v110, v102 op_sel_hi:[1,1,0]
	v_add_f32_e32 v107, v107, v128
	v_add_f32_e32 v100, v105, v100
	v_add_f32_e32 v101, v101, v102
	v_add_f32_e32 v104, v104, v107
	v_add_f32_e32 v100, v100, v101
	v_add_f32_e32 v104, v109, v104
	v_add_f32_e32 v105, v108, v100
	ds_bpermute_b32 v106, v221, v104
	ds_bpermute_b32 v107, v221, v105
	v_cvt_f32_f16_sdwa v108, v150 dst_sel:DWORD dst_unused:UNUSED_PAD src0_sel:WORD_1
	v_cvt_f32_f16_e32 v109, v150
	v_cvt_f32_f16_sdwa v110, v151 dst_sel:DWORD dst_unused:UNUSED_PAD src0_sel:WORD_1
	s_waitcnt lgkmcnt(1)
	v_add_f32_e32 v128, v104, v106
	s_waitcnt lgkmcnt(0)
	v_add_f32_e32 v129, v105, v107
	v_cvt_f32_f16_sdwa v107, v148 dst_sel:DWORD dst_unused:UNUSED_PAD src0_sel:WORD_1
	v_cvt_f32_f16_e32 v106, v148
	v_cvt_f32_f16_sdwa v105, v149 dst_sel:DWORD dst_unused:UNUSED_PAD src0_sel:WORD_1
	v_cvt_f32_f16_e32 v104, v149
	v_cvt_f32_f16_e32 v111, v151
	v_sub_f32_e32 v106, v106, v216
	v_sub_f32_e32 v105, v105, v216
	v_sub_f32_e32 v104, v104, v216
	v_sub_f32_e32 v107, v107, v216
	v_pk_add_f32 v[84:85], v[84:85], v[208:209]
	v_pk_mul_f32 v[106:107], v[216:217], v[106:107] op_sel:[1,0]
	v_pk_mul_f32 v[104:105], v[216:217], v[104:105] op_sel:[1,0]
	v_pk_fma_f32 v[84:85], v[106:107], v[92:93], v[84:85]
	v_pk_fma_f32 v[86:87], v[104:105], v[94:95], v[86:87]
	v_sub_f32_e32 v104, v111, v216
	v_sub_f32_e32 v105, v110, v216
	v_sub_f32_e32 v106, v109, v216
	v_sub_f32_e32 v107, v108, v216
	v_pk_add_f32 v[78:79], v[78:79], v[202:203]
	v_pk_add_f32 v[76:77], v[76:77], v[204:205]
	v_pk_mul_f32 v[106:107], v[216:217], v[106:107] op_sel:[1,0]
	v_pk_mul_f32 v[104:105], v[216:217], v[104:105] op_sel:[1,0]
	ds_write_b128 v235, v[96:99] offset:64
	v_pk_fma_f32 v[104:105], v[104:105], v[90:91], v[78:79]
	v_pk_fma_f32 v[78:79], v[106:107], v[88:89], v[76:77]
	v_cvt_f16_f32_e32 v106, v84
	v_cvt_f16_f32_e32 v107, v85
	v_cvt_pk_f16_f32 v76, v84, v85
	v_cvt_f16_f32_e32 v84, v86
	v_cvt_f16_f32_e32 v85, v87
	v_cvt_pk_f16_f32 v77, v86, v87
	v_cvt_f16_f32_e32 v86, v78
	v_cvt_f16_f32_e32 v87, v79
	v_cvt_f16_f32_e32 v108, v104
	v_cvt_f16_f32_e32 v109, v105
	v_cvt_pk_f16_f32 v78, v78, v79
	v_cvt_pk_f16_f32 v79, v104, v105
	ds_read_b128 v[96:99], v236
	ds_read_b128 v[100:103], v236 offset:1152
	ds_write_b128 v235, v[76:79]
	v_cvt_f32_f16_e32 v76, v106
	v_cvt_f32_f16_e32 v77, v107
	v_cvt_f32_f16_e32 v78, v84
	v_cvt_f32_f16_e32 v79, v85
	v_cvt_f32_f16_e32 v85, v86
	v_cvt_f32_f16_e32 v87, v87
	v_cvt_f32_f16_e32 v104, v108
	v_cvt_f32_f16_e32 v105, v109
	v_add_f32_e32 v76, v76, v77
	v_add_f32_e32 v78, v78, v79
	v_add_f32_e32 v76, v76, v78
	v_add_f32_e32 v78, v85, v87
	v_add_f32_e32 v85, v104, v105
	v_add_f32_e32 v78, v78, v85
	v_add_f32_e32 v76, v76, v78
	v_add_f32_e32 v85, 0, v76
	v_mul_f32_e32 v76, v77, v77
	v_mul_f32_e32 v77, v79, v79
	v_fma_mix_f32 v76, v106, v106, v76 op_sel_hi:[1,1,0]
	v_fma_mix_f32 v77, v84, v84, v77 op_sel_hi:[1,1,0]
	v_mul_f32_e32 v78, v105, v105
	v_add_f32_e32 v76, v76, v77
	v_mul_f32_e32 v77, v87, v87
	v_fma_mix_f32 v77, v86, v86, v77 op_sel_hi:[1,1,0]
	v_fma_mix_f32 v78, v108, v108, v78 op_sel_hi:[1,1,0]
	v_cvt_f32_f16_sdwa v79, v136 dst_sel:DWORD dst_unused:UNUSED_PAD src0_sel:WORD_1
	v_add_f32_e32 v77, v77, v78
	v_add_f32_e32 v84, v76, v77
	v_cvt_f32_f16_e32 v78, v136
	v_cvt_f32_f16_sdwa v77, v137 dst_sel:DWORD dst_unused:UNUSED_PAD src0_sel:WORD_1
	v_cvt_f32_f16_e32 v76, v137
	v_cvt_f32_f16_sdwa v86, v138 dst_sel:DWORD dst_unused:UNUSED_PAD src0_sel:WORD_1
	v_cvt_f32_f16_e32 v87, v138
	v_cvt_f32_f16_sdwa v104, v139 dst_sel:DWORD dst_unused:UNUSED_PAD src0_sel:WORD_1
	v_cvt_f32_f16_e32 v105, v139
	v_sub_f32_e32 v76, v76, v216
	v_sub_f32_e32 v77, v77, v216
	v_sub_f32_e32 v78, v78, v216
	v_sub_f32_e32 v79, v79, v216
	v_pk_add_f32 v[70:71], v[70:71], v[198:199]
	v_pk_add_f32 v[68:69], v[68:69], v[200:201]
	v_pk_mul_f32 v[78:79], v[216:217], v[78:79] op_sel:[1,0]
	v_pk_mul_f32 v[76:77], v[216:217], v[76:77] op_sel:[1,0]
	v_pk_fma_f32 v[68:69], v[78:79], v[80:81], v[68:69]
	v_pk_fma_f32 v[70:71], v[76:77], v[82:83], v[70:71]
	v_sub_f32_e32 v76, v105, v216
	v_sub_f32_e32 v77, v104, v216
	v_sub_f32_e32 v78, v87, v216
	v_sub_f32_e32 v79, v86, v216
	v_pk_add_f32 v[66:67], v[66:67], v[192:193]
	v_pk_add_f32 v[64:65], v[64:65], v[194:195]
	v_pk_mul_f32 v[78:79], v[216:217], v[78:79] op_sel:[1,0]
	v_pk_mul_f32 v[76:77], v[216:217], v[76:77] op_sel:[1,0]
	ds_bpermute_b32 v130, v237, v128
	v_pk_fma_f32 v[76:77], v[76:77], v[74:75], v[66:67]
	v_pk_fma_f32 v[66:67], v[78:79], v[72:73], v[64:65]
	v_cvt_f16_f32_e32 v78, v68
	v_cvt_f16_f32_e32 v79, v69
	v_cvt_pk_f16_f32 v64, v68, v69
	v_cvt_f16_f32_e32 v68, v70
	v_cvt_f16_f32_e32 v69, v71
	v_cvt_pk_f16_f32 v65, v70, v71
	v_cvt_f16_f32_e32 v71, v67
	v_cvt_f16_f32_e32 v87, v77
	v_cvt_f16_f32_e32 v70, v66
	v_cvt_f16_f32_e32 v86, v76
	v_cvt_f32_f16_e32 v105, v68
	v_cvt_f32_f16_e32 v69, v69
	v_cvt_f32_f16_e32 v71, v71
	v_cvt_f32_f16_e32 v104, v78
	v_cvt_f32_f16_e32 v79, v79
	v_cvt_f32_f16_e32 v87, v87
	v_cvt_f32_f16_e32 v106, v70
	v_cvt_f32_f16_e32 v107, v86
	v_add_f32_e32 v105, v105, v69
	v_mul_f32_e32 v69, v69, v69
	v_fma_mix_f32 v68, v68, v68, v69 op_sel_hi:[1,1,0]
	v_mul_f32_e32 v69, v71, v71
	v_add_f32_e32 v104, v104, v79
	v_mul_f32_e32 v79, v79, v79
	v_fma_mix_f32 v69, v70, v70, v69 op_sel_hi:[1,1,0]
	v_mul_f32_e32 v70, v87, v87
	v_add_f32_e32 v104, v104, v105
	v_add_f32_e32 v105, v106, v71
	v_add_f32_e32 v106, v107, v87
	v_fma_mix_f32 v78, v78, v78, v79 op_sel_hi:[1,1,0]
	v_fma_mix_f32 v70, v86, v86, v70 op_sel_hi:[1,1,0]
	v_add_f32_e32 v105, v105, v106
	v_add_f32_e32 v68, v78, v68
	v_add_f32_e32 v69, v69, v70
	v_add_f32_e32 v104, v104, v105
	v_add_f32_e32 v68, v68, v69
	v_add_f32_e32 v85, v85, v104
	v_add_f32_e32 v68, v84, v68
	ds_bpermute_b32 v69, v221, v85
	ds_bpermute_b32 v70, v221, v68
	v_cvt_pk_f16_f32 v66, v66, v67
	v_cvt_pk_f16_f32 v67, v76, v77
	ds_write_b128 v235, v[64:67] offset:64
	s_waitcnt lgkmcnt(2)
	v_add_f32_e32 v64, v85, v69
	s_waitcnt lgkmcnt(1)
	v_add_f32_e32 v65, v68, v70
	ds_bpermute_b32 v131, v237, v129
	ds_bpermute_b32 v66, v237, v64
	ds_bpermute_b32 v67, v237, v65
	ds_read_b128 v[104:107], v236
	ds_read_b128 v[108:111], v236 offset:1152
	v_add_f32_e32 v128, v128, v130
	s_waitcnt lgkmcnt(4)
	v_add_f32_e32 v129, v129, v131
	s_waitcnt lgkmcnt(3)
	v_add_f32_e32 v130, v64, v66
	s_waitcnt lgkmcnt(2)
	v_add_f32_e32 v131, v65, v67
	v_add_co_u32_e32 v64, vcc, s77, v214
	s_nop 1
	v_addc_co_u32_e32 v65, vcc, 0, v215, vcc
	global_load_dwordx4 v[84:87], v[64:65], off nt
	global_load_dwordx4 v[76:79], v[64:65], off offset:64 nt
	v_add_co_u32_e32 v64, vcc, s78, v214
	s_nop 1
	v_addc_co_u32_e32 v65, vcc, 0, v215, vcc
	global_load_dwordx4 v[68:71], v[64:65], off nt
	s_nop 0
	global_load_dwordx4 v[64:67], v[64:65], off offset:64 nt
	v_add_u32_e32 v132, 0xc000, v144
	buffer_store_dwordx4 v[96:99], v132, s[24:27], 0 offen nt
	s_nop 1
	v_add_u32_e32 v96, 0xf000, v144
	buffer_store_dwordx4 v[100:103], v96, s[24:27], 0 offen nt
	v_add_u32_e32 v96, 0x12000, v144
	global_store_dwordx2 v[140:141], v[128:129], off offset:3072
	s_waitcnt lgkmcnt(1)
	buffer_store_dwordx4 v[104:107], v96, s[24:27], 0 offen nt
	v_add_u32_e32 v96, 0x15000, v144
	s_waitcnt lgkmcnt(0)
	buffer_store_dwordx4 v[108:111], v96, s[24:27], 0 offen nt
	v_add_co_u32_e32 v96, vcc, s79, v140
	s_nop 1
	v_addc_co_u32_e32 v97, vcc, 0, v141, vcc
	global_store_dwordx2 v[96:97], v[130:131], off offset:512
	s_waitcnt vmcnt(19)
	v_cvt_f32_f16_sdwa v99, v124 dst_sel:DWORD dst_unused:UNUSED_PAD src0_sel:WORD_1
	v_cvt_f32_f16_e32 v98, v124
	v_cvt_f32_f16_sdwa v97, v125 dst_sel:DWORD dst_unused:UNUSED_PAD src0_sel:WORD_1
	v_cvt_f32_f16_e32 v96, v125
	v_cvt_f32_f16_sdwa v100, v126 dst_sel:DWORD dst_unused:UNUSED_PAD src0_sel:WORD_1
	v_cvt_f32_f16_e32 v101, v126
	v_cvt_f32_f16_sdwa v102, v127 dst_sel:DWORD dst_unused:UNUSED_PAD src0_sel:WORD_1
	v_cvt_f32_f16_e32 v103, v127
	v_sub_f32_e32 v96, v96, v212
	v_sub_f32_e32 v97, v97, v212
	v_sub_f32_e32 v98, v98, v212
	v_sub_f32_e32 v99, v99, v212
	v_pk_add_f32 v[62:63], v[62:63], v[206:207]
	v_pk_add_f32 v[60:61], v[60:61], v[208:209]
	v_pk_mul_f32 v[98:99], v[212:213], v[98:99] op_sel:[1,0]
	v_pk_mul_f32 v[96:97], v[212:213], v[96:97] op_sel:[1,0]
	v_pk_fma_f32 v[60:61], v[92:93], v[98:99], v[60:61]
	v_pk_fma_f32 v[62:63], v[94:95], v[96:97], v[62:63]
	v_sub_f32_e32 v96, v103, v212
	v_sub_f32_e32 v97, v102, v212
	v_sub_f32_e32 v98, v101, v212
	v_sub_f32_e32 v99, v100, v212
	v_pk_add_f32 v[58:59], v[58:59], v[202:203]
	v_pk_add_f32 v[56:57], v[56:57], v[204:205]
	v_pk_mul_f32 v[98:99], v[212:213], v[98:99] op_sel:[1,0]
	v_pk_mul_f32 v[96:97], v[212:213], v[96:97] op_sel:[1,0]
	v_pk_add_f32 v[54:55], v[54:55], v[198:199]
	v_pk_fma_f32 v[96:97], v[90:91], v[96:97], v[58:59]
	v_pk_fma_f32 v[58:59], v[88:89], v[98:99], v[56:57]
	v_cvt_f16_f32_e32 v98, v60
	v_cvt_f16_f32_e32 v99, v61
	v_cvt_pk_f16_f32 v56, v60, v61
	v_cvt_f16_f32_e32 v60, v62
	v_cvt_f16_f32_e32 v61, v63
	v_cvt_pk_f16_f32 v57, v62, v63
	v_cvt_f16_f32_e32 v62, v58
	v_cvt_f16_f32_e32 v63, v59
	v_cvt_f16_f32_e32 v100, v96
	v_cvt_f16_f32_e32 v101, v97
	v_cvt_pk_f16_f32 v58, v58, v59
	v_cvt_pk_f16_f32 v59, v96, v97
	ds_write_b128 v235, v[56:59]
	v_cvt_f32_f16_e32 v56, v98
	v_cvt_f32_f16_e32 v57, v99
	v_cvt_f32_f16_e32 v58, v60
	v_cvt_f32_f16_e32 v59, v61
	v_cvt_f32_f16_e32 v61, v62
	v_cvt_f32_f16_e32 v63, v63
	v_cvt_f32_f16_e32 v96, v100
	v_cvt_f32_f16_e32 v97, v101
	v_add_f32_e32 v56, v56, v57
	v_add_f32_e32 v58, v58, v59
	v_add_f32_e32 v56, v56, v58
	v_add_f32_e32 v58, v61, v63
	v_add_f32_e32 v61, v96, v97
	v_add_f32_e32 v58, v58, v61
	v_add_f32_e32 v56, v56, v58
	v_add_f32_e32 v61, 0, v56
	v_mul_f32_e32 v56, v57, v57
	v_mul_f32_e32 v57, v59, v59
	v_fma_mix_f32 v56, v98, v98, v56 op_sel_hi:[1,1,0]
	v_fma_mix_f32 v57, v60, v60, v57 op_sel_hi:[1,1,0]
	v_mul_f32_e32 v58, v97, v97
	v_add_f32_e32 v56, v56, v57
	v_mul_f32_e32 v57, v63, v63
	v_fma_mix_f32 v57, v62, v62, v57 op_sel_hi:[1,1,0]
	v_fma_mix_f32 v58, v100, v100, v58 op_sel_hi:[1,1,0]
	s_waitcnt vmcnt(18)
	v_cvt_f32_f16_sdwa v59, v120 dst_sel:DWORD dst_unused:UNUSED_PAD src0_sel:WORD_1
	v_add_f32_e32 v57, v57, v58
	v_add_f32_e32 v60, v56, v57
	v_cvt_f32_f16_e32 v58, v120
	v_cvt_f32_f16_sdwa v57, v121 dst_sel:DWORD dst_unused:UNUSED_PAD src0_sel:WORD_1
	v_cvt_f32_f16_e32 v56, v121
	v_cvt_f32_f16_sdwa v62, v122 dst_sel:DWORD dst_unused:UNUSED_PAD src0_sel:WORD_1
	v_cvt_f32_f16_e32 v63, v122
	v_cvt_f32_f16_sdwa v96, v123 dst_sel:DWORD dst_unused:UNUSED_PAD src0_sel:WORD_1
	v_cvt_f32_f16_e32 v97, v123
	v_sub_f32_e32 v56, v56, v212
	v_sub_f32_e32 v57, v57, v212
	v_sub_f32_e32 v58, v58, v212
	v_sub_f32_e32 v59, v59, v212
	v_pk_add_f32 v[52:53], v[52:53], v[200:201]
	v_pk_mul_f32 v[58:59], v[212:213], v[58:59] op_sel:[1,0]
	v_pk_mul_f32 v[56:57], v[212:213], v[56:57] op_sel:[1,0]
	v_pk_fma_f32 v[52:53], v[80:81], v[58:59], v[52:53]
	v_pk_fma_f32 v[54:55], v[82:83], v[56:57], v[54:55]
	v_sub_f32_e32 v56, v97, v212
	v_sub_f32_e32 v57, v96, v212
	v_sub_f32_e32 v58, v63, v212
	v_sub_f32_e32 v59, v62, v212
	v_pk_add_f32 v[50:51], v[50:51], v[192:193]
	v_pk_add_f32 v[48:49], v[48:49], v[194:195]
	v_pk_mul_f32 v[58:59], v[212:213], v[58:59] op_sel:[1,0]
	v_pk_mul_f32 v[56:57], v[212:213], v[56:57] op_sel:[1,0]
	s_waitcnt vmcnt(17)
	v_cvt_f32_f16_sdwa v98, v119 dst_sel:DWORD dst_unused:UNUSED_PAD src0_sel:WORD_1
	v_pk_fma_f32 v[56:57], v[74:75], v[56:57], v[50:51]
	v_pk_fma_f32 v[50:51], v[72:73], v[58:59], v[48:49]
	v_cvt_f16_f32_e32 v58, v52
	v_cvt_f16_f32_e32 v59, v53
	v_cvt_pk_f16_f32 v48, v52, v53
	v_cvt_f16_f32_e32 v52, v54
	v_cvt_f16_f32_e32 v53, v55
	v_cvt_pk_f16_f32 v49, v54, v55
	v_cvt_f16_f32_e32 v55, v51
	v_cvt_f16_f32_e32 v63, v57
	v_cvt_f16_f32_e32 v54, v50
	v_cvt_f16_f32_e32 v62, v56
	v_cvt_pk_f16_f32 v50, v50, v51
	v_cvt_pk_f16_f32 v51, v56, v57
	v_cvt_f32_f16_e32 v57, v59
	v_cvt_f32_f16_e32 v59, v52
	v_cvt_f32_f16_e32 v53, v53
	v_cvt_f32_f16_e32 v55, v55
	v_cvt_f32_f16_e32 v56, v58
	v_cvt_f32_f16_e32 v63, v63
	v_cvt_f32_f16_e32 v96, v54
	v_cvt_f32_f16_e32 v97, v62
	v_add_f32_e32 v59, v59, v53
	v_mul_f32_e32 v53, v53, v53
	v_fma_mix_f32 v52, v52, v52, v53 op_sel_hi:[1,1,0]
	v_mul_f32_e32 v53, v55, v55
	v_add_f32_e32 v56, v56, v57
	v_mul_f32_e32 v57, v57, v57
	v_fma_mix_f32 v53, v54, v54, v53 op_sel_hi:[1,1,0]
	v_mul_f32_e32 v54, v63, v63
	v_add_f32_e32 v56, v56, v59
	v_add_f32_e32 v59, v96, v55
	v_add_f32_e32 v96, v97, v63
	v_fma_mix_f32 v57, v58, v58, v57 op_sel_hi:[1,1,0]
	v_fma_mix_f32 v54, v62, v62, v54 op_sel_hi:[1,1,0]
	v_add_f32_e32 v59, v59, v96
	v_add_f32_e32 v52, v57, v52
	v_add_f32_e32 v53, v53, v54
	v_add_f32_e32 v56, v56, v59
	v_add_f32_e32 v52, v52, v53
	v_add_f32_e32 v56, v61, v56
	v_add_f32_e32 v57, v60, v52
	ds_bpermute_b32 v58, v221, v56
	ds_bpermute_b32 v59, v221, v57
	v_cvt_f32_f16_sdwa v96, v118 dst_sel:DWORD dst_unused:UNUSED_PAD src0_sel:WORD_1
	v_cvt_f32_f16_e32 v97, v118
	v_cvt_f32_f16_e32 v99, v119
	s_waitcnt lgkmcnt(1)
	v_add_f32_e32 v60, v56, v58
	s_waitcnt lgkmcnt(0)
	v_add_f32_e32 v61, v57, v59
	v_cvt_f32_f16_sdwa v59, v116 dst_sel:DWORD dst_unused:UNUSED_PAD src0_sel:WORD_1
	v_cvt_f32_f16_e32 v58, v116
	v_cvt_f32_f16_sdwa v57, v117 dst_sel:DWORD dst_unused:UNUSED_PAD src0_sel:WORD_1
	v_cvt_f32_f16_e32 v56, v117
	v_sub_f32_e32 v59, v59, v210
	v_sub_f32_e32 v58, v58, v210
	v_sub_f32_e32 v57, v57, v210
	v_sub_f32_e32 v56, v56, v210
	v_pk_add_f32 v[46:47], v[46:47], v[206:207]
	v_pk_add_f32 v[44:45], v[44:45], v[208:209]
	v_pk_mul_f32 v[58:59], v[210:211], v[58:59] op_sel:[1,0]
	v_pk_mul_f32 v[56:57], v[210:211], v[56:57] op_sel:[1,0]
	v_pk_fma_f32 v[44:45], v[92:93], v[58:59], v[44:45]
	v_pk_fma_f32 v[46:47], v[94:95], v[56:57], v[46:47]
	v_sub_f32_e32 v56, v99, v210
	v_sub_f32_e32 v57, v98, v210
	v_sub_f32_e32 v58, v97, v210
	v_sub_f32_e32 v59, v96, v210
	v_pk_add_f32 v[42:43], v[42:43], v[202:203]
	v_pk_add_f32 v[40:41], v[40:41], v[204:205]
	v_pk_mul_f32 v[58:59], v[210:211], v[58:59] op_sel:[1,0]
	v_pk_mul_f32 v[56:57], v[210:211], v[56:57] op_sel:[1,0]
	ds_write_b128 v235, v[48:51] offset:64
	v_pk_fma_f32 v[56:57], v[90:91], v[56:57], v[42:43]
	v_pk_fma_f32 v[42:43], v[88:89], v[58:59], v[40:41]
	v_cvt_f16_f32_e32 v58, v44
	v_cvt_f16_f32_e32 v59, v45
	v_cvt_pk_f16_f32 v40, v44, v45
	v_cvt_f16_f32_e32 v44, v46
	v_cvt_f16_f32_e32 v45, v47
	v_cvt_pk_f16_f32 v41, v46, v47
	v_cvt_f16_f32_e32 v46, v42
	v_cvt_f16_f32_e32 v47, v43
	v_cvt_f16_f32_e32 v96, v56
	v_cvt_f16_f32_e32 v97, v57
	v_cvt_pk_f16_f32 v42, v42, v43
	v_cvt_pk_f16_f32 v43, v56, v57
	ds_read_b128 v[48:51], v236
	ds_read_b128 v[52:55], v236 offset:1152
	ds_write_b128 v235, v[40:43]
	v_cvt_f32_f16_e32 v40, v58
	v_cvt_f32_f16_e32 v41, v59
	v_cvt_f32_f16_e32 v42, v44
	v_cvt_f32_f16_e32 v43, v45
	v_cvt_f32_f16_e32 v45, v46
	v_cvt_f32_f16_e32 v47, v47
	v_cvt_f32_f16_e32 v56, v96
	v_cvt_f32_f16_e32 v57, v97
	v_add_f32_e32 v40, v40, v41
	v_add_f32_e32 v42, v42, v43
	v_add_f32_e32 v40, v40, v42
	v_add_f32_e32 v42, v45, v47
	v_add_f32_e32 v45, v56, v57
	v_add_f32_e32 v42, v42, v45
	v_add_f32_e32 v40, v40, v42
	v_add_f32_e32 v45, 0, v40
	v_mul_f32_e32 v40, v41, v41
	v_mul_f32_e32 v41, v43, v43
	v_fma_mix_f32 v40, v58, v58, v40 op_sel_hi:[1,1,0]
	v_fma_mix_f32 v41, v44, v44, v41 op_sel_hi:[1,1,0]
	v_mul_f32_e32 v42, v57, v57
	v_add_f32_e32 v40, v40, v41
	v_mul_f32_e32 v41, v47, v47
	v_fma_mix_f32 v41, v46, v46, v41 op_sel_hi:[1,1,0]
	v_fma_mix_f32 v42, v96, v96, v42 op_sel_hi:[1,1,0]
	s_waitcnt vmcnt(16)
	v_cvt_f32_f16_sdwa v43, v112 dst_sel:DWORD dst_unused:UNUSED_PAD src0_sel:WORD_1
	v_add_f32_e32 v41, v41, v42
	v_add_f32_e32 v44, v40, v41
	v_cvt_f32_f16_e32 v42, v112
	v_cvt_f32_f16_sdwa v41, v113 dst_sel:DWORD dst_unused:UNUSED_PAD src0_sel:WORD_1
	v_cvt_f32_f16_e32 v40, v113
	v_cvt_f32_f16_sdwa v46, v114 dst_sel:DWORD dst_unused:UNUSED_PAD src0_sel:WORD_1
	v_cvt_f32_f16_e32 v47, v114
	v_cvt_f32_f16_sdwa v56, v115 dst_sel:DWORD dst_unused:UNUSED_PAD src0_sel:WORD_1
	v_cvt_f32_f16_e32 v57, v115
	v_sub_f32_e32 v40, v40, v210
	v_sub_f32_e32 v41, v41, v210
	v_sub_f32_e32 v42, v42, v210
	v_sub_f32_e32 v43, v43, v210
	v_pk_add_f32 v[38:39], v[38:39], v[198:199]
	v_pk_add_f32 v[36:37], v[36:37], v[200:201]
	v_pk_mul_f32 v[42:43], v[210:211], v[42:43] op_sel:[1,0]
	v_pk_mul_f32 v[40:41], v[210:211], v[40:41] op_sel:[1,0]
	v_pk_fma_f32 v[36:37], v[80:81], v[42:43], v[36:37]
	v_pk_fma_f32 v[38:39], v[82:83], v[40:41], v[38:39]
	v_sub_f32_e32 v40, v57, v210
	v_sub_f32_e32 v41, v56, v210
	v_sub_f32_e32 v42, v47, v210
	v_sub_f32_e32 v43, v46, v210
	v_pk_add_f32 v[34:35], v[34:35], v[192:193]
	v_pk_add_f32 v[32:33], v[32:33], v[194:195]
	v_pk_mul_f32 v[42:43], v[210:211], v[42:43] op_sel:[1,0]
	v_pk_mul_f32 v[40:41], v[210:211], v[40:41] op_sel:[1,0]
	ds_bpermute_b32 v62, v237, v60
	v_pk_fma_f32 v[40:41], v[74:75], v[40:41], v[34:35]
	v_pk_fma_f32 v[34:35], v[72:73], v[42:43], v[32:33]
	v_cvt_f16_f32_e32 v42, v36
	v_cvt_f16_f32_e32 v43, v37
	v_cvt_pk_f16_f32 v32, v36, v37
	v_cvt_f16_f32_e32 v36, v38
	v_cvt_f16_f32_e32 v37, v39
	v_cvt_pk_f16_f32 v33, v38, v39
	v_cvt_f16_f32_e32 v39, v35
	v_cvt_f16_f32_e32 v47, v41
	v_cvt_f16_f32_e32 v38, v34
	v_cvt_f16_f32_e32 v46, v40
	v_cvt_f32_f16_e32 v57, v36
	v_cvt_f32_f16_e32 v37, v37
	v_cvt_f32_f16_e32 v39, v39
	v_cvt_f32_f16_e32 v56, v42
	v_cvt_f32_f16_e32 v43, v43
	v_cvt_f32_f16_e32 v47, v47
	v_cvt_f32_f16_e32 v58, v38
	v_cvt_f32_f16_e32 v59, v46
	v_add_f32_e32 v57, v57, v37
	v_mul_f32_e32 v37, v37, v37
	v_fma_mix_f32 v36, v36, v36, v37 op_sel_hi:[1,1,0]
	v_mul_f32_e32 v37, v39, v39
	v_add_f32_e32 v56, v56, v43
	v_mul_f32_e32 v43, v43, v43
	v_fma_mix_f32 v37, v38, v38, v37 op_sel_hi:[1,1,0]
	v_mul_f32_e32 v38, v47, v47
	v_add_f32_e32 v56, v56, v57
	v_add_f32_e32 v57, v58, v39
	v_add_f32_e32 v58, v59, v47
	v_fma_mix_f32 v42, v42, v42, v43 op_sel_hi:[1,1,0]
	v_fma_mix_f32 v38, v46, v46, v38 op_sel_hi:[1,1,0]
	v_add_f32_e32 v57, v57, v58
	v_add_f32_e32 v36, v42, v36
	v_add_f32_e32 v37, v37, v38
	v_add_f32_e32 v56, v56, v57
	v_add_f32_e32 v36, v36, v37
	v_add_f32_e32 v45, v45, v56
	v_add_f32_e32 v36, v44, v36
	ds_bpermute_b32 v37, v221, v45
	ds_bpermute_b32 v38, v221, v36
	v_cvt_pk_f16_f32 v34, v34, v35
	v_cvt_pk_f16_f32 v35, v40, v41
	ds_write_b128 v235, v[32:35] offset:64
	s_waitcnt lgkmcnt(2)
	v_add_f32_e32 v32, v45, v37
	s_waitcnt lgkmcnt(1)
	v_add_f32_e32 v33, v36, v38
	ds_bpermute_b32 v63, v237, v61
	ds_bpermute_b32 v44, v237, v32
	ds_bpermute_b32 v45, v237, v33
	ds_read_b128 v[34:37], v236
	ds_read_b128 v[38:41], v236 offset:1152
	v_add_f32_e32 v42, v60, v62
	s_waitcnt lgkmcnt(4)
	v_add_f32_e32 v43, v61, v63
	s_waitcnt lgkmcnt(3)
	v_add_f32_e32 v44, v32, v44
	s_waitcnt lgkmcnt(2)
	v_add_f32_e32 v45, v33, v45
	v_add_u32_e32 v32, 0x30000, v144
	buffer_store_dwordx4 v[48:51], v32, s[24:27], 0 offen nt
	v_add_u32_e32 v32, 0x33000, v144
	buffer_store_dwordx4 v[52:55], v32, s[24:27], 0 offen nt
	v_add_co_u32_e32 v32, vcc, s76, v140
	s_nop 1
	v_addc_co_u32_e32 v33, vcc, 0, v141, vcc
	global_store_dwordx2 v[32:33], v[42:43], off
	v_add_u32_e32 v42, 0x36000, v144
	s_waitcnt lgkmcnt(1)
	buffer_store_dwordx4 v[34:37], v42, s[24:27], 0 offen nt
	s_nop 1
	v_add_u32_e32 v34, 0x39000, v144
	s_waitcnt lgkmcnt(0)
	buffer_store_dwordx4 v[38:41], v34, s[24:27], 0 offen nt
	global_store_dwordx2 v[32:33], v[44:45], off offset:1536
	s_waitcnt vmcnt(15)
	v_cvt_f32_f16_sdwa v37, v84 dst_sel:DWORD dst_unused:UNUSED_PAD src0_sel:WORD_1
	v_cvt_f32_f16_e32 v36, v84
	v_cvt_f32_f16_sdwa v35, v85 dst_sel:DWORD dst_unused:UNUSED_PAD src0_sel:WORD_1
	v_cvt_f32_f16_e32 v34, v85
	v_cvt_f32_f16_sdwa v38, v86 dst_sel:DWORD dst_unused:UNUSED_PAD src0_sel:WORD_1
	v_cvt_f32_f16_e32 v39, v86
	v_cvt_f32_f16_sdwa v40, v87 dst_sel:DWORD dst_unused:UNUSED_PAD src0_sel:WORD_1
	v_cvt_f32_f16_e32 v41, v87
	v_sub_f32_e32 v34, v34, v196
	v_sub_f32_e32 v35, v35, v196
	v_sub_f32_e32 v36, v36, v196
	v_sub_f32_e32 v37, v37, v196
	v_pk_add_f32 v[30:31], v[30:31], v[206:207]
	v_pk_add_f32 v[28:29], v[28:29], v[208:209]
	v_pk_mul_f32 v[36:37], v[196:197], v[36:37] op_sel:[1,0]
	v_pk_mul_f32 v[34:35], v[196:197], v[34:35] op_sel:[1,0]
	v_pk_fma_f32 v[28:29], v[92:93], v[36:37], v[28:29]
	v_pk_fma_f32 v[30:31], v[94:95], v[34:35], v[30:31]
	v_sub_f32_e32 v34, v41, v196
	v_sub_f32_e32 v35, v40, v196
	v_sub_f32_e32 v36, v39, v196
	v_sub_f32_e32 v37, v38, v196
	v_pk_add_f32 v[26:27], v[26:27], v[202:203]
	v_pk_add_f32 v[24:25], v[24:25], v[204:205]
	v_pk_mul_f32 v[36:37], v[196:197], v[36:37] op_sel:[1,0]
	v_pk_mul_f32 v[34:35], v[196:197], v[34:35] op_sel:[1,0]
	v_pk_add_f32 v[22:23], v[22:23], v[198:199]
	v_pk_fma_f32 v[34:35], v[90:91], v[34:35], v[26:27]
	v_pk_fma_f32 v[26:27], v[88:89], v[36:37], v[24:25]
	v_cvt_f16_f32_e32 v36, v28
	v_cvt_f16_f32_e32 v37, v29
	v_cvt_pk_f16_f32 v24, v28, v29
	v_cvt_f16_f32_e32 v28, v30
	v_cvt_f16_f32_e32 v29, v31
	v_cvt_pk_f16_f32 v25, v30, v31
	v_cvt_f16_f32_e32 v30, v26
	v_cvt_f16_f32_e32 v31, v27
	v_cvt_f16_f32_e32 v38, v34
	v_cvt_f16_f32_e32 v39, v35
	v_cvt_pk_f16_f32 v26, v26, v27
	v_cvt_pk_f16_f32 v27, v34, v35
	ds_write_b128 v235, v[24:27]
	v_cvt_f32_f16_e32 v24, v36
	v_cvt_f32_f16_e32 v25, v37
	v_cvt_f32_f16_e32 v26, v28
	v_cvt_f32_f16_e32 v27, v29
	v_cvt_f32_f16_e32 v29, v30
	v_cvt_f32_f16_e32 v31, v31
	v_cvt_f32_f16_e32 v34, v38
	v_cvt_f32_f16_e32 v35, v39
	v_add_f32_e32 v24, v24, v25
	v_add_f32_e32 v26, v26, v27
	v_add_f32_e32 v24, v24, v26
	v_add_f32_e32 v26, v29, v31
	v_add_f32_e32 v29, v34, v35
	v_add_f32_e32 v26, v26, v29
	v_add_f32_e32 v24, v24, v26
	v_add_f32_e32 v29, 0, v24
	v_mul_f32_e32 v24, v25, v25
	v_mul_f32_e32 v25, v27, v27
	v_fma_mix_f32 v24, v36, v36, v24 op_sel_hi:[1,1,0]
	v_fma_mix_f32 v25, v28, v28, v25 op_sel_hi:[1,1,0]
	v_mul_f32_e32 v26, v35, v35
	v_add_f32_e32 v24, v24, v25
	v_mul_f32_e32 v25, v31, v31
	v_fma_mix_f32 v25, v30, v30, v25 op_sel_hi:[1,1,0]
	v_fma_mix_f32 v26, v38, v38, v26 op_sel_hi:[1,1,0]
	s_waitcnt vmcnt(14)
	v_cvt_f32_f16_sdwa v27, v76 dst_sel:DWORD dst_unused:UNUSED_PAD src0_sel:WORD_1
	v_add_f32_e32 v25, v25, v26
	v_add_f32_e32 v28, v24, v25
	v_cvt_f32_f16_e32 v26, v76
	v_cvt_f32_f16_sdwa v25, v77 dst_sel:DWORD dst_unused:UNUSED_PAD src0_sel:WORD_1
	v_cvt_f32_f16_e32 v24, v77
	v_cvt_f32_f16_sdwa v30, v78 dst_sel:DWORD dst_unused:UNUSED_PAD src0_sel:WORD_1
	v_cvt_f32_f16_e32 v31, v78
	v_cvt_f32_f16_sdwa v34, v79 dst_sel:DWORD dst_unused:UNUSED_PAD src0_sel:WORD_1
	v_cvt_f32_f16_e32 v35, v79
	v_sub_f32_e32 v24, v24, v196
	v_sub_f32_e32 v25, v25, v196
	v_sub_f32_e32 v26, v26, v196
	v_sub_f32_e32 v27, v27, v196
	v_pk_add_f32 v[20:21], v[20:21], v[200:201]
	v_pk_mul_f32 v[26:27], v[196:197], v[26:27] op_sel:[1,0]
	v_pk_mul_f32 v[24:25], v[196:197], v[24:25] op_sel:[1,0]
	v_pk_fma_f32 v[20:21], v[80:81], v[26:27], v[20:21]
	v_pk_fma_f32 v[22:23], v[82:83], v[24:25], v[22:23]
	v_sub_f32_e32 v24, v35, v196
	v_sub_f32_e32 v25, v34, v196
	v_sub_f32_e32 v26, v31, v196
	v_sub_f32_e32 v27, v30, v196
	v_pk_add_f32 v[18:19], v[18:19], v[192:193]
	v_pk_add_f32 v[16:17], v[16:17], v[194:195]
	v_pk_mul_f32 v[26:27], v[196:197], v[26:27] op_sel:[1,0]
	v_pk_mul_f32 v[24:25], v[196:197], v[24:25] op_sel:[1,0]
	s_waitcnt vmcnt(13)
	v_cvt_f32_f16_sdwa v36, v71 dst_sel:DWORD dst_unused:UNUSED_PAD src0_sel:WORD_1
	v_pk_fma_f32 v[24:25], v[74:75], v[24:25], v[18:19]
	v_pk_fma_f32 v[18:19], v[72:73], v[26:27], v[16:17]
	v_cvt_f16_f32_e32 v26, v20
	v_cvt_f16_f32_e32 v27, v21
	v_cvt_pk_f16_f32 v16, v20, v21
	v_cvt_f16_f32_e32 v20, v22
	v_cvt_f16_f32_e32 v21, v23
	v_cvt_pk_f16_f32 v17, v22, v23
	v_cvt_f16_f32_e32 v23, v19
	v_cvt_f16_f32_e32 v31, v25
	v_cvt_f16_f32_e32 v22, v18
	v_cvt_f16_f32_e32 v30, v24
	v_cvt_pk_f16_f32 v18, v18, v19
	v_cvt_pk_f16_f32 v19, v24, v25
	v_cvt_f32_f16_e32 v25, v27
	v_cvt_f32_f16_e32 v27, v20
	v_cvt_f32_f16_e32 v21, v21
	v_cvt_f32_f16_e32 v23, v23
	v_cvt_f32_f16_e32 v24, v26
	v_cvt_f32_f16_e32 v31, v31
	v_cvt_f32_f16_e32 v34, v22
	v_cvt_f32_f16_e32 v35, v30
	v_add_f32_e32 v27, v27, v21
	v_mul_f32_e32 v21, v21, v21
	v_fma_mix_f32 v20, v20, v20, v21 op_sel_hi:[1,1,0]
	v_mul_f32_e32 v21, v23, v23
	v_add_f32_e32 v24, v24, v25
	v_mul_f32_e32 v25, v25, v25
	v_fma_mix_f32 v21, v22, v22, v21 op_sel_hi:[1,1,0]
	v_mul_f32_e32 v22, v31, v31
	v_add_f32_e32 v24, v24, v27
	v_add_f32_e32 v27, v34, v23
	v_add_f32_e32 v34, v35, v31
	v_fma_mix_f32 v25, v26, v26, v25 op_sel_hi:[1,1,0]
	v_fma_mix_f32 v22, v30, v30, v22 op_sel_hi:[1,1,0]
	v_add_f32_e32 v27, v27, v34
	v_add_f32_e32 v20, v25, v20
	v_add_f32_e32 v21, v21, v22
	v_add_f32_e32 v24, v24, v27
	v_add_f32_e32 v20, v20, v21
	v_add_f32_e32 v24, v29, v24
	v_add_f32_e32 v25, v28, v20
	ds_bpermute_b32 v26, v221, v24
	ds_bpermute_b32 v27, v221, v25
	v_cvt_f32_f16_sdwa v34, v70 dst_sel:DWORD dst_unused:UNUSED_PAD src0_sel:WORD_1
	v_cvt_f32_f16_e32 v35, v70
	v_cvt_f32_f16_e32 v37, v71
	s_waitcnt lgkmcnt(1)
	v_add_f32_e32 v28, v24, v26
	s_waitcnt lgkmcnt(0)
	v_add_f32_e32 v29, v25, v27
	v_cvt_f32_f16_sdwa v27, v68 dst_sel:DWORD dst_unused:UNUSED_PAD src0_sel:WORD_1
	v_cvt_f32_f16_e32 v26, v68
	v_cvt_f32_f16_sdwa v25, v69 dst_sel:DWORD dst_unused:UNUSED_PAD src0_sel:WORD_1
	v_cvt_f32_f16_e32 v24, v69
	v_sub_f32_e32 v27, v27, v190
	v_sub_f32_e32 v26, v26, v190
	v_sub_f32_e32 v25, v25, v190
	v_sub_f32_e32 v24, v24, v190
	v_pk_add_f32 v[14:15], v[14:15], v[206:207]
	v_pk_add_f32 v[12:13], v[12:13], v[208:209]
	v_pk_mul_f32 v[26:27], v[190:191], v[26:27] op_sel:[1,0]
	v_pk_mul_f32 v[24:25], v[190:191], v[24:25] op_sel:[1,0]
	v_pk_fma_f32 v[12:13], v[92:93], v[26:27], v[12:13]
	v_pk_fma_f32 v[14:15], v[94:95], v[24:25], v[14:15]
	v_sub_f32_e32 v24, v37, v190
	v_sub_f32_e32 v25, v36, v190
	v_sub_f32_e32 v26, v35, v190
	v_sub_f32_e32 v27, v34, v190
	v_pk_add_f32 v[10:11], v[10:11], v[202:203]
	v_pk_add_f32 v[8:9], v[8:9], v[204:205]
	v_pk_mul_f32 v[26:27], v[190:191], v[26:27] op_sel:[1,0]
	v_pk_mul_f32 v[24:25], v[190:191], v[24:25] op_sel:[1,0]
	ds_write_b128 v235, v[16:19] offset:64
	v_pk_fma_f32 v[24:25], v[90:91], v[24:25], v[10:11]
	v_pk_fma_f32 v[10:11], v[88:89], v[26:27], v[8:9]
	v_cvt_f16_f32_e32 v26, v12
	v_cvt_f16_f32_e32 v27, v13
	v_cvt_pk_f16_f32 v8, v12, v13
	v_cvt_f16_f32_e32 v12, v14
	v_cvt_f16_f32_e32 v13, v15
	v_cvt_pk_f16_f32 v9, v14, v15
	v_cvt_f16_f32_e32 v14, v10
	v_cvt_f16_f32_e32 v15, v11
	v_cvt_f16_f32_e32 v34, v24
	v_cvt_f16_f32_e32 v35, v25
	v_cvt_pk_f16_f32 v10, v10, v11
	v_cvt_pk_f16_f32 v11, v24, v25
	ds_read_b128 v[16:19], v236
	ds_read_b128 v[20:23], v236 offset:1152
	ds_write_b128 v235, v[8:11]
	v_cvt_f32_f16_e32 v8, v26
	v_cvt_f32_f16_e32 v9, v27
	v_cvt_f32_f16_e32 v10, v12
	v_cvt_f32_f16_e32 v11, v13
	v_cvt_f32_f16_e32 v13, v14
	v_cvt_f32_f16_e32 v15, v15
	v_cvt_f32_f16_e32 v24, v34
	v_cvt_f32_f16_e32 v25, v35
	v_add_f32_e32 v8, v8, v9
	v_add_f32_e32 v10, v10, v11
	v_add_f32_e32 v8, v8, v10
	v_add_f32_e32 v10, v13, v15
	v_add_f32_e32 v13, v24, v25
	v_add_f32_e32 v10, v10, v13
	v_add_f32_e32 v8, v8, v10
	v_add_f32_e32 v13, 0, v8
	v_mul_f32_e32 v8, v9, v9
	v_mul_f32_e32 v9, v11, v11
	v_fma_mix_f32 v8, v26, v26, v8 op_sel_hi:[1,1,0]
	v_fma_mix_f32 v9, v12, v12, v9 op_sel_hi:[1,1,0]
	v_mul_f32_e32 v10, v25, v25
	v_add_f32_e32 v8, v8, v9
	v_mul_f32_e32 v9, v15, v15
	v_fma_mix_f32 v9, v14, v14, v9 op_sel_hi:[1,1,0]
	v_fma_mix_f32 v10, v34, v34, v10 op_sel_hi:[1,1,0]
	s_waitcnt vmcnt(12)
	v_cvt_f32_f16_sdwa v11, v64 dst_sel:DWORD dst_unused:UNUSED_PAD src0_sel:WORD_1
	v_add_f32_e32 v9, v9, v10
	v_add_f32_e32 v12, v8, v9
	v_cvt_f32_f16_e32 v10, v64
	v_cvt_f32_f16_sdwa v9, v65 dst_sel:DWORD dst_unused:UNUSED_PAD src0_sel:WORD_1
	v_cvt_f32_f16_e32 v8, v65
	v_cvt_f32_f16_sdwa v14, v66 dst_sel:DWORD dst_unused:UNUSED_PAD src0_sel:WORD_1
	v_cvt_f32_f16_e32 v15, v66
	v_cvt_f32_f16_sdwa v24, v67 dst_sel:DWORD dst_unused:UNUSED_PAD src0_sel:WORD_1
	v_cvt_f32_f16_e32 v25, v67
	v_sub_f32_e32 v8, v8, v190
	v_sub_f32_e32 v9, v9, v190
	v_sub_f32_e32 v10, v10, v190
	v_sub_f32_e32 v11, v11, v190
	v_pk_add_f32 v[6:7], v[6:7], v[198:199]
	v_pk_add_f32 v[4:5], v[4:5], v[200:201]
	v_pk_mul_f32 v[10:11], v[190:191], v[10:11] op_sel:[1,0]
	v_pk_mul_f32 v[8:9], v[190:191], v[8:9] op_sel:[1,0]
	v_pk_fma_f32 v[4:5], v[80:81], v[10:11], v[4:5]
	v_pk_fma_f32 v[6:7], v[82:83], v[8:9], v[6:7]
	v_sub_f32_e32 v8, v25, v190
	v_sub_f32_e32 v9, v24, v190
	v_sub_f32_e32 v10, v15, v190
	v_sub_f32_e32 v11, v14, v190
	v_pk_add_f32 v[2:3], v[2:3], v[192:193]
	v_pk_add_f32 v[0:1], v[0:1], v[194:195]
	v_pk_mul_f32 v[10:11], v[190:191], v[10:11] op_sel:[1,0]
	v_pk_mul_f32 v[8:9], v[190:191], v[8:9] op_sel:[1,0]
	ds_bpermute_b32 v30, v237, v28
	v_pk_fma_f32 v[8:9], v[74:75], v[8:9], v[2:3]
	v_pk_fma_f32 v[2:3], v[72:73], v[10:11], v[0:1]
	v_cvt_f16_f32_e32 v10, v4
	v_cvt_f16_f32_e32 v11, v5
	v_cvt_pk_f16_f32 v0, v4, v5
	v_cvt_f16_f32_e32 v4, v6
	v_cvt_f16_f32_e32 v5, v7
	v_cvt_pk_f16_f32 v1, v6, v7
	v_cvt_f16_f32_e32 v7, v3
	v_cvt_f16_f32_e32 v15, v9
	v_cvt_f16_f32_e32 v6, v2
	v_cvt_f16_f32_e32 v14, v8
	v_cvt_f32_f16_e32 v25, v4
	v_cvt_f32_f16_e32 v5, v5
	v_cvt_f32_f16_e32 v7, v7
	v_cvt_f32_f16_e32 v24, v10
	v_cvt_f32_f16_e32 v11, v11
	v_cvt_f32_f16_e32 v15, v15
	v_cvt_f32_f16_e32 v26, v6
	v_cvt_f32_f16_e32 v27, v14
	v_add_f32_e32 v25, v25, v5
	v_mul_f32_e32 v5, v5, v5
	v_fma_mix_f32 v4, v4, v4, v5 op_sel_hi:[1,1,0]
	v_mul_f32_e32 v5, v7, v7
	v_add_f32_e32 v24, v24, v11
	v_mul_f32_e32 v11, v11, v11
	v_fma_mix_f32 v5, v6, v6, v5 op_sel_hi:[1,1,0]
	v_mul_f32_e32 v6, v15, v15
	v_add_f32_e32 v24, v24, v25
	v_add_f32_e32 v25, v26, v7
	v_add_f32_e32 v26, v27, v15
	v_fma_mix_f32 v10, v10, v10, v11 op_sel_hi:[1,1,0]
	v_fma_mix_f32 v6, v14, v14, v6 op_sel_hi:[1,1,0]
	v_add_f32_e32 v25, v25, v26
	v_add_f32_e32 v4, v10, v4
	v_add_f32_e32 v5, v5, v6
	v_add_f32_e32 v24, v24, v25
	v_add_f32_e32 v4, v4, v5
	v_add_f32_e32 v13, v13, v24
	v_add_f32_e32 v4, v12, v4
	ds_bpermute_b32 v5, v221, v13
	ds_bpermute_b32 v6, v221, v4
	v_cvt_pk_f16_f32 v2, v2, v3
	v_cvt_pk_f16_f32 v3, v8, v9
	ds_write_b128 v235, v[0:3] offset:64
	s_waitcnt lgkmcnt(2)
	v_add_f32_e32 v10, v13, v5
	s_waitcnt lgkmcnt(1)
	v_add_f32_e32 v11, v4, v6
	ds_bpermute_b32 v31, v237, v29
	ds_bpermute_b32 v12, v237, v10
	ds_bpermute_b32 v13, v237, v11
	ds_read_b128 v[0:3], v236
	ds_read_b128 v[4:7], v236 offset:1152
	v_add_f32_e32 v8, v28, v30
	s_waitcnt lgkmcnt(4)
	v_add_f32_e32 v9, v29, v31
	s_waitcnt lgkmcnt(3)
	v_add_f32_e32 v10, v10, v12
	s_waitcnt lgkmcnt(2)
	v_add_f32_e32 v11, v11, v13
	v_add_u32_e32 v12, 0x3c000, v144
	buffer_store_dwordx4 v[16:19], v12, s[24:27], 0 offen nt
	v_add_u32_e32 v12, 0x3f000, v144
	buffer_store_dwordx4 v[20:23], v12, s[24:27], 0 offen nt
	global_store_dwordx2 v[32:33], v[8:9], off offset:3072
	v_add_u32_e32 v8, 0x42000, v144
	s_waitcnt lgkmcnt(1)
	buffer_store_dwordx4 v[0:3], v8, s[24:27], 0 offen nt
	s_nop 1
	v_add_u32_e32 v0, 0x45000, v144
	s_waitcnt lgkmcnt(0)
	buffer_store_dwordx4 v[4:7], v0, s[24:27], 0 offen nt
	v_add_co_u32_e32 v0, vcc, 0x4000, v140
	s_nop 1
	v_addc_co_u32_e32 v1, vcc, 0, v141, vcc
	global_store_dwordx2 v[0:1], v[10:11], off offset:512
	s_mov_b32 s83, s81
	s_mov_b32 s84, s82
	s_mov_b64 s[40:41], s[0:1]
	s_mov_b64 s[38:39], s[8:9]
	s_mov_b64 vcc, s[6:7]
	s_cbranch_vccz .LBB10_12
	s_waitcnt vmcnt(0)
	s_cmpk_gt_u32 s44, 0xff
	s_cbranch_scc1 .LBB10_31
	s_barrier

.LBB10_32:
	s_endpgm
	s_endpgm
	s_endpgm
	s_endpgm
	s_endpgm
	s_endpgm
	s_endpgm
	s_endpgm
	s_endpgm
	s_endpgm
	s_endpgm
	s_endpgm
	s_endpgm
	s_endpgm
	s_endpgm
	s_endpgm
	s_endpgm
	s_endpgm
	s_endpgm
	s_endpgm
	s_endpgm
	s_endpgm
	s_endpgm
	s_endpgm
	s_endpgm
	s_endpgm
	s_endpgm
	s_endpgm
	s_endpgm
	s_endpgm
	s_endpgm
	s_endpgm
	s_endpgm
	s_endpgm
	s_endpgm
	s_endpgm
	s_endpgm
	s_endpgm
	s_endpgm
	s_endpgm
	s_endpgm
	s_endpgm
	s_endpgm
	s_endpgm
	s_endpgm
	s_endpgm
	s_endpgm
	s_endpgm
	s_endpgm
	s_endpgm
	s_endpgm
	s_endpgm
	s_endpgm
	s_endpgm
	.section	.rodata,"a",@progbits
	.p2align	6, 0x0
	.amdhsa_kernel _Z6k_gemmIN2pg6EpiResELi3072EEvNS0_4GemmET_
		.amdhsa_group_segment_fixed_size 0
		.amdhsa_private_segment_fixed_size 0
		.amdhsa_kernarg_size 344
		.amdhsa_user_sgpr_count 2
		.amdhsa_user_sgpr_dispatch_ptr 0
		.amdhsa_user_sgpr_queue_ptr 0
		.amdhsa_user_sgpr_kernarg_segment_ptr 1
		.amdhsa_user_sgpr_dispatch_id 0
		.amdhsa_user_sgpr_kernarg_preload_length 0
		.amdhsa_user_sgpr_kernarg_preload_offset 0
		.amdhsa_user_sgpr_private_segment_size 0
		.amdhsa_uses_dynamic_stack 0
		.amdhsa_enable_private_segment 0
		.amdhsa_system_sgpr_workgroup_id_x 1
		.amdhsa_system_sgpr_workgroup_id_y 0
		.amdhsa_system_sgpr_workgroup_id_z 0
		.amdhsa_system_sgpr_workgroup_info 0
		.amdhsa_system_vgpr_workitem_id 0
		.amdhsa_next_free_vgpr 254
		.amdhsa_next_free_sgpr 100
		.amdhsa_accum_offset 256
		.amdhsa_reserve_vcc 1
		.amdhsa_float_round_mode_32 0
		.amdhsa_float_round_mode_16_64 0
		.amdhsa_float_denorm_mode_32 3
		.amdhsa_float_denorm_mode_16_64 3
		.amdhsa_dx10_clamp 1
		.amdhsa_ieee_mode 1
		.amdhsa_fp16_overflow 0
		.amdhsa_tg_split 0
		.amdhsa_exception_fp_ieee_invalid_op 0
		.amdhsa_exception_fp_denorm_src 0
		.amdhsa_exception_fp_ieee_div_zero 0
		.amdhsa_exception_fp_ieee_overflow 0
		.amdhsa_exception_fp_ieee_underflow 0
		.amdhsa_exception_fp_ieee_inexact 0
		.amdhsa_exception_int_div_zero 0
	.end_amdhsa_kernel

amdhsa.kernels:
  - .agpr_count:     16
    .args:
      - .actual_access:  read_only
        .address_space:  global
        .offset:         0
        .size:           8
        .value_kind:     global_buffer
      - .actual_access:  read_only
        .address_space:  global
        .offset:         8
        .size:           8
        .value_kind:     global_buffer
      - .actual_access:  write_only
        .address_space:  global
        .offset:         16
        .size:           8
        .value_kind:     global_buffer
    .group_segment_fixed_size: 45056
    .kernarg_segment_align: 8
    .kernarg_segment_size: 24
    .language:       OpenCL C
    .language_version:
      - 2
      - 0
    .max_flat_workgroup_size: 256
    .name:           _Z6k_attnPKDF16_PKfPDF16_
    .private_segment_fixed_size: 0
    .sgpr_count:     16
    .sgpr_spill_count: 0
    .symbol:         _Z6k_attnPKDF16_PKfPDF16_.kd
    .uniform_work_group_size: 1
    .uses_dynamic_stack: false
    .vgpr_count:     84
    .vgpr_spill_count: 0
    .wavefront_size: 64
  - .agpr_count:     0
    .args:
      - .actual_access:  read_only
        .address_space:  global
        .offset:         0
        .size:           8
        .value_kind:     global_buffer
      - .actual_access:  read_only
        .address_space:  global
        .offset:         8
        .size:           8
        .value_kind:     global_buffer
      - .actual_access:  write_only
        .address_space:  global
        .offset:         16
        .size:           8
        .value_kind:     global_buffer
      - .actual_access:  write_only
        .address_space:  global
        .offset:         24
        .size:           8
        .value_kind:     global_buffer
      - .actual_access:  write_only
        .address_space:  global
        .offset:         32
        .size:           8
        .value_kind:     global_buffer
      - .actual_access:  write_only
        .address_space:  global
        .offset:         40
        .size:           8
        .value_kind:     global_buffer
    .group_segment_fixed_size: 0
    .kernarg_segment_align: 8
    .kernarg_segment_size: 48
    .language:       OpenCL C
    .language_version:
      - 2
      - 0
    .max_flat_workgroup_size: 256
    .name:           _Z11k_prep_miscPKiPKfPfPDv2_fS3_S3_
    .private_segment_fixed_size: 0
    .sgpr_count:     16
    .sgpr_spill_count: 0
    .symbol:         _Z11k_prep_miscPKiPKfPfPDv2_fS3_S3_.kd
    .uniform_work_group_size: 1
    .uses_dynamic_stack: false
    .vgpr_count:     6
    .vgpr_spill_count: 0
    .wavefront_size: 64
  - .agpr_count:     0
    .args:
      - .actual_access:  read_only
        .address_space:  global
        .offset:         0
        .size:           8
        .value_kind:     global_buffer
      - .actual_access:  write_only
        .address_space:  global
        .offset:         8
        .size:           8
        .value_kind:     global_buffer
    .group_segment_fixed_size: 0
    .kernarg_segment_align: 8
    .kernarg_segment_size: 16
    .language:       OpenCL C
    .language_version:
      - 2
      - 0
    .max_flat_workgroup_size: 256
    .name:           _Z7k_cvt_xPKfPDF16_
    .private_segment_fixed_size: 0
    .sgpr_count:     14
    .sgpr_spill_count: 0
    .symbol:         _Z7k_cvt_xPKfPDF16_.kd
    .uniform_work_group_size: 1
    .uses_dynamic_stack: false
    .vgpr_count:     12
    .vgpr_spill_count: 0
    .wavefront_size: 64
  - .agpr_count:     0
    .args:
      - .offset:         0
        .size:           176
        .value_kind:     by_value
    .group_segment_fixed_size: 9216
    .kernarg_segment_align: 8
    .kernarg_segment_size: 176
    .language:       OpenCL C
    .language_version:
      - 2
      - 0
    .max_flat_workgroup_size: 256
    .name:           _Z8k_wtrans8PrepArgs
    .private_segment_fixed_size: 0
    .sgpr_count:     44
    .sgpr_spill_count: 0
    .symbol:         _Z8k_wtrans8PrepArgs.kd
    .uniform_work_group_size: 1
    .uses_dynamic_stack: false
    .vgpr_count:     18
    .vgpr_spill_count: 0
    .wavefront_size: 64
  - .agpr_count:     0
    .args:
      - .offset:         0
        .size:           176
        .value_kind:     by_value
      - .actual_access:  read_only
        .address_space:  global
        .offset:         176
        .size:           8
        .value_kind:     global_buffer
      - .actual_access:  read_only
        .address_space:  global
        .offset:         184
        .size:           8
        .value_kind:     global_buffer
    .group_segment_fixed_size: 2048
    .kernarg_segment_align: 8
    .kernarg_segment_size: 192
    .language:       OpenCL C
    .language_version:
      - 2
      - 0
    .max_flat_workgroup_size: 256
    .name:           _Z8k_colvec8PrepArgsPKfS1_
    .private_segment_fixed_size: 0
    .sgpr_count:     38
    .sgpr_spill_count: 0
    .symbol:         _Z8k_colvec8PrepArgsPKfS1_.kd
    .uniform_work_group_size: 1
    .uses_dynamic_stack: false
    .vgpr_count:     114
    .vgpr_spill_count: 0
    .wavefront_size: 64
  - .agpr_count:     0
    .args:
      - .actual_access:  read_only
        .address_space:  global
        .offset:         0
        .size:           8
        .value_kind:     global_buffer
      - .actual_access:  write_only
        .address_space:  global
        .offset:         8
        .size:           8
        .value_kind:     global_buffer
    .group_segment_fixed_size: 0
    .kernarg_segment_align: 8
    .kernarg_segment_size: 16
    .language:       OpenCL C
    .language_version:
      - 2
      - 0
    .max_flat_workgroup_size: 256
    .name:           _Z9k_rowstatPKDv2_fPS_
    .private_segment_fixed_size: 0
    .sgpr_count:     14
    .sgpr_spill_count: 0
    .symbol:         _Z9k_rowstatPKDv2_fPS_.kd
    .uniform_work_group_size: 1
    .uses_dynamic_stack: false
    .vgpr_count:     28
    .vgpr_spill_count: 0
    .wavefront_size: 64
  - .agpr_count:     0
    .args:
      - .actual_access:  read_only
        .address_space:  global
        .offset:         0
        .size:           8
        .value_kind:     global_buffer
      - .actual_access:  read_only
        .address_space:  global
        .offset:         8
        .size:           8
        .value_kind:     global_buffer
      - .actual_access:  read_only
        .address_space:  global
        .offset:         16
        .size:           8
        .value_kind:     global_buffer
      - .actual_access:  read_only
        .address_space:  global
        .offset:         24
        .size:           8
        .value_kind:     global_buffer
      - .actual_access:  write_only
        .address_space:  global
        .offset:         32
        .size:           8
        .value_kind:     global_buffer
    .group_segment_fixed_size: 0
    .kernarg_segment_align: 8
    .kernarg_segment_size: 40
    .language:       OpenCL C
    .language_version:
      - 2
      - 0
    .max_flat_workgroup_size: 256
    .name:           _Z10k_final_lnPKDF16_PKDv2_fPKfS5_Pf
    .private_segment_fixed_size: 0
    .sgpr_count:     19
    .sgpr_spill_count: 0
    .symbol:         _Z10k_final_lnPKDF16_PKDv2_fPKfS5_Pf.kd
    .uniform_work_group_size: 1
    .uses_dynamic_stack: false
    .vgpr_count:     19
    .vgpr_spill_count: 0
    .wavefront_size: 64
  - .agpr_count:     0
    .args:
      - .offset:         0
        .size:           32
        .value_kind:     by_value
      - .offset:         32
        .size:           32
        .value_kind:     by_value
      - .offset:         64
        .size:           4
        .value_kind:     hidden_block_count_x
      - .offset:         68
        .size:           4
        .value_kind:     hidden_block_count_y
      - .offset:         72
        .size:           4
        .value_kind:     hidden_block_count_z
      - .offset:         76
        .size:           2
        .value_kind:     hidden_group_size_x
      - .offset:         78
        .size:           2
        .value_kind:     hidden_group_size_y
      - .offset:         80
        .size:           2
        .value_kind:     hidden_group_size_z
      - .offset:         82
        .size:           2
        .value_kind:     hidden_remainder_x
      - .offset:         84
        .size:           2
        .value_kind:     hidden_remainder_y
      - .offset:         86
        .size:           2
        .value_kind:     hidden_remainder_z
      - .offset:         104
        .size:           8
        .value_kind:     hidden_global_offset_x
      - .offset:         112
        .size:           8
        .value_kind:     hidden_global_offset_y
      - .offset:         120
        .size:           8
        .value_kind:     hidden_global_offset_z
      - .offset:         128
        .size:           2
        .value_kind:     hidden_grid_dims
      - .offset:         184
        .size:           4
        .value_kind:     hidden_dynamic_lds_size
    .group_segment_fixed_size: 0
    .kernarg_segment_align: 8
    .kernarg_segment_size: 320
    .language:       OpenCL C
    .language_version:
      - 2
      - 0
    .max_flat_workgroup_size: 512
    .name:           _Z6k_gemmIN2pg6EpiLinILi0EEELi768EEvNS0_4GemmET_
    .private_segment_fixed_size: 0
    .sgpr_count:     83
    .sgpr_spill_count: 0
    .symbol:         _Z6k_gemmIN2pg6EpiLinILi0EEELi768EEvNS0_4GemmET_.kd
    .uniform_work_group_size: 1
    .uses_dynamic_stack: false
    .vgpr_count:     254
    .vgpr_spill_count: 0
    .wavefront_size: 64
  - .agpr_count:     0
    .args:
      - .offset:         0
        .size:           32
        .value_kind:     by_value
      - .offset:         32
        .size:           56
        .value_kind:     by_value
      - .offset:         88
        .size:           4
        .value_kind:     hidden_block_count_x
      - .offset:         92
        .size:           4
        .value_kind:     hidden_block_count_y
      - .offset:         96
        .size:           4
        .value_kind:     hidden_block_count_z
      - .offset:         100
        .size:           2
        .value_kind:     hidden_group_size_x
      - .offset:         102
        .size:           2
        .value_kind:     hidden_group_size_y
      - .offset:         104
        .size:           2
        .value_kind:     hidden_group_size_z
      - .offset:         106
        .size:           2
        .value_kind:     hidden_remainder_x
      - .offset:         108
        .size:           2
        .value_kind:     hidden_remainder_y
      - .offset:         110
        .size:           2
        .value_kind:     hidden_remainder_z
      - .offset:         128
        .size:           8
        .value_kind:     hidden_global_offset_x
      - .offset:         136
        .size:           8
        .value_kind:     hidden_global_offset_y
      - .offset:         144
        .size:           8
        .value_kind:     hidden_global_offset_z
      - .offset:         152
        .size:           2
        .value_kind:     hidden_grid_dims
      - .offset:         208
        .size:           4
        .value_kind:     hidden_dynamic_lds_size
    .group_segment_fixed_size: 0
    .kernarg_segment_align: 8
    .kernarg_segment_size: 344
    .language:       OpenCL C
    .language_version:
      - 2
      - 0
    .max_flat_workgroup_size: 512
    .name:           _Z6k_gemmIN2pg6EpiResELi768EEvNS0_4GemmET_
    .private_segment_fixed_size: 0
    .sgpr_count:     106
    .sgpr_spill_count: 0
    .symbol:         _Z6k_gemmIN2pg6EpiResELi768EEvNS0_4GemmET_.kd
    .uniform_work_group_size: 1
    .uses_dynamic_stack: false
    .vgpr_count:     254
    .vgpr_spill_count: 0
    .wavefront_size: 64
  - .agpr_count:     0
    .args:
      - .offset:         0
        .size:           32
        .value_kind:     by_value
      - .offset:         32
        .size:           32
        .value_kind:     by_value
      - .offset:         64
        .size:           4
        .value_kind:     hidden_block_count_x
      - .offset:         68
        .size:           4
        .value_kind:     hidden_block_count_y
      - .offset:         72
        .size:           4
        .value_kind:     hidden_block_count_z
      - .offset:         76
        .size:           2
        .value_kind:     hidden_group_size_x
      - .offset:         78
        .size:           2
        .value_kind:     hidden_group_size_y
      - .offset:         80
        .size:           2
        .value_kind:     hidden_group_size_z
      - .offset:         82
        .size:           2
        .value_kind:     hidden_remainder_x
      - .offset:         84
        .size:           2
        .value_kind:     hidden_remainder_y
      - .offset:         86
        .size:           2
        .value_kind:     hidden_remainder_z
      - .offset:         104
        .size:           8
        .value_kind:     hidden_global_offset_x
      - .offset:         112
        .size:           8
        .value_kind:     hidden_global_offset_y
      - .offset:         120
        .size:           8
        .value_kind:     hidden_global_offset_z
      - .offset:         128
        .size:           2
        .value_kind:     hidden_grid_dims
      - .offset:         184
        .size:           4
        .value_kind:     hidden_dynamic_lds_size
    .group_segment_fixed_size: 0
    .kernarg_segment_align: 8
    .kernarg_segment_size: 320
    .language:       OpenCL C
    .language_version:
      - 2
      - 0
    .max_flat_workgroup_size: 512
    .name:           _Z6k_gemmIN2pg6EpiLinILi1EEELi768EEvNS0_4GemmET_
    .private_segment_fixed_size: 0
    .sgpr_count:     83
    .sgpr_spill_count: 0
    .symbol:         _Z6k_gemmIN2pg6EpiLinILi1EEELi768EEvNS0_4GemmET_.kd
    .uniform_work_group_size: 1
    .uses_dynamic_stack: false
    .vgpr_count:     254
    .vgpr_spill_count: 0
    .wavefront_size: 64
  - .agpr_count:     0
    .args:
      - .offset:         0
        .size:           32
        .value_kind:     by_value
      - .offset:         32
        .size:           56
        .value_kind:     by_value
      - .offset:         88
        .size:           4
        .value_kind:     hidden_block_count_x
      - .offset:         92
        .size:           4
        .value_kind:     hidden_block_count_y
      - .offset:         96
        .size:           4
        .value_kind:     hidden_block_count_z
      - .offset:         100
        .size:           2
        .value_kind:     hidden_group_size_x
      - .offset:         102
        .size:           2
        .value_kind:     hidden_group_size_y
      - .offset:         104
        .size:           2
        .value_kind:     hidden_group_size_z
      - .offset:         106
        .size:           2
        .value_kind:     hidden_remainder_x
      - .offset:         108
        .size:           2
        .value_kind:     hidden_remainder_y
      - .offset:         110
        .size:           2
        .value_kind:     hidden_remainder_z
      - .offset:         128
        .size:           8
        .value_kind:     hidden_global_offset_x
      - .offset:         136
        .size:           8
        .value_kind:     hidden_global_offset_y
      - .offset:         144
        .size:           8
        .value_kind:     hidden_global_offset_z
      - .offset:         152
        .size:           2
        .value_kind:     hidden_grid_dims
      - .offset:         208
        .size:           4
        .value_kind:     hidden_dynamic_lds_size
    .group_segment_fixed_size: 0
    .kernarg_segment_align: 8
    .kernarg_segment_size: 344
    .language:       OpenCL C
    .language_version:
      - 2
      - 0
    .max_flat_workgroup_size: 512
    .name:           _Z6k_gemmIN2pg6EpiResELi3072EEvNS0_4GemmET_
    .private_segment_fixed_size: 0
    .sgpr_count:     106
    .sgpr_spill_count: 0
    .symbol:         _Z6k_gemmIN2pg6EpiResELi3072EEvNS0_4GemmET_.kd
    .uniform_work_group_size: 1
    .uses_dynamic_stack: false
    .vgpr_count:     254
    .vgpr_spill_count: 0
    .wavefront_size: 64
